# v11: v9 + LDS-DMA groups reordered so the address VALU supplies the M0 wait state (89 s_nop removed from GEMM loops)
# baseline (speedup 1.0000x reference)
; #define PG8_STAGE(bufoff, gbase, voff) do { _Pragma("unroll") for (int _i = 0; _i < 2; ++_i) \
;         __builtin_amdgcn_global_load_lds((const unsigned*)((const char*)(gbase) + (voff)[_i]), (PG8_LAS unsigned*)(lds + (bufoff) + ldsw + _i * 8192), 16, 0, 0); } while (0)
; #define PG8_LDA(dst, b, h) do { _Pragma("unroll") for (int m = 0; m < 4; ++m) _Pragma("unroll") for (int k = 0; k < 2; ++k) dst[m][k] = *(const PG8_LAS bf16x8*)(lds + PG8_SA(b, h) + aoff + m * 2048 + k * 1024); } while (0)
; #define PG8_LDB(dst, b, h) do { _Pragma("unroll") for (int n = 0; n < 2; ++n) _Pragma("unroll") for (int k = 0; k < 2; ++k) dst[n][k] = *(const PG8_LAS bf16x8*)(lds + PG8_SB(b, h) + boff + n * 2048 + k * 1024); } while (0)
; #define PG8_MMA(ai, bj, At, Bt) do { __builtin_amdgcn_s_setprio(1); _Pragma("unroll") for (int m = 0; m < 4; ++m) _Pragma("unroll") for (int n = 0; n < 2; ++n) _Pragma("unroll") for (int k = 0; k < 2; ++k) \
;         acc[ai][bj][m][n] = __builtin_amdgcn_mfma_f32_16x16x32_bf16(Bt[n][k], At[m][k], acc[ai][bj][m][n], 0, 0, 0); __builtin_amdgcn_s_setprio(0); } while (0)
; #define PG8_WAIT_V(n) asm volatile("s_waitcnt vmcnt(" #n ")" ::: "memory")
; #define PG8_WAIT_L(n) asm volatile("s_waitcnt lgkmcnt(" #n ")" ::: "memory")
; #define PG8_BAR __builtin_amdgcn_s_barrier()
; #define PG8_SCHED __builtin_amdgcn_sched_barrier(0)
; template <class Epi, class Sched, bool ALIGN_EPI = false, bool SP2 = false>
; __device__ __forceinline__ void gemm_phase(PG8_LAS unsigned char* lds, const Gemm g, const Sched& S, const Epi& E) {
;     ...
;         for (int t = 0; t < nt; t += 2) {
;             const bool last = (t == nt - 2);
;             const char* a1 = cA + (size_t)(t + 1) * kstep;
;             const char* a2 = last ? nA : cA + (size_t)(t + 2) * kstep; const char* b2 = last ? nB : cB + (size_t)(t + 2) * kstep;
;             const char* a3 = a2 + kstep; const char* b3 = b2 + kstep;
;             if (last && has_next) S.a_ready(nxt);
;             if constexpr (SP2) {
;             PG8_LDB(B0, 0, 0); PG8_LDB(B1, 0, 1); PG8_SCHED; PG8_LDA(At, 0, 0); PG8_STAGE(PG8_SA(1, 1), a1 + hstep, voffA);
;             PG8_WAIT_V(8); PG8_WAIT_L(0); PG8_BAR; PG8_MMA(0, 0, At, B0); PG8_MMA(0, 1, At, B1); PG8_BAR; PG8_SCHED;
;             PG8_LDA(At, 0, 1); PG8_STAGE(PG8_SB(0, 0), b2, voffB); PG8_STAGE(PG8_SB(0, 1), b2 + hstep, voffB); PG8_STAGE(PG8_SA(0, 0), a2, voffA);
.LBB0_230:
	ds_read_b128 v[152:155], v149
	ds_read_b128 v[156:159], v149 offset:1024
	ds_read_b128 v[160:163], v149 offset:2048
	ds_read_b128 v[164:167], v149 offset:3072
	ds_read_b128 v[168:171], v150
	ds_read_b128 v[172:175], v150 offset:1024
	ds_read_b128 v[176:179], v150 offset:2048
	ds_read_b128 v[180:183], v150 offset:3072
	s_add_u32 s28, s26, 0xfff80080
	s_addc_u32 s29, s27, -1
	s_cmp_eq_u32 s78, 28
	s_cselect_b32 s35, s15, s29
	s_cselect_b32 s34, s60, s28
	s_cselect_b32 s29, s13, s63
	s_cselect_b32 s28, s61, s62
	v_lshl_add_u64 v[216:217], s[26:27], 0, v[138:139]
	s_add_i32 m0, s3, 0xc000
	ds_read_b128 v[184:187], v151
	ds_read_b128 v[188:191], v151 offset:1024
	ds_read_b128 v[192:195], v151 offset:2048
	ds_read_b128 v[196:199], v151 offset:3072
	ds_read_b128 v[200:203], v151 offset:4096
	ds_read_b128 v[204:207], v151 offset:5120
	ds_read_b128 v[208:211], v151 offset:6144
	ds_read_b128 v[212:215], v151 offset:7168
	global_load_lds_dwordx4 v[216:217], off
	s_add_i32 m0, s3, 0xe000
	v_lshl_add_u64 v[216:217], s[26:27], 0, v[140:141]
	global_load_lds_dwordx4 v[216:217], off
	s_waitcnt vmcnt(8)
	s_waitcnt lgkmcnt(0)
	s_barrier
	s_setprio 1
	s_waitcnt lgkmcnt(0)
	v_mfma_f32_16x16x32_bf16 v[126:129], v[152:155], v[184:187], v[126:129]
	v_mfma_f32_16x16x32_bf16 v[122:125], v[160:163], v[184:187], v[122:125]
	v_mfma_f32_16x16x32_bf16 v[118:121], v[152:155], v[192:195], v[118:121]
	v_mfma_f32_16x16x32_bf16 v[114:117], v[160:163], v[192:195], v[114:117]
	v_mfma_f32_16x16x32_bf16 v[102:105], v[152:155], v[200:203], v[102:105]
	v_mfma_f32_16x16x32_bf16 v[98:101], v[160:163], v[200:203], v[98:101]
	v_mfma_f32_16x16x32_bf16 v[86:89], v[152:155], v[208:211], v[86:89]
	v_mfma_f32_16x16x32_bf16 v[82:85], v[160:163], v[208:211], v[82:85]
	v_mfma_f32_16x16x32_bf16 v[126:129], v[156:159], v[188:191], v[126:129]
	v_mfma_f32_16x16x32_bf16 v[122:125], v[164:167], v[188:191], v[122:125]
	v_mfma_f32_16x16x32_bf16 v[118:121], v[156:159], v[196:199], v[118:121]
	v_mfma_f32_16x16x32_bf16 v[114:117], v[164:167], v[196:199], v[114:117]
	v_mfma_f32_16x16x32_bf16 v[102:105], v[156:159], v[204:207], v[102:105]
	v_mfma_f32_16x16x32_bf16 v[98:101], v[164:167], v[204:207], v[98:101]
	v_mfma_f32_16x16x32_bf16 v[86:89], v[156:159], v[212:215], v[86:89]
	v_mfma_f32_16x16x32_bf16 v[82:85], v[164:167], v[212:215], v[82:85]
	v_mfma_f32_16x16x32_bf16 v[110:113], v[168:171], v[184:187], v[110:113]
	v_mfma_f32_16x16x32_bf16 v[106:109], v[176:179], v[184:187], v[106:109]
	v_mfma_f32_16x16x32_bf16 v[94:97], v[168:171], v[192:195], v[94:97]
	v_mfma_f32_16x16x32_bf16 v[90:93], v[176:179], v[192:195], v[90:93]
	v_mfma_f32_16x16x32_bf16 v[78:81], v[168:171], v[200:203], v[78:81]
	v_mfma_f32_16x16x32_bf16 v[74:77], v[176:179], v[200:203], v[74:77]
	v_mfma_f32_16x16x32_bf16 v[70:73], v[168:171], v[208:211], v[70:73]
	v_mfma_f32_16x16x32_bf16 v[66:69], v[176:179], v[208:211], v[66:69]
	v_mfma_f32_16x16x32_bf16 v[110:113], v[172:175], v[188:191], v[110:113]
	v_mfma_f32_16x16x32_bf16 v[106:109], v[180:183], v[188:191], v[106:109]
	v_mfma_f32_16x16x32_bf16 v[94:97], v[172:175], v[196:199], v[94:97]
	v_mfma_f32_16x16x32_bf16 v[90:93], v[180:183], v[196:199], v[90:93]
	v_mfma_f32_16x16x32_bf16 v[78:81], v[172:175], v[204:207], v[78:81]
	v_mfma_f32_16x16x32_bf16 v[74:77], v[180:183], v[204:207], v[74:77]
	v_mfma_f32_16x16x32_bf16 v[70:73], v[172:175], v[212:215], v[70:73]
	v_mfma_f32_16x16x32_bf16 v[66:69], v[180:183], v[212:215], v[66:69]
	s_setprio 0
	s_barrier
	s_add_i32 s79, s56, s2
	v_lshl_add_u64 v[216:217], s[28:29], 0, v[134:135]
	s_mov_b32 m0, s79
	ds_read_b128 v[184:187], v151 offset:16384
	ds_read_b128 v[188:191], v151 offset:17408
	ds_read_b128 v[192:195], v151 offset:18432
	ds_read_b128 v[196:199], v151 offset:19456
	ds_read_b128 v[200:203], v151 offset:20480
	ds_read_b128 v[204:207], v151 offset:21504
	ds_read_b128 v[208:211], v151 offset:22528
	ds_read_b128 v[212:215], v151 offset:23552
	global_load_lds_dwordx4 v[216:217], off
	s_add_i32 m0, s79, 0x2000
	s_add_u32 s96, s28, 0x80000
	v_lshl_add_u64 v[218:219], s[28:29], 0, v[130:131]
	s_addc_u32 s97, s29, 0
	s_add_i32 s79, s57, s2
	global_load_lds_dwordx4 v[218:219], off
	v_lshl_add_u64 v[220:221], s[96:97], 0, v[134:135]
	s_mov_b32 m0, s79
	v_lshl_add_u64 v[222:223], s[34:35], 0, v[132:133]
	global_load_lds_dwordx4 v[220:221], off
	s_add_i32 m0, s79, 0x2000
	v_lshl_add_u64 v[220:221], s[96:97], 0, v[130:131]
	global_load_lds_dwordx4 v[220:221], off
	s_mov_b32 m0, s3
	v_lshl_add_u64 v[220:221], s[34:35], 0, v[136:137]
	global_load_lds_dwordx4 v[220:221], off
	s_mov_b32 m0, s11
	s_nop 0
	global_load_lds_dwordx4 v[222:223], off
	s_waitcnt vmcnt(8)
	s_waitcnt lgkmcnt(0)
	s_barrier
; #define PG8_STAGE(bufoff, gbase, voff) do { _Pragma("unroll") for (int _i = 0; _i < 2; ++_i) \
;         __builtin_amdgcn_global_load_lds((const unsigned*)((const char*)(gbase) + (voff)[_i]), (PG8_LAS unsigned*)(lds + (bufoff) + ldsw + _i * 8192), 16, 0, 0); } while (0)
; #define PG8_LDA(dst, b, h) do { _Pragma("unroll") for (int m = 0; m < 4; ++m) _Pragma("unroll") for (int k = 0; k < 2; ++k) dst[m][k] = *(const PG8_LAS bf16x8*)(lds + PG8_SA(b, h) + aoff + m * 2048 + k * 1024); } while (0)
; #define PG8_LDB(dst, b, h) do { _Pragma("unroll") for (int n = 0; n < 2; ++n) _Pragma("unroll") for (int k = 0; k < 2; ++k) dst[n][k] = *(const PG8_LAS bf16x8*)(lds + PG8_SB(b, h) + boff + n * 2048 + k * 1024); } while (0)
; #define PG8_MMA(ai, bj, At, Bt) do { __builtin_amdgcn_s_setprio(1); _Pragma("unroll") for (int m = 0; m < 4; ++m) _Pragma("unroll") for (int n = 0; n < 2; ++n) _Pragma("unroll") for (int k = 0; k < 2; ++k) \
;         acc[ai][bj][m][n] = __builtin_amdgcn_mfma_f32_16x16x32_bf16(Bt[n][k], At[m][k], acc[ai][bj][m][n], 0, 0, 0); __builtin_amdgcn_s_setprio(0); } while (0)
; #define PG8_WAIT_V(n) asm volatile("s_waitcnt vmcnt(" #n ")" ::: "memory")
; #define PG8_WAIT_L(n) asm volatile("s_waitcnt lgkmcnt(" #n ")" ::: "memory")
; #define PG8_BAR __builtin_amdgcn_s_barrier()
; #define PG8_SCHED __builtin_amdgcn_sched_barrier(0)
; template <class Epi, class Sched, bool ALIGN_EPI = false, bool SP2 = false>
; __device__ __forceinline__ void gemm_phase(PG8_LAS unsigned char* lds, const Gemm g, const Sched& S, const Epi& E) {
;     ...
;             PG8_WAIT_V(8); PG8_WAIT_L(0); PG8_BAR; PG8_MMA(1, 0, At, B0); PG8_MMA(1, 1, At, B1); PG8_BAR; PG8_SCHED;
;             PG8_LDB(B0, 1, 0); PG8_LDB(B1, 1, 1); PG8_SCHED; PG8_LDA(At, 1, 0); PG8_STAGE(PG8_SA(0, 1), a2 + hstep, voffA);
;             PG8_WAIT_V(8); PG8_WAIT_L(0); PG8_BAR; PG8_MMA(0, 0, At, B0); PG8_MMA(0, 1, At, B1); PG8_BAR; PG8_SCHED;
	s_setprio 1
	s_waitcnt lgkmcnt(0)
	v_mfma_f32_16x16x32_bf16 v[62:65], v[152:155], v[184:187], v[62:65]
	v_mfma_f32_16x16x32_bf16 v[58:61], v[160:163], v[184:187], v[58:61]
	v_mfma_f32_16x16x32_bf16 v[54:57], v[152:155], v[192:195], v[54:57]
	v_mfma_f32_16x16x32_bf16 v[50:53], v[160:163], v[192:195], v[50:53]
	v_mfma_f32_16x16x32_bf16 v[38:41], v[152:155], v[200:203], v[38:41]
	v_mfma_f32_16x16x32_bf16 v[34:37], v[160:163], v[200:203], v[34:37]
	v_mfma_f32_16x16x32_bf16 v[22:25], v[152:155], v[208:211], v[22:25]
	v_mfma_f32_16x16x32_bf16 v[18:21], v[160:163], v[208:211], v[18:21]
	v_mfma_f32_16x16x32_bf16 v[62:65], v[156:159], v[188:191], v[62:65]
	v_mfma_f32_16x16x32_bf16 v[58:61], v[164:167], v[188:191], v[58:61]
	v_mfma_f32_16x16x32_bf16 v[54:57], v[156:159], v[196:199], v[54:57]
	v_mfma_f32_16x16x32_bf16 v[50:53], v[164:167], v[196:199], v[50:53]
	v_mfma_f32_16x16x32_bf16 v[38:41], v[156:159], v[204:207], v[38:41]
	v_mfma_f32_16x16x32_bf16 v[34:37], v[164:167], v[204:207], v[34:37]
	v_mfma_f32_16x16x32_bf16 v[22:25], v[156:159], v[212:215], v[22:25]
	v_mfma_f32_16x16x32_bf16 v[18:21], v[164:167], v[212:215], v[18:21]
	v_mfma_f32_16x16x32_bf16 v[46:49], v[168:171], v[184:187], v[46:49]
	v_mfma_f32_16x16x32_bf16 v[42:45], v[176:179], v[184:187], v[42:45]
	v_mfma_f32_16x16x32_bf16 v[30:33], v[168:171], v[192:195], v[30:33]
	v_mfma_f32_16x16x32_bf16 v[26:29], v[176:179], v[192:195], v[26:29]
	v_mfma_f32_16x16x32_bf16 v[14:17], v[168:171], v[200:203], v[14:17]
	v_mfma_f32_16x16x32_bf16 v[10:13], v[176:179], v[200:203], v[10:13]
	v_mfma_f32_16x16x32_bf16 v[6:9], v[168:171], v[208:211], v[6:9]
	v_mfma_f32_16x16x32_bf16 v[2:5], v[176:179], v[208:211], v[2:5]
	v_mfma_f32_16x16x32_bf16 v[46:49], v[172:175], v[188:191], v[46:49]
	v_mfma_f32_16x16x32_bf16 v[42:45], v[180:183], v[188:191], v[42:45]
	v_mfma_f32_16x16x32_bf16 v[30:33], v[172:175], v[196:199], v[30:33]
	v_mfma_f32_16x16x32_bf16 v[26:29], v[180:183], v[196:199], v[26:29]
	v_mfma_f32_16x16x32_bf16 v[14:17], v[172:175], v[204:207], v[14:17]
	v_mfma_f32_16x16x32_bf16 v[10:13], v[180:183], v[204:207], v[10:13]
	v_mfma_f32_16x16x32_bf16 v[6:9], v[172:175], v[212:215], v[6:9]
	v_mfma_f32_16x16x32_bf16 v[2:5], v[180:183], v[212:215], v[2:5]
	s_setprio 0
	s_barrier
	s_add_i32 s79, 0, 0x18000
	s_add_i32 s96, 0, 0x1c000
	v_add_u32_e32 v164, s79, v147
	v_add_u32_e32 v180, s96, v147
	ds_read_b128 v[152:155], v164
	ds_read_b128 v[156:159], v164 offset:1024
	ds_read_b128 v[160:163], v164 offset:2048
	ds_read_b128 v[164:167], v164 offset:3072
	ds_read_b128 v[168:171], v180
	ds_read_b128 v[172:175], v180 offset:1024
	ds_read_b128 v[176:179], v180 offset:2048
	ds_read_b128 v[180:183], v180 offset:3072
	s_add_u32 s34, s34, 0x80000
	s_addc_u32 s35, s35, 0
	s_mov_b32 m0, s33
	v_lshl_add_u64 v[224:225], s[34:35], 0, v[136:137]
	ds_read_b128 v[184:187], v151 offset:32768
	ds_read_b128 v[188:191], v151 offset:33792
	ds_read_b128 v[192:195], v151 offset:34816
	ds_read_b128 v[196:199], v151 offset:35840
	ds_read_b128 v[200:203], v151 offset:36864
	ds_read_b128 v[204:207], v151 offset:37888
	ds_read_b128 v[208:211], v151 offset:38912
	ds_read_b128 v[212:215], v151 offset:39936
	global_load_lds_dwordx4 v[224:225], off
	s_mov_b32 m0, s36
	v_lshl_add_u64 v[224:225], s[34:35], 0, v[132:133]
	global_load_lds_dwordx4 v[224:225], off
	s_waitcnt vmcnt(8)
	s_waitcnt lgkmcnt(0)
	s_barrier
	s_setprio 1
	s_waitcnt lgkmcnt(0)
	v_mfma_f32_16x16x32_bf16 v[126:129], v[152:155], v[184:187], v[126:129]
	v_mfma_f32_16x16x32_bf16 v[122:125], v[160:163], v[184:187], v[122:125]
	v_mfma_f32_16x16x32_bf16 v[118:121], v[152:155], v[192:195], v[118:121]
	v_mfma_f32_16x16x32_bf16 v[114:117], v[160:163], v[192:195], v[114:117]
	v_mfma_f32_16x16x32_bf16 v[102:105], v[152:155], v[200:203], v[102:105]
	v_mfma_f32_16x16x32_bf16 v[98:101], v[160:163], v[200:203], v[98:101]
	v_mfma_f32_16x16x32_bf16 v[86:89], v[152:155], v[208:211], v[86:89]
	v_mfma_f32_16x16x32_bf16 v[82:85], v[160:163], v[208:211], v[82:85]
	v_mfma_f32_16x16x32_bf16 v[126:129], v[156:159], v[188:191], v[126:129]
	v_mfma_f32_16x16x32_bf16 v[122:125], v[164:167], v[188:191], v[122:125]
	v_mfma_f32_16x16x32_bf16 v[118:121], v[156:159], v[196:199], v[118:121]
	v_mfma_f32_16x16x32_bf16 v[114:117], v[164:167], v[196:199], v[114:117]
	v_mfma_f32_16x16x32_bf16 v[102:105], v[156:159], v[204:207], v[102:105]
	v_mfma_f32_16x16x32_bf16 v[98:101], v[164:167], v[204:207], v[98:101]
	v_mfma_f32_16x16x32_bf16 v[86:89], v[156:159], v[212:215], v[86:89]
	v_mfma_f32_16x16x32_bf16 v[82:85], v[164:167], v[212:215], v[82:85]
	v_mfma_f32_16x16x32_bf16 v[110:113], v[168:171], v[184:187], v[110:113]
	v_mfma_f32_16x16x32_bf16 v[106:109], v[176:179], v[184:187], v[106:109]
	v_mfma_f32_16x16x32_bf16 v[94:97], v[168:171], v[192:195], v[94:97]
	v_mfma_f32_16x16x32_bf16 v[90:93], v[176:179], v[192:195], v[90:93]
	v_mfma_f32_16x16x32_bf16 v[78:81], v[168:171], v[200:203], v[78:81]
	v_mfma_f32_16x16x32_bf16 v[74:77], v[176:179], v[200:203], v[74:77]
	v_mfma_f32_16x16x32_bf16 v[70:73], v[168:171], v[208:211], v[70:73]
	v_mfma_f32_16x16x32_bf16 v[66:69], v[176:179], v[208:211], v[66:69]
	v_mfma_f32_16x16x32_bf16 v[110:113], v[172:175], v[188:191], v[110:113]
	v_mfma_f32_16x16x32_bf16 v[106:109], v[180:183], v[188:191], v[106:109]
	v_mfma_f32_16x16x32_bf16 v[94:97], v[172:175], v[196:199], v[94:97]
	v_mfma_f32_16x16x32_bf16 v[90:93], v[180:183], v[196:199], v[90:93]
	v_mfma_f32_16x16x32_bf16 v[78:81], v[172:175], v[204:207], v[78:81]
	v_mfma_f32_16x16x32_bf16 v[74:77], v[180:183], v[204:207], v[74:77]
	v_mfma_f32_16x16x32_bf16 v[70:73], v[172:175], v[212:215], v[70:73]
	v_mfma_f32_16x16x32_bf16 v[66:69], v[180:183], v[212:215], v[66:69]
	s_setprio 0
	s_barrier
; #define PG8_STAGE(bufoff, gbase, voff) do { _Pragma("unroll") for (int _i = 0; _i < 2; ++_i) \
;         __builtin_amdgcn_global_load_lds((const unsigned*)((const char*)(gbase) + (voff)[_i]), (PG8_LAS unsigned*)(lds + (bufoff) + ldsw + _i * 8192), 16, 0, 0); } while (0)
; #define PG8_LDA(dst, b, h) do { _Pragma("unroll") for (int m = 0; m < 4; ++m) _Pragma("unroll") for (int k = 0; k < 2; ++k) dst[m][k] = *(const PG8_LAS bf16x8*)(lds + PG8_SA(b, h) + aoff + m * 2048 + k * 1024); } while (0)
; #define PG8_MMA(ai, bj, At, Bt) do { __builtin_amdgcn_s_setprio(1); _Pragma("unroll") for (int m = 0; m < 4; ++m) _Pragma("unroll") for (int n = 0; n < 2; ++n) _Pragma("unroll") for (int k = 0; k < 2; ++k) \
;         acc[ai][bj][m][n] = __builtin_amdgcn_mfma_f32_16x16x32_bf16(Bt[n][k], At[m][k], acc[ai][bj][m][n], 0, 0, 0); __builtin_amdgcn_s_setprio(0); } while (0)
; #define PG8_WAIT_V(n) asm volatile("s_waitcnt vmcnt(" #n ")" ::: "memory")
; #define PG8_WAIT_L(n) asm volatile("s_waitcnt lgkmcnt(" #n ")" ::: "memory")
; #define PG8_BAR __builtin_amdgcn_s_barrier()
; #define PG8_SCHED __builtin_amdgcn_sched_barrier(0)
; template <class Epi, class Sched, bool ALIGN_EPI = false, bool SP2 = false>
; __device__ __forceinline__ void gemm_phase(PG8_LAS unsigned char* lds, const Gemm g, const Sched& S, const Epi& E) {
;     ...
;             PG8_LDA(At, 1, 1); PG8_STAGE(PG8_SB(1, 0), b3, voffB); PG8_STAGE(PG8_SB(1, 1), b3 + hstep, voffB); PG8_STAGE(PG8_SA(1, 0), a3, voffA);
;             PG8_WAIT_V(8); PG8_WAIT_L(0); PG8_BAR; PG8_MMA(1, 0, At, B0); PG8_MMA(1, 1, At, B1); PG8_BAR; PG8_SCHED;
;     ...
;         if constexpr (ALIGN_EPI) { if (wr == 0) PG8_BAR; }
	s_add_i32 s34, s79, s2
	v_lshl_add_u64 v[216:217], v[216:217], 0, s[6:7]
	s_mov_b32 m0, s34
	ds_read_b128 v[184:187], v151 offset:49152
	ds_read_b128 v[188:191], v151 offset:50176
	ds_read_b128 v[192:195], v151 offset:51200
	ds_read_b128 v[196:199], v151 offset:52224
	ds_read_b128 v[200:203], v151 offset:53248
	ds_read_b128 v[204:207], v151 offset:54272
	ds_read_b128 v[208:211], v151 offset:55296
	ds_read_b128 v[212:215], v151 offset:56320
	global_load_lds_dwordx4 v[216:217], off
	s_add_i32 m0, s34, 0x2000
	s_add_u32 s28, s28, 0x80080
	v_lshl_add_u64 v[216:217], v[218:219], 0, s[6:7]
	s_addc_u32 s29, s29, 0
	s_add_i32 s34, s96, s2
	global_load_lds_dwordx4 v[216:217], off
	s_mov_b32 m0, s34
	v_lshl_add_u64 v[216:217], s[28:29], 0, v[134:135]
	global_load_lds_dwordx4 v[216:217], off
	s_add_i32 m0, s34, 0x2000
	v_lshl_add_u64 v[216:217], s[28:29], 0, v[130:131]
	global_load_lds_dwordx4 v[216:217], off
	s_mov_b32 m0, s38
	v_lshl_add_u64 v[216:217], v[220:221], 0, s[6:7]
	global_load_lds_dwordx4 v[216:217], off
	s_mov_b32 m0, s39
	v_lshl_add_u64 v[216:217], v[222:223], 0, s[6:7]
	global_load_lds_dwordx4 v[216:217], off
	s_waitcnt vmcnt(8)
	s_waitcnt lgkmcnt(0)
	s_barrier
	s_setprio 1
	s_waitcnt lgkmcnt(0)
	v_mfma_f32_16x16x32_bf16 v[62:65], v[152:155], v[184:187], v[62:65]
	v_mfma_f32_16x16x32_bf16 v[58:61], v[160:163], v[184:187], v[58:61]
	v_mfma_f32_16x16x32_bf16 v[54:57], v[152:155], v[192:195], v[54:57]
	v_mfma_f32_16x16x32_bf16 v[50:53], v[160:163], v[192:195], v[50:53]
	v_mfma_f32_16x16x32_bf16 v[38:41], v[152:155], v[200:203], v[38:41]
	v_mfma_f32_16x16x32_bf16 v[34:37], v[160:163], v[200:203], v[34:37]
	v_mfma_f32_16x16x32_bf16 v[22:25], v[152:155], v[208:211], v[22:25]
	v_mfma_f32_16x16x32_bf16 v[18:21], v[160:163], v[208:211], v[18:21]
	v_mfma_f32_16x16x32_bf16 v[62:65], v[156:159], v[188:191], v[62:65]
	v_mfma_f32_16x16x32_bf16 v[58:61], v[164:167], v[188:191], v[58:61]
	v_mfma_f32_16x16x32_bf16 v[54:57], v[156:159], v[196:199], v[54:57]
	v_mfma_f32_16x16x32_bf16 v[50:53], v[164:167], v[196:199], v[50:53]
	v_mfma_f32_16x16x32_bf16 v[38:41], v[156:159], v[204:207], v[38:41]
	v_mfma_f32_16x16x32_bf16 v[34:37], v[164:167], v[204:207], v[34:37]
	v_mfma_f32_16x16x32_bf16 v[22:25], v[156:159], v[212:215], v[22:25]
	v_mfma_f32_16x16x32_bf16 v[18:21], v[164:167], v[212:215], v[18:21]
	v_mfma_f32_16x16x32_bf16 v[46:49], v[168:171], v[184:187], v[46:49]
	v_mfma_f32_16x16x32_bf16 v[42:45], v[176:179], v[184:187], v[42:45]
	v_mfma_f32_16x16x32_bf16 v[30:33], v[168:171], v[192:195], v[30:33]
	v_mfma_f32_16x16x32_bf16 v[26:29], v[176:179], v[192:195], v[26:29]
	v_mfma_f32_16x16x32_bf16 v[14:17], v[168:171], v[200:203], v[14:17]
	v_mfma_f32_16x16x32_bf16 v[10:13], v[176:179], v[200:203], v[10:13]
	v_mfma_f32_16x16x32_bf16 v[6:9], v[168:171], v[208:211], v[6:9]
	v_mfma_f32_16x16x32_bf16 v[2:5], v[176:179], v[208:211], v[2:5]
	v_mfma_f32_16x16x32_bf16 v[46:49], v[172:175], v[188:191], v[46:49]
	v_mfma_f32_16x16x32_bf16 v[42:45], v[180:183], v[188:191], v[42:45]
	v_mfma_f32_16x16x32_bf16 v[30:33], v[172:175], v[196:199], v[30:33]
	v_mfma_f32_16x16x32_bf16 v[26:29], v[180:183], v[196:199], v[26:29]
	v_mfma_f32_16x16x32_bf16 v[14:17], v[172:175], v[204:207], v[14:17]
	v_mfma_f32_16x16x32_bf16 v[10:13], v[180:183], v[204:207], v[10:13]
	v_mfma_f32_16x16x32_bf16 v[6:9], v[172:175], v[212:215], v[6:9]
	v_mfma_f32_16x16x32_bf16 v[2:5], v[180:183], v[212:215], v[2:5]
	s_setprio 0
	s_barrier
	s_add_i32 s78, s78, 2
	s_add_u32 s26, s26, 0x100
	s_addc_u32 s27, s27, 0
	s_add_u32 s62, s62, 0x100
	s_addc_u32 s63, s63, 0
	s_cmp_gt_u32 s78, 29
	s_cbranch_scc0 .LBB0_230
	s_and_b64 vcc, exec, s[8:9]
	s_mov_b32 s88, s4
	s_cbranch_vccz .LBB0_233
	s_barrier

; #define PG8_STAGE(bufoff, gbase, voff) do { _Pragma("unroll") for (int _i = 0; _i < 2; ++_i) \
;         __builtin_amdgcn_global_load_lds((const unsigned*)((const char*)(gbase) + (voff)[_i]), (PG8_LAS unsigned*)(lds + (bufoff) + ldsw + _i * 8192), 16, 0, 0); } while (0)
; #define PG8_LDA(dst, b, h) do { _Pragma("unroll") for (int m = 0; m < 4; ++m) _Pragma("unroll") for (int k = 0; k < 2; ++k) dst[m][k] = *(const PG8_LAS bf16x8*)(lds + PG8_SA(b, h) + aoff + m * 2048 + k * 1024); } while (0)
; #define PG8_LDB(dst, b, h) do { _Pragma("unroll") for (int n = 0; n < 2; ++n) _Pragma("unroll") for (int k = 0; k < 2; ++k) dst[n][k] = *(const PG8_LAS bf16x8*)(lds + PG8_SB(b, h) + boff + n * 2048 + k * 1024); } while (0)
; #define PG8_MMA(ai, bj, At, Bt) do { __builtin_amdgcn_s_setprio(1); _Pragma("unroll") for (int m = 0; m < 4; ++m) _Pragma("unroll") for (int n = 0; n < 2; ++n) _Pragma("unroll") for (int k = 0; k < 2; ++k) \
;         acc[ai][bj][m][n] = __builtin_amdgcn_mfma_f32_16x16x32_bf16(Bt[n][k], At[m][k], acc[ai][bj][m][n], 0, 0, 0); __builtin_amdgcn_s_setprio(0); } while (0)
; #define PG8_WAIT_V(n) asm volatile("s_waitcnt vmcnt(" #n ")" ::: "memory")
; #define PG8_WAIT_L(n) asm volatile("s_waitcnt lgkmcnt(" #n ")" ::: "memory")
; #define PG8_BAR __builtin_amdgcn_s_barrier()
; #define PG8_SCHED __builtin_amdgcn_sched_barrier(0)
; template <class Epi, class Sched, bool ALIGN_EPI = false, bool SP2 = false>
; __device__ __forceinline__ void gemm_phase(PG8_LAS unsigned char* lds, const Gemm g, const Sched& S, const Epi& E) {
;     ...
;         for (int t = 0; t < nt; t += 2) {
;             const bool last = (t == nt - 2);
;             const char* a1 = cA + (size_t)(t + 1) * kstep;
;             const char* a2 = last ? nA : cA + (size_t)(t + 2) * kstep; const char* b2 = last ? nB : cB + (size_t)(t + 2) * kstep;
;             const char* a3 = a2 + kstep; const char* b3 = b2 + kstep;
;             if (last && has_next) S.a_ready(nxt);
;             if constexpr (SP2) {
;             PG8_LDB(B0, 0, 0); PG8_LDB(B1, 0, 1); PG8_SCHED; PG8_LDA(At, 0, 0); PG8_STAGE(PG8_SA(1, 1), a1 + hstep, voffA);
;             PG8_WAIT_V(8); PG8_WAIT_L(0); PG8_BAR; PG8_MMA(0, 0, At, B0); PG8_MMA(0, 1, At, B1); PG8_BAR; PG8_SCHED;
;             PG8_LDA(At, 0, 1); PG8_STAGE(PG8_SB(0, 0), b2, voffB); PG8_STAGE(PG8_SB(0, 1), b2 + hstep, voffB); PG8_STAGE(PG8_SA(0, 0), a2, voffA);
.LBB0_892:
	ds_read_b128 v[144:147], v155
	ds_read_b128 v[148:151], v155 offset:1024
	ds_read_b128 v[166:169], v155 offset:2048
	ds_read_b128 v[170:173], v155 offset:3072
	ds_read_b128 v[174:177], v156
	ds_read_b128 v[178:181], v156 offset:1024
	ds_read_b128 v[182:185], v156 offset:2048
	ds_read_b128 v[190:193], v156 offset:3072
	s_add_u32 s28, s26, 0x100
	s_addc_u32 s29, s27, 0
	s_cmp_eq_u32 s45, 28
	s_cselect_b32 s35, s7, s29
	s_cselect_b32 s34, s19, s28
	s_cselect_b32 s31, s17, s44
	s_cselect_b32 s30, s42, s43
	v_lshl_add_u64 v[160:161], s[26:27], 0, v[136:137]
	s_add_i32 m0, s3, 0xc000
	ds_read_b128 v[194:197], v157
	ds_read_b128 v[198:201], v157 offset:1024
	ds_read_b128 v[202:205], v157 offset:2048
	ds_read_b128 v[206:209], v157 offset:3072
	ds_read_b128 v[210:213], v157 offset:4096
	ds_read_b128 v[214:217], v157 offset:5120
	ds_read_b128 v[218:221], v157 offset:6144
	ds_read_b128 v[222:225], v157 offset:7168
	global_load_lds_dwordx4 v[160:161], off
	s_add_i32 m0, s3, 0xe000
	v_lshl_add_u64 v[160:161], s[26:27], 0, v[138:139]
	global_load_lds_dwordx4 v[160:161], off
	s_waitcnt vmcnt(8)
	s_waitcnt lgkmcnt(0)
	s_barrier
	s_setprio 1
	s_waitcnt lgkmcnt(0)
	v_mfma_f32_16x16x32_bf16 v[126:129], v[144:147], v[194:197], v[126:129]
	v_mfma_f32_16x16x32_bf16 v[122:125], v[166:169], v[194:197], v[122:125]
	v_mfma_f32_16x16x32_bf16 v[110:113], v[144:147], v[202:205], v[110:113]
	v_mfma_f32_16x16x32_bf16 v[106:109], v[166:169], v[202:205], v[106:109]
	v_mfma_f32_16x16x32_bf16 v[94:97], v[144:147], v[210:213], v[94:97]
	v_mfma_f32_16x16x32_bf16 v[90:93], v[166:169], v[210:213], v[90:93]
	v_mfma_f32_16x16x32_bf16 v[78:81], v[144:147], v[218:221], v[78:81]
	v_mfma_f32_16x16x32_bf16 v[74:77], v[166:169], v[218:221], v[74:77]
	v_mfma_f32_16x16x32_bf16 v[126:129], v[148:151], v[198:201], v[126:129]
	v_mfma_f32_16x16x32_bf16 v[122:125], v[170:173], v[198:201], v[122:125]
	v_mfma_f32_16x16x32_bf16 v[110:113], v[148:151], v[206:209], v[110:113]
	v_mfma_f32_16x16x32_bf16 v[106:109], v[170:173], v[206:209], v[106:109]
	v_mfma_f32_16x16x32_bf16 v[94:97], v[148:151], v[214:217], v[94:97]
	v_mfma_f32_16x16x32_bf16 v[90:93], v[170:173], v[214:217], v[90:93]
	v_mfma_f32_16x16x32_bf16 v[78:81], v[148:151], v[222:225], v[78:81]
	v_mfma_f32_16x16x32_bf16 v[74:77], v[170:173], v[222:225], v[74:77]
	v_mfma_f32_16x16x32_bf16 v[118:121], v[174:177], v[194:197], v[118:121]
	v_mfma_f32_16x16x32_bf16 v[114:117], v[182:185], v[194:197], v[114:117]
	v_mfma_f32_16x16x32_bf16 v[102:105], v[174:177], v[202:205], v[102:105]
	v_mfma_f32_16x16x32_bf16 v[98:101], v[182:185], v[202:205], v[98:101]
	v_mfma_f32_16x16x32_bf16 v[86:89], v[174:177], v[210:213], v[86:89]
	v_mfma_f32_16x16x32_bf16 v[82:85], v[182:185], v[210:213], v[82:85]
	v_mfma_f32_16x16x32_bf16 v[70:73], v[174:177], v[218:221], v[70:73]
	v_mfma_f32_16x16x32_bf16 v[66:69], v[182:185], v[218:221], v[66:69]
	v_mfma_f32_16x16x32_bf16 v[118:121], v[178:181], v[198:201], v[118:121]
	v_mfma_f32_16x16x32_bf16 v[114:117], v[190:193], v[198:201], v[114:117]
	v_mfma_f32_16x16x32_bf16 v[102:105], v[178:181], v[206:209], v[102:105]
	v_mfma_f32_16x16x32_bf16 v[98:101], v[190:193], v[206:209], v[98:101]
	v_mfma_f32_16x16x32_bf16 v[86:89], v[178:181], v[214:217], v[86:89]
	v_mfma_f32_16x16x32_bf16 v[82:85], v[190:193], v[214:217], v[82:85]
	v_mfma_f32_16x16x32_bf16 v[70:73], v[178:181], v[222:225], v[70:73]
	v_mfma_f32_16x16x32_bf16 v[66:69], v[190:193], v[222:225], v[66:69]
	s_setprio 0
	s_barrier
	s_add_i32 s26, s39, s2
	v_lshl_add_u64 v[160:161], s[30:31], 0, v[130:131]
	s_mov_b32 m0, s26
	ds_read_b128 v[194:197], v157 offset:16384
	ds_read_b128 v[198:201], v157 offset:17408
	ds_read_b128 v[202:205], v157 offset:18432
	ds_read_b128 v[206:209], v157 offset:19456
	ds_read_b128 v[210:213], v157 offset:20480
	ds_read_b128 v[214:217], v157 offset:21504
	ds_read_b128 v[218:221], v157 offset:22528
	ds_read_b128 v[222:225], v157 offset:23552
	global_load_lds_dwordx4 v[160:161], off
	s_add_i32 m0, s26, 0x2000
	s_add_u32 s26, s30, 0x80000
	v_lshl_add_u64 v[186:187], s[30:31], 0, v[132:133]
	s_addc_u32 s27, s31, 0
	s_add_i32 s46, s40, s2
	global_load_lds_dwordx4 v[186:187], off
	v_lshl_add_u64 v[226:227], s[26:27], 0, v[130:131]
	s_mov_b32 m0, s46
	v_lshl_add_u64 v[228:229], s[34:35], 0, v[132:133]
	global_load_lds_dwordx4 v[226:227], off
	s_add_i32 m0, s46, 0x2000
	v_lshl_add_u64 v[226:227], s[26:27], 0, v[132:133]
	global_load_lds_dwordx4 v[226:227], off
	s_mov_b32 m0, s3
	v_lshl_add_u64 v[226:227], s[34:35], 0, v[130:131]
	global_load_lds_dwordx4 v[226:227], off
	s_mov_b32 m0, s4
	s_nop 0
	global_load_lds_dwordx4 v[228:229], off
	s_waitcnt vmcnt(8)
	s_waitcnt lgkmcnt(0)
	s_barrier
; #define PG8_STAGE(bufoff, gbase, voff) do { _Pragma("unroll") for (int _i = 0; _i < 2; ++_i) \
;         __builtin_amdgcn_global_load_lds((const unsigned*)((const char*)(gbase) + (voff)[_i]), (PG8_LAS unsigned*)(lds + (bufoff) + ldsw + _i * 8192), 16, 0, 0); } while (0)
; #define PG8_LDA(dst, b, h) do { _Pragma("unroll") for (int m = 0; m < 4; ++m) _Pragma("unroll") for (int k = 0; k < 2; ++k) dst[m][k] = *(const PG8_LAS bf16x8*)(lds + PG8_SA(b, h) + aoff + m * 2048 + k * 1024); } while (0)
; #define PG8_LDB(dst, b, h) do { _Pragma("unroll") for (int n = 0; n < 2; ++n) _Pragma("unroll") for (int k = 0; k < 2; ++k) dst[n][k] = *(const PG8_LAS bf16x8*)(lds + PG8_SB(b, h) + boff + n * 2048 + k * 1024); } while (0)
; #define PG8_MMA(ai, bj, At, Bt) do { __builtin_amdgcn_s_setprio(1); _Pragma("unroll") for (int m = 0; m < 4; ++m) _Pragma("unroll") for (int n = 0; n < 2; ++n) _Pragma("unroll") for (int k = 0; k < 2; ++k) \
;         acc[ai][bj][m][n] = __builtin_amdgcn_mfma_f32_16x16x32_bf16(Bt[n][k], At[m][k], acc[ai][bj][m][n], 0, 0, 0); __builtin_amdgcn_s_setprio(0); } while (0)
; #define PG8_WAIT_V(n) asm volatile("s_waitcnt vmcnt(" #n ")" ::: "memory")
; #define PG8_WAIT_L(n) asm volatile("s_waitcnt lgkmcnt(" #n ")" ::: "memory")
; #define PG8_BAR __builtin_amdgcn_s_barrier()
; #define PG8_SCHED __builtin_amdgcn_sched_barrier(0)
; template <class Epi, class Sched, bool ALIGN_EPI = false, bool SP2 = false>
; __device__ __forceinline__ void gemm_phase(PG8_LAS unsigned char* lds, const Gemm g, const Sched& S, const Epi& E) {
;     ...
;             PG8_WAIT_V(8); PG8_WAIT_L(0); PG8_BAR; PG8_MMA(1, 0, At, B0); PG8_MMA(1, 1, At, B1); PG8_BAR; PG8_SCHED;
;             PG8_LDB(B0, 1, 0); PG8_LDB(B1, 1, 1); PG8_SCHED; PG8_LDA(At, 1, 0); PG8_STAGE(PG8_SA(0, 1), a2 + hstep, voffA);
;             PG8_WAIT_V(8); PG8_WAIT_L(0); PG8_BAR; PG8_MMA(0, 0, At, B0); PG8_MMA(0, 1, At, B1); PG8_BAR; PG8_SCHED;
	s_setprio 1
	s_waitcnt lgkmcnt(0)
	v_mfma_f32_16x16x32_bf16 v[62:65], v[144:147], v[194:197], v[62:65]
	v_mfma_f32_16x16x32_bf16 v[58:61], v[166:169], v[194:197], v[58:61]
	v_mfma_f32_16x16x32_bf16 v[46:49], v[144:147], v[202:205], v[46:49]
	v_mfma_f32_16x16x32_bf16 v[42:45], v[166:169], v[202:205], v[42:45]
	v_mfma_f32_16x16x32_bf16 v[30:33], v[144:147], v[210:213], v[30:33]
	v_mfma_f32_16x16x32_bf16 v[26:29], v[166:169], v[210:213], v[26:29]
	v_mfma_f32_16x16x32_bf16 v[14:17], v[144:147], v[218:221], v[14:17]
	v_mfma_f32_16x16x32_bf16 v[10:13], v[166:169], v[218:221], v[10:13]
	v_mfma_f32_16x16x32_bf16 v[62:65], v[148:151], v[198:201], v[62:65]
	v_mfma_f32_16x16x32_bf16 v[58:61], v[170:173], v[198:201], v[58:61]
	v_mfma_f32_16x16x32_bf16 v[46:49], v[148:151], v[206:209], v[46:49]
	v_mfma_f32_16x16x32_bf16 v[42:45], v[170:173], v[206:209], v[42:45]
	v_mfma_f32_16x16x32_bf16 v[30:33], v[148:151], v[214:217], v[30:33]
	v_mfma_f32_16x16x32_bf16 v[26:29], v[170:173], v[214:217], v[26:29]
	v_mfma_f32_16x16x32_bf16 v[14:17], v[148:151], v[222:225], v[14:17]
	v_mfma_f32_16x16x32_bf16 v[10:13], v[170:173], v[222:225], v[10:13]
	v_mfma_f32_16x16x32_bf16 v[54:57], v[174:177], v[194:197], v[54:57]
	v_mfma_f32_16x16x32_bf16 v[50:53], v[182:185], v[194:197], v[50:53]
	v_mfma_f32_16x16x32_bf16 v[38:41], v[174:177], v[202:205], v[38:41]
	v_mfma_f32_16x16x32_bf16 v[34:37], v[182:185], v[202:205], v[34:37]
	v_mfma_f32_16x16x32_bf16 v[22:25], v[174:177], v[210:213], v[22:25]
	v_mfma_f32_16x16x32_bf16 v[18:21], v[182:185], v[210:213], v[18:21]
	v_mfma_f32_16x16x32_bf16 v[6:9], v[174:177], v[218:221], v[6:9]
	v_mfma_f32_16x16x32_bf16 v[2:5], v[182:185], v[218:221], v[2:5]
	v_mfma_f32_16x16x32_bf16 v[54:57], v[178:181], v[198:201], v[54:57]
	v_mfma_f32_16x16x32_bf16 v[50:53], v[190:193], v[198:201], v[50:53]
	v_mfma_f32_16x16x32_bf16 v[38:41], v[178:181], v[206:209], v[38:41]
	v_mfma_f32_16x16x32_bf16 v[34:37], v[190:193], v[206:209], v[34:37]
	v_mfma_f32_16x16x32_bf16 v[22:25], v[178:181], v[214:217], v[22:25]
	v_mfma_f32_16x16x32_bf16 v[18:21], v[190:193], v[214:217], v[18:21]
	v_mfma_f32_16x16x32_bf16 v[6:9], v[178:181], v[222:225], v[6:9]
	v_mfma_f32_16x16x32_bf16 v[2:5], v[190:193], v[222:225], v[2:5]
	s_setprio 0
	s_barrier
	s_add_i32 s46, 0, 0x18000
	v_add_u32_e32 v134, s46, v153
	s_add_i32 s47, 0, 0x1c000
	ds_read_b128 v[144:147], v134
	ds_read_b128 v[148:151], v134 offset:1024
	ds_read_b128 v[166:169], v134 offset:2048
	ds_read_b128 v[170:173], v134 offset:3072
	v_add_u32_e32 v134, s47, v153
	ds_read_b128 v[174:177], v134
	ds_read_b128 v[178:181], v134 offset:1024
	ds_read_b128 v[182:185], v134 offset:2048
	ds_read_b128 v[190:193], v134 offset:3072
	s_add_u32 s26, s34, 0x80000
	s_addc_u32 s27, s35, 0
	s_mov_b32 m0, s5
	v_lshl_add_u64 v[230:231], s[26:27], 0, v[130:131]
	ds_read_b128 v[194:197], v157 offset:32768
	ds_read_b128 v[198:201], v157 offset:33792
	ds_read_b128 v[202:205], v157 offset:34816
	ds_read_b128 v[206:209], v157 offset:35840
	ds_read_b128 v[210:213], v157 offset:36864
	ds_read_b128 v[214:217], v157 offset:37888
	ds_read_b128 v[218:221], v157 offset:38912
	ds_read_b128 v[222:225], v157 offset:39936
	global_load_lds_dwordx4 v[230:231], off
	s_mov_b32 m0, s25
	v_lshl_add_u64 v[230:231], s[26:27], 0, v[132:133]
	global_load_lds_dwordx4 v[230:231], off
	s_waitcnt vmcnt(8)
	s_waitcnt lgkmcnt(0)
	s_barrier
	s_setprio 1
	s_waitcnt lgkmcnt(0)
	v_mfma_f32_16x16x32_bf16 v[126:129], v[144:147], v[194:197], v[126:129]
	v_mfma_f32_16x16x32_bf16 v[122:125], v[166:169], v[194:197], v[122:125]
	v_mfma_f32_16x16x32_bf16 v[110:113], v[144:147], v[202:205], v[110:113]
	v_mfma_f32_16x16x32_bf16 v[106:109], v[166:169], v[202:205], v[106:109]
	v_mfma_f32_16x16x32_bf16 v[94:97], v[144:147], v[210:213], v[94:97]
	v_mfma_f32_16x16x32_bf16 v[90:93], v[166:169], v[210:213], v[90:93]
	v_mfma_f32_16x16x32_bf16 v[78:81], v[144:147], v[218:221], v[78:81]
	v_mfma_f32_16x16x32_bf16 v[74:77], v[166:169], v[218:221], v[74:77]
	v_mfma_f32_16x16x32_bf16 v[126:129], v[148:151], v[198:201], v[126:129]
	v_mfma_f32_16x16x32_bf16 v[122:125], v[170:173], v[198:201], v[122:125]
	v_mfma_f32_16x16x32_bf16 v[110:113], v[148:151], v[206:209], v[110:113]
	v_mfma_f32_16x16x32_bf16 v[106:109], v[170:173], v[206:209], v[106:109]
	v_mfma_f32_16x16x32_bf16 v[94:97], v[148:151], v[214:217], v[94:97]
	v_mfma_f32_16x16x32_bf16 v[90:93], v[170:173], v[214:217], v[90:93]
	v_mfma_f32_16x16x32_bf16 v[78:81], v[148:151], v[222:225], v[78:81]
	v_mfma_f32_16x16x32_bf16 v[74:77], v[170:173], v[222:225], v[74:77]
	v_mfma_f32_16x16x32_bf16 v[118:121], v[174:177], v[194:197], v[118:121]
	v_mfma_f32_16x16x32_bf16 v[114:117], v[182:185], v[194:197], v[114:117]
	v_mfma_f32_16x16x32_bf16 v[102:105], v[174:177], v[202:205], v[102:105]
	v_mfma_f32_16x16x32_bf16 v[98:101], v[182:185], v[202:205], v[98:101]
	v_mfma_f32_16x16x32_bf16 v[86:89], v[174:177], v[210:213], v[86:89]
	v_mfma_f32_16x16x32_bf16 v[82:85], v[182:185], v[210:213], v[82:85]
	v_mfma_f32_16x16x32_bf16 v[70:73], v[174:177], v[218:221], v[70:73]
	v_mfma_f32_16x16x32_bf16 v[66:69], v[182:185], v[218:221], v[66:69]
	v_mfma_f32_16x16x32_bf16 v[118:121], v[178:181], v[198:201], v[118:121]
	v_mfma_f32_16x16x32_bf16 v[114:117], v[190:193], v[198:201], v[114:117]
	v_mfma_f32_16x16x32_bf16 v[102:105], v[178:181], v[206:209], v[102:105]
	v_mfma_f32_16x16x32_bf16 v[98:101], v[190:193], v[206:209], v[98:101]
	v_mfma_f32_16x16x32_bf16 v[86:89], v[178:181], v[214:217], v[86:89]
	v_mfma_f32_16x16x32_bf16 v[82:85], v[190:193], v[214:217], v[82:85]
	v_mfma_f32_16x16x32_bf16 v[70:73], v[178:181], v[222:225], v[70:73]
	v_mfma_f32_16x16x32_bf16 v[66:69], v[190:193], v[222:225], v[66:69]
	s_setprio 0
	s_barrier
; #define PG8_STAGE(bufoff, gbase, voff) do { _Pragma("unroll") for (int _i = 0; _i < 2; ++_i) \
;         __builtin_amdgcn_global_load_lds((const unsigned*)((const char*)(gbase) + (voff)[_i]), (PG8_LAS unsigned*)(lds + (bufoff) + ldsw + _i * 8192), 16, 0, 0); } while (0)
; #define PG8_LDA(dst, b, h) do { _Pragma("unroll") for (int m = 0; m < 4; ++m) _Pragma("unroll") for (int k = 0; k < 2; ++k) dst[m][k] = *(const PG8_LAS bf16x8*)(lds + PG8_SA(b, h) + aoff + m * 2048 + k * 1024); } while (0)
; #define PG8_MMA(ai, bj, At, Bt) do { __builtin_amdgcn_s_setprio(1); _Pragma("unroll") for (int m = 0; m < 4; ++m) _Pragma("unroll") for (int n = 0; n < 2; ++n) _Pragma("unroll") for (int k = 0; k < 2; ++k) \
;         acc[ai][bj][m][n] = __builtin_amdgcn_mfma_f32_16x16x32_bf16(Bt[n][k], At[m][k], acc[ai][bj][m][n], 0, 0, 0); __builtin_amdgcn_s_setprio(0); } while (0)
; #define PG8_WAIT_V(n) asm volatile("s_waitcnt vmcnt(" #n ")" ::: "memory")
; #define PG8_WAIT_L(n) asm volatile("s_waitcnt lgkmcnt(" #n ")" ::: "memory")
; #define PG8_BAR __builtin_amdgcn_s_barrier()
; #define PG8_SCHED __builtin_amdgcn_sched_barrier(0)
; template <class Epi, class Sched, bool ALIGN_EPI = false, bool SP2 = false>
; __device__ __forceinline__ void gemm_phase(PG8_LAS unsigned char* lds, const Gemm g, const Sched& S, const Epi& E) {
;     ...
;             PG8_LDA(At, 1, 1); PG8_STAGE(PG8_SB(1, 0), b3, voffB); PG8_STAGE(PG8_SB(1, 1), b3 + hstep, voffB); PG8_STAGE(PG8_SA(1, 0), a3, voffA);
;             PG8_WAIT_V(8); PG8_WAIT_L(0); PG8_BAR; PG8_MMA(1, 0, At, B0); PG8_MMA(1, 1, At, B1); PG8_BAR; PG8_SCHED;
;     ...
;         if constexpr (ALIGN_EPI) { if (wr == 0) PG8_BAR; }
	s_add_i32 s26, s46, s2
	v_lshl_add_u64 v[160:161], v[160:161], 0, s[12:13]
	s_mov_b32 m0, s26
	ds_read_b128 v[194:197], v157 offset:49152
	ds_read_b128 v[198:201], v157 offset:50176
	ds_read_b128 v[202:205], v157 offset:51200
	ds_read_b128 v[206:209], v157 offset:52224
	ds_read_b128 v[210:213], v157 offset:53248
	ds_read_b128 v[214:217], v157 offset:54272
	ds_read_b128 v[218:221], v157 offset:55296
	ds_read_b128 v[222:225], v157 offset:56320
	global_load_lds_dwordx4 v[160:161], off
	s_add_i32 m0, s26, 0x2000
	s_add_u32 s26, s30, 0x80080
	v_lshl_add_u64 v[160:161], v[186:187], 0, s[12:13]
	s_addc_u32 s27, s31, 0
	s_add_i32 s30, s47, s2
	global_load_lds_dwordx4 v[160:161], off
	s_mov_b32 m0, s30
	v_lshl_add_u64 v[160:161], s[26:27], 0, v[130:131]
	global_load_lds_dwordx4 v[160:161], off
	s_add_i32 m0, s30, 0x2000
	v_lshl_add_u64 v[160:161], s[26:27], 0, v[132:133]
	global_load_lds_dwordx4 v[160:161], off
	s_mov_b32 m0, s37
	v_lshl_add_u64 v[160:161], v[226:227], 0, s[12:13]
	global_load_lds_dwordx4 v[160:161], off
	s_mov_b32 m0, s38
	v_lshl_add_u64 v[160:161], v[228:229], 0, s[12:13]
	global_load_lds_dwordx4 v[160:161], off
	s_waitcnt vmcnt(8)
	s_waitcnt lgkmcnt(0)
	s_barrier
	s_setprio 1
	s_waitcnt lgkmcnt(0)
	v_mfma_f32_16x16x32_bf16 v[62:65], v[144:147], v[194:197], v[62:65]
	v_mfma_f32_16x16x32_bf16 v[58:61], v[166:169], v[194:197], v[58:61]
	v_mfma_f32_16x16x32_bf16 v[46:49], v[144:147], v[202:205], v[46:49]
	v_mfma_f32_16x16x32_bf16 v[42:45], v[166:169], v[202:205], v[42:45]
	v_mfma_f32_16x16x32_bf16 v[30:33], v[144:147], v[210:213], v[30:33]
	v_mfma_f32_16x16x32_bf16 v[26:29], v[166:169], v[210:213], v[26:29]
	v_mfma_f32_16x16x32_bf16 v[14:17], v[144:147], v[218:221], v[14:17]
	v_mfma_f32_16x16x32_bf16 v[10:13], v[166:169], v[218:221], v[10:13]
	v_mfma_f32_16x16x32_bf16 v[62:65], v[148:151], v[198:201], v[62:65]
	v_mfma_f32_16x16x32_bf16 v[58:61], v[170:173], v[198:201], v[58:61]
	v_mfma_f32_16x16x32_bf16 v[46:49], v[148:151], v[206:209], v[46:49]
	v_mfma_f32_16x16x32_bf16 v[42:45], v[170:173], v[206:209], v[42:45]
	v_mfma_f32_16x16x32_bf16 v[30:33], v[148:151], v[214:217], v[30:33]
	v_mfma_f32_16x16x32_bf16 v[26:29], v[170:173], v[214:217], v[26:29]
	v_mfma_f32_16x16x32_bf16 v[14:17], v[148:151], v[222:225], v[14:17]
	v_mfma_f32_16x16x32_bf16 v[10:13], v[170:173], v[222:225], v[10:13]
	v_mfma_f32_16x16x32_bf16 v[54:57], v[174:177], v[194:197], v[54:57]
	v_mfma_f32_16x16x32_bf16 v[50:53], v[182:185], v[194:197], v[50:53]
	v_mfma_f32_16x16x32_bf16 v[38:41], v[174:177], v[202:205], v[38:41]
	v_mfma_f32_16x16x32_bf16 v[34:37], v[182:185], v[202:205], v[34:37]
	v_mfma_f32_16x16x32_bf16 v[22:25], v[174:177], v[210:213], v[22:25]
	v_mfma_f32_16x16x32_bf16 v[18:21], v[182:185], v[210:213], v[18:21]
	v_mfma_f32_16x16x32_bf16 v[6:9], v[174:177], v[218:221], v[6:9]
	v_mfma_f32_16x16x32_bf16 v[2:5], v[182:185], v[218:221], v[2:5]
	v_mfma_f32_16x16x32_bf16 v[54:57], v[178:181], v[198:201], v[54:57]
	v_mfma_f32_16x16x32_bf16 v[50:53], v[190:193], v[198:201], v[50:53]
	v_mfma_f32_16x16x32_bf16 v[38:41], v[178:181], v[206:209], v[38:41]
	v_mfma_f32_16x16x32_bf16 v[34:37], v[190:193], v[206:209], v[34:37]
	v_mfma_f32_16x16x32_bf16 v[22:25], v[178:181], v[214:217], v[22:25]
	v_mfma_f32_16x16x32_bf16 v[18:21], v[190:193], v[214:217], v[18:21]
	v_mfma_f32_16x16x32_bf16 v[6:9], v[178:181], v[222:225], v[6:9]
	v_mfma_f32_16x16x32_bf16 v[2:5], v[190:193], v[222:225], v[2:5]
	s_setprio 0
	s_barrier
	s_add_i32 s45, s45, 2
	s_add_u32 s43, s43, 0x100
	s_addc_u32 s44, s44, 0
	s_cmp_gt_u32 s45, 29
	s_mov_b64 s[26:27], s[28:29]
	s_cbranch_scc0 .LBB0_892
	s_and_b64 vcc, exec, s[14:15]
	s_cbranch_vccz .LBB0_895
	s_barrier

; #define PG8_STAGE(bufoff, gbase, voff) do { _Pragma("unroll") for (int _i = 0; _i < 2; ++_i) \
;         __builtin_amdgcn_global_load_lds((const unsigned*)((const char*)(gbase) + (voff)[_i]), (PG8_LAS unsigned*)(lds + (bufoff) + ldsw + _i * 8192), 16, 0, 0); } while (0)
; #define PG8_LDA(dst, b, h) do { _Pragma("unroll") for (int m = 0; m < 4; ++m) _Pragma("unroll") for (int k = 0; k < 2; ++k) dst[m][k] = *(const PG8_LAS bf16x8*)(lds + PG8_SA(b, h) + aoff + m * 2048 + k * 1024); } while (0)
; #define PG8_LDB(dst, b, h) do { _Pragma("unroll") for (int n = 0; n < 2; ++n) _Pragma("unroll") for (int k = 0; k < 2; ++k) dst[n][k] = *(const PG8_LAS bf16x8*)(lds + PG8_SB(b, h) + boff + n * 2048 + k * 1024); } while (0)
; #define PG8_MMA(ai, bj, At, Bt) do { __builtin_amdgcn_s_setprio(1); _Pragma("unroll") for (int m = 0; m < 4; ++m) _Pragma("unroll") for (int n = 0; n < 2; ++n) _Pragma("unroll") for (int k = 0; k < 2; ++k) \
;         acc[ai][bj][m][n] = __builtin_amdgcn_mfma_f32_16x16x32_bf16(Bt[n][k], At[m][k], acc[ai][bj][m][n], 0, 0, 0); __builtin_amdgcn_s_setprio(0); } while (0)
; #define PG8_BAR __builtin_amdgcn_s_barrier()
; template <class Epi, class Sched, bool ALIGN_EPI = false, bool SP2 = false>
; __device__ __forceinline__ void gemm_phase(PG8_LAS unsigned char* lds, const Gemm g, const Sched& S, const Epi& E) {
;     ...
;         const char* nA = has_next ? (const char*)g.A + (size_t)nxt.pm * tstep + (size_t)nxt.k0 * 2 : cA; const char* nB = has_next ? (const char*)g.Bt + (size_t)nxt.pn * tstep + (size_t)nxt.k0 * 2 : cB;
;         for (int t = 0; t < nt; t += 2) {
;             const bool last = (t == nt - 2);
;             const char* a1 = cA + (size_t)(t + 1) * kstep;
;             const char* a2 = last ? nA : cA + (size_t)(t + 2) * kstep; const char* b2 = last ? nB : cB + (size_t)(t + 2) * kstep;
;             const char* a3 = a2 + kstep; const char* b3 = b2 + kstep;
;             if (last && has_next) S.a_ready(nxt);
;             if constexpr (SP2) {
;             PG8_LDB(B0, 0, 0); PG8_LDB(B1, 0, 1); PG8_SCHED; PG8_LDA(At, 0, 0); PG8_STAGE(PG8_SA(1, 1), a1 + hstep, voffA);
;             PG8_WAIT_V(8); PG8_WAIT_L(0); PG8_BAR; PG8_MMA(0, 0, At, B0); PG8_MMA(0, 1, At, B1); PG8_BAR; PG8_SCHED;
;             PG8_LDA(At, 0, 1); PG8_STAGE(PG8_SB(0, 0), b2, voffB); PG8_STAGE(PG8_SB(0, 1), b2 + hstep, voffB); PG8_STAGE(PG8_SA(0, 0), a2, voffA);
.LBB0_944:
	s_add_u32 s25, s16, s23
	s_addc_u32 s27, s17, 0
	s_add_u32 s38, s25, 0x100
	s_addc_u32 s39, s27, 0
	s_and_b64 s[36:37], s[34:35], exec
	s_cselect_b32 s39, s7, s39
	s_cselect_b32 s38, s6, s38
	s_add_u32 s23, s14, s23
	s_addc_u32 s36, s15, 0
	s_add_u32 s23, s23, 0x100
	s_addc_u32 s36, s36, 0
	s_and_b64 s[34:35], s[34:35], exec
	s_cselect_b32 s41, s29, s36
	s_cselect_b32 s40, s28, s23
	s_add_u32 s44, s25, 0x80080
	s_addc_u32 s45, s27, 0
	s_add_i32 s59, s49, s2
	ds_read_b128 v[144:147], v141
	ds_read_b128 v[148:151], v141 offset:1024
	ds_read_b128 v[152:155], v141 offset:2048
	ds_read_b128 v[156:159], v141 offset:3072
	ds_read_b128 v[166:169], v142
	ds_read_b128 v[170:173], v142 offset:1024
	ds_read_b128 v[174:177], v142 offset:2048
	ds_read_b128 v[178:181], v142 offset:3072
	s_add_i32 m0, s3, 0xc000
	s_add_i32 s60, s3, 0xe000
	s_add_i32 s56, s59, 0x2000
	s_add_u32 s42, s40, 0x80000
	s_addc_u32 s43, s41, 0
	s_add_i32 s58, s50, s2
	s_add_i32 s57, s58, 0x2000
	s_add_i32 s55, 0, 0x18000
	s_add_i32 s54, 0, 0x1c000
	s_add_u32 s36, s38, 0x80000
	s_addc_u32 s37, s39, 0
	s_add_i32 s53, s55, s2
	s_add_i32 s25, s53, 0x2000
	s_add_u32 s34, s40, 0x80080
	s_addc_u32 s35, s41, 0
	s_add_i32 s27, s54, s2
	s_add_i32 s23, s27, 0x2000
	v_lshl_add_u64 v[160:161], s[44:45], 0, v[132:133]
	ds_read_b128 v[182:185], v143
	ds_read_b128 v[190:193], v143 offset:1024
	ds_read_b128 v[194:197], v143 offset:2048
	ds_read_b128 v[198:201], v143 offset:3072
	ds_read_b128 v[202:205], v143 offset:4096
	ds_read_b128 v[206:209], v143 offset:5120
	ds_read_b128 v[210:213], v143 offset:6144
	ds_read_b128 v[214:217], v143 offset:7168
	global_load_lds_dwordx4 v[160:161], off
	s_mov_b32 m0, s60
	v_lshl_add_u64 v[160:161], s[44:45], 0, v[130:131]
	global_load_lds_dwordx4 v[160:161], off
	s_waitcnt vmcnt(8)
	s_waitcnt lgkmcnt(0)
	s_barrier
	s_setprio 1
	s_waitcnt lgkmcnt(0)
	v_mfma_f32_16x16x32_bf16 v[126:129], v[144:147], v[182:185], v[126:129]
	v_mfma_f32_16x16x32_bf16 v[122:125], v[152:155], v[182:185], v[122:125]
	v_mfma_f32_16x16x32_bf16 v[118:121], v[144:147], v[194:197], v[118:121]
	v_mfma_f32_16x16x32_bf16 v[114:117], v[152:155], v[194:197], v[114:117]
	v_mfma_f32_16x16x32_bf16 v[106:109], v[144:147], v[202:205], v[106:109]
	v_mfma_f32_16x16x32_bf16 v[98:101], v[152:155], v[202:205], v[98:101]
	v_mfma_f32_16x16x32_bf16 v[90:93], v[144:147], v[210:213], v[90:93]
	v_mfma_f32_16x16x32_bf16 v[82:85], v[152:155], v[210:213], v[82:85]
	v_mfma_f32_16x16x32_bf16 v[126:129], v[148:151], v[190:193], v[126:129]
	v_mfma_f32_16x16x32_bf16 v[122:125], v[156:159], v[190:193], v[122:125]
	v_mfma_f32_16x16x32_bf16 v[118:121], v[148:151], v[198:201], v[118:121]
	v_mfma_f32_16x16x32_bf16 v[114:117], v[156:159], v[198:201], v[114:117]
	v_mfma_f32_16x16x32_bf16 v[106:109], v[148:151], v[206:209], v[106:109]
	v_mfma_f32_16x16x32_bf16 v[98:101], v[156:159], v[206:209], v[98:101]
	v_mfma_f32_16x16x32_bf16 v[90:93], v[148:151], v[214:217], v[90:93]
	v_mfma_f32_16x16x32_bf16 v[82:85], v[156:159], v[214:217], v[82:85]
	v_mfma_f32_16x16x32_bf16 v[110:113], v[166:169], v[182:185], v[110:113]
	v_mfma_f32_16x16x32_bf16 v[102:105], v[174:177], v[182:185], v[102:105]
	v_mfma_f32_16x16x32_bf16 v[94:97], v[166:169], v[194:197], v[94:97]
	v_mfma_f32_16x16x32_bf16 v[86:89], v[174:177], v[194:197], v[86:89]
	v_mfma_f32_16x16x32_bf16 v[78:81], v[166:169], v[202:205], v[78:81]
	v_mfma_f32_16x16x32_bf16 v[74:77], v[174:177], v[202:205], v[74:77]
	v_mfma_f32_16x16x32_bf16 v[70:73], v[166:169], v[210:213], v[70:73]
	v_mfma_f32_16x16x32_bf16 v[66:69], v[174:177], v[210:213], v[66:69]
	v_mfma_f32_16x16x32_bf16 v[110:113], v[170:173], v[190:193], v[110:113]
	v_mfma_f32_16x16x32_bf16 v[102:105], v[178:181], v[190:193], v[102:105]
	v_mfma_f32_16x16x32_bf16 v[94:97], v[170:173], v[198:201], v[94:97]
	v_mfma_f32_16x16x32_bf16 v[86:89], v[178:181], v[198:201], v[86:89]
	v_mfma_f32_16x16x32_bf16 v[78:81], v[170:173], v[206:209], v[78:81]
	v_mfma_f32_16x16x32_bf16 v[74:77], v[178:181], v[206:209], v[74:77]
	v_mfma_f32_16x16x32_bf16 v[70:73], v[170:173], v[214:217], v[70:73]
	v_mfma_f32_16x16x32_bf16 v[66:69], v[178:181], v[214:217], v[66:69]
	s_setprio 0
	s_barrier
	s_mov_b32 m0, s59
	v_lshl_add_u64 v[160:161], s[40:41], 0, v[132:133]
	ds_read_b128 v[182:185], v143 offset:16384
	ds_read_b128 v[190:193], v143 offset:17408
	ds_read_b128 v[194:197], v143 offset:18432
	ds_read_b128 v[198:201], v143 offset:19456
	ds_read_b128 v[202:205], v143 offset:20480
	ds_read_b128 v[206:209], v143 offset:21504
	ds_read_b128 v[210:213], v143 offset:22528
	ds_read_b128 v[214:217], v143 offset:23552
	global_load_lds_dwordx4 v[160:161], off
	v_lshl_add_u64 v[186:187], s[40:41], 0, v[130:131]
	s_mov_b32 m0, s56
	v_lshl_add_u64 v[218:219], s[42:43], 0, v[132:133]
	global_load_lds_dwordx4 v[186:187], off
	s_mov_b32 m0, s58
	v_lshl_add_u64 v[220:221], s[38:39], 0, v[130:131]
	global_load_lds_dwordx4 v[218:219], off
	s_mov_b32 m0, s57
	v_lshl_add_u64 v[218:219], s[42:43], 0, v[130:131]
	global_load_lds_dwordx4 v[218:219], off
	s_mov_b32 m0, s3
	v_lshl_add_u64 v[218:219], s[38:39], 0, v[132:133]
	global_load_lds_dwordx4 v[218:219], off
	s_mov_b32 m0, s4
	s_nop 0
	global_load_lds_dwordx4 v[220:221], off
	s_waitcnt vmcnt(8)
	s_waitcnt lgkmcnt(0)
	s_barrier
; #define PG8_STAGE(bufoff, gbase, voff) do { _Pragma("unroll") for (int _i = 0; _i < 2; ++_i) \
;         __builtin_amdgcn_global_load_lds((const unsigned*)((const char*)(gbase) + (voff)[_i]), (PG8_LAS unsigned*)(lds + (bufoff) + ldsw + _i * 8192), 16, 0, 0); } while (0)
; #define PG8_LDA(dst, b, h) do { _Pragma("unroll") for (int m = 0; m < 4; ++m) _Pragma("unroll") for (int k = 0; k < 2; ++k) dst[m][k] = *(const PG8_LAS bf16x8*)(lds + PG8_SA(b, h) + aoff + m * 2048 + k * 1024); } while (0)
; #define PG8_LDB(dst, b, h) do { _Pragma("unroll") for (int n = 0; n < 2; ++n) _Pragma("unroll") for (int k = 0; k < 2; ++k) dst[n][k] = *(const PG8_LAS bf16x8*)(lds + PG8_SB(b, h) + boff + n * 2048 + k * 1024); } while (0)
; #define PG8_MMA(ai, bj, At, Bt) do { __builtin_amdgcn_s_setprio(1); _Pragma("unroll") for (int m = 0; m < 4; ++m) _Pragma("unroll") for (int n = 0; n < 2; ++n) _Pragma("unroll") for (int k = 0; k < 2; ++k) \
;         acc[ai][bj][m][n] = __builtin_amdgcn_mfma_f32_16x16x32_bf16(Bt[n][k], At[m][k], acc[ai][bj][m][n], 0, 0, 0); __builtin_amdgcn_s_setprio(0); } while (0)
; #define PG8_WAIT_V(n) asm volatile("s_waitcnt vmcnt(" #n ")" ::: "memory")
; #define PG8_WAIT_L(n) asm volatile("s_waitcnt lgkmcnt(" #n ")" ::: "memory")
; #define PG8_BAR __builtin_amdgcn_s_barrier()
; #define PG8_SCHED __builtin_amdgcn_sched_barrier(0)
; template <class Epi, class Sched, bool ALIGN_EPI = false, bool SP2 = false>
; __device__ __forceinline__ void gemm_phase(PG8_LAS unsigned char* lds, const Gemm g, const Sched& S, const Epi& E) {
;     ...
;             PG8_WAIT_V(8); PG8_WAIT_L(0); PG8_BAR; PG8_MMA(1, 0, At, B0); PG8_MMA(1, 1, At, B1); PG8_BAR; PG8_SCHED;
;             PG8_LDB(B0, 1, 0); PG8_LDB(B1, 1, 1); PG8_SCHED; PG8_LDA(At, 1, 0); PG8_STAGE(PG8_SA(0, 1), a2 + hstep, voffA);
;             PG8_WAIT_V(8); PG8_WAIT_L(0); PG8_BAR; PG8_MMA(0, 0, At, B0); PG8_MMA(0, 1, At, B1); PG8_BAR; PG8_SCHED;
	s_setprio 1
	s_waitcnt lgkmcnt(0)
	v_mfma_f32_16x16x32_bf16 v[62:65], v[144:147], v[182:185], v[62:65]
	v_mfma_f32_16x16x32_bf16 v[58:61], v[152:155], v[182:185], v[58:61]
	v_mfma_f32_16x16x32_bf16 v[54:57], v[144:147], v[194:197], v[54:57]
	v_mfma_f32_16x16x32_bf16 v[50:53], v[152:155], v[194:197], v[50:53]
	v_mfma_f32_16x16x32_bf16 v[38:41], v[144:147], v[202:205], v[38:41]
	v_mfma_f32_16x16x32_bf16 v[34:37], v[152:155], v[202:205], v[34:37]
	v_mfma_f32_16x16x32_bf16 v[22:25], v[144:147], v[210:213], v[22:25]
	v_mfma_f32_16x16x32_bf16 v[18:21], v[152:155], v[210:213], v[18:21]
	v_mfma_f32_16x16x32_bf16 v[62:65], v[148:151], v[190:193], v[62:65]
	v_mfma_f32_16x16x32_bf16 v[58:61], v[156:159], v[190:193], v[58:61]
	v_mfma_f32_16x16x32_bf16 v[54:57], v[148:151], v[198:201], v[54:57]
	v_mfma_f32_16x16x32_bf16 v[50:53], v[156:159], v[198:201], v[50:53]
	v_mfma_f32_16x16x32_bf16 v[38:41], v[148:151], v[206:209], v[38:41]
	v_mfma_f32_16x16x32_bf16 v[34:37], v[156:159], v[206:209], v[34:37]
	v_mfma_f32_16x16x32_bf16 v[22:25], v[148:151], v[214:217], v[22:25]
	v_mfma_f32_16x16x32_bf16 v[18:21], v[156:159], v[214:217], v[18:21]
	v_mfma_f32_16x16x32_bf16 v[46:49], v[166:169], v[182:185], v[46:49]
	v_mfma_f32_16x16x32_bf16 v[42:45], v[174:177], v[182:185], v[42:45]
	v_mfma_f32_16x16x32_bf16 v[30:33], v[166:169], v[194:197], v[30:33]
	v_mfma_f32_16x16x32_bf16 v[26:29], v[174:177], v[194:197], v[26:29]
	v_mfma_f32_16x16x32_bf16 v[14:17], v[166:169], v[202:205], v[14:17]
	v_mfma_f32_16x16x32_bf16 v[10:13], v[174:177], v[202:205], v[10:13]
	v_mfma_f32_16x16x32_bf16 v[6:9], v[166:169], v[210:213], v[6:9]
	v_mfma_f32_16x16x32_bf16 v[2:5], v[174:177], v[210:213], v[2:5]
	v_mfma_f32_16x16x32_bf16 v[46:49], v[170:173], v[190:193], v[46:49]
	v_mfma_f32_16x16x32_bf16 v[42:45], v[178:181], v[190:193], v[42:45]
	v_mfma_f32_16x16x32_bf16 v[30:33], v[170:173], v[198:201], v[30:33]
	v_mfma_f32_16x16x32_bf16 v[26:29], v[178:181], v[198:201], v[26:29]
	v_mfma_f32_16x16x32_bf16 v[14:17], v[170:173], v[206:209], v[14:17]
	v_mfma_f32_16x16x32_bf16 v[10:13], v[178:181], v[206:209], v[10:13]
	v_mfma_f32_16x16x32_bf16 v[6:9], v[170:173], v[214:217], v[6:9]
	v_mfma_f32_16x16x32_bf16 v[2:5], v[178:181], v[214:217], v[2:5]
	s_setprio 0
	s_barrier
	v_add_u32_e32 v156, s55, v138
	v_add_u32_e32 v162, s54, v138
	ds_read_b128 v[144:147], v156
	ds_read_b128 v[148:151], v156 offset:1024
	ds_read_b128 v[152:155], v156 offset:2048
	ds_read_b128 v[156:159], v156 offset:3072
	ds_read_b128 v[166:169], v162
	ds_read_b128 v[170:173], v162 offset:1024
	ds_read_b128 v[174:177], v162 offset:2048
	ds_read_b128 v[178:181], v162 offset:3072
	s_mov_b32 m0, s5
	v_lshl_add_u64 v[222:223], s[36:37], 0, v[132:133]
	ds_read_b128 v[182:185], v143 offset:32768
	ds_read_b128 v[190:193], v143 offset:33792
	ds_read_b128 v[194:197], v143 offset:34816
	ds_read_b128 v[198:201], v143 offset:35840
	ds_read_b128 v[202:205], v143 offset:36864
	ds_read_b128 v[206:209], v143 offset:37888
	ds_read_b128 v[210:213], v143 offset:38912
	ds_read_b128 v[214:217], v143 offset:39936
	global_load_lds_dwordx4 v[222:223], off
	s_mov_b32 m0, s11
	v_lshl_add_u64 v[222:223], s[36:37], 0, v[130:131]
	global_load_lds_dwordx4 v[222:223], off
	s_waitcnt vmcnt(8)
	s_waitcnt lgkmcnt(0)
	s_barrier
	s_setprio 1
	s_waitcnt lgkmcnt(0)
	v_mfma_f32_16x16x32_bf16 v[126:129], v[144:147], v[182:185], v[126:129]
	v_mfma_f32_16x16x32_bf16 v[122:125], v[152:155], v[182:185], v[122:125]
	v_mfma_f32_16x16x32_bf16 v[118:121], v[144:147], v[194:197], v[118:121]
	v_mfma_f32_16x16x32_bf16 v[114:117], v[152:155], v[194:197], v[114:117]
	v_mfma_f32_16x16x32_bf16 v[106:109], v[144:147], v[202:205], v[106:109]
	v_mfma_f32_16x16x32_bf16 v[98:101], v[152:155], v[202:205], v[98:101]
	v_mfma_f32_16x16x32_bf16 v[90:93], v[144:147], v[210:213], v[90:93]
	v_mfma_f32_16x16x32_bf16 v[82:85], v[152:155], v[210:213], v[82:85]
	v_mfma_f32_16x16x32_bf16 v[126:129], v[148:151], v[190:193], v[126:129]
	v_mfma_f32_16x16x32_bf16 v[122:125], v[156:159], v[190:193], v[122:125]
	v_mfma_f32_16x16x32_bf16 v[118:121], v[148:151], v[198:201], v[118:121]
	v_mfma_f32_16x16x32_bf16 v[114:117], v[156:159], v[198:201], v[114:117]
	v_mfma_f32_16x16x32_bf16 v[106:109], v[148:151], v[206:209], v[106:109]
	v_mfma_f32_16x16x32_bf16 v[98:101], v[156:159], v[206:209], v[98:101]
	v_mfma_f32_16x16x32_bf16 v[90:93], v[148:151], v[214:217], v[90:93]
	v_mfma_f32_16x16x32_bf16 v[82:85], v[156:159], v[214:217], v[82:85]
	v_mfma_f32_16x16x32_bf16 v[110:113], v[166:169], v[182:185], v[110:113]
	v_mfma_f32_16x16x32_bf16 v[102:105], v[174:177], v[182:185], v[102:105]
	v_mfma_f32_16x16x32_bf16 v[94:97], v[166:169], v[194:197], v[94:97]
	v_mfma_f32_16x16x32_bf16 v[86:89], v[174:177], v[194:197], v[86:89]
	v_mfma_f32_16x16x32_bf16 v[78:81], v[166:169], v[202:205], v[78:81]
	v_mfma_f32_16x16x32_bf16 v[74:77], v[174:177], v[202:205], v[74:77]
	v_mfma_f32_16x16x32_bf16 v[70:73], v[166:169], v[210:213], v[70:73]
	v_mfma_f32_16x16x32_bf16 v[66:69], v[174:177], v[210:213], v[66:69]
	v_mfma_f32_16x16x32_bf16 v[110:113], v[170:173], v[190:193], v[110:113]
	v_mfma_f32_16x16x32_bf16 v[102:105], v[178:181], v[190:193], v[102:105]
	v_mfma_f32_16x16x32_bf16 v[94:97], v[170:173], v[198:201], v[94:97]
	v_mfma_f32_16x16x32_bf16 v[86:89], v[178:181], v[198:201], v[86:89]
	v_mfma_f32_16x16x32_bf16 v[78:81], v[170:173], v[206:209], v[78:81]
	v_mfma_f32_16x16x32_bf16 v[74:77], v[178:181], v[206:209], v[74:77]
	v_mfma_f32_16x16x32_bf16 v[70:73], v[170:173], v[214:217], v[70:73]
	v_mfma_f32_16x16x32_bf16 v[66:69], v[178:181], v[214:217], v[66:69]
	s_setprio 0
	s_barrier
; #define PG8_STAGE(bufoff, gbase, voff) do { _Pragma("unroll") for (int _i = 0; _i < 2; ++_i) \
;         __builtin_amdgcn_global_load_lds((const unsigned*)((const char*)(gbase) + (voff)[_i]), (PG8_LAS unsigned*)(lds + (bufoff) + ldsw + _i * 8192), 16, 0, 0); } while (0)
; #define PG8_LDA(dst, b, h) do { _Pragma("unroll") for (int m = 0; m < 4; ++m) _Pragma("unroll") for (int k = 0; k < 2; ++k) dst[m][k] = *(const PG8_LAS bf16x8*)(lds + PG8_SA(b, h) + aoff + m * 2048 + k * 1024); } while (0)
; #define PG8_MMA(ai, bj, At, Bt) do { __builtin_amdgcn_s_setprio(1); _Pragma("unroll") for (int m = 0; m < 4; ++m) _Pragma("unroll") for (int n = 0; n < 2; ++n) _Pragma("unroll") for (int k = 0; k < 2; ++k) \
;         acc[ai][bj][m][n] = __builtin_amdgcn_mfma_f32_16x16x32_bf16(Bt[n][k], At[m][k], acc[ai][bj][m][n], 0, 0, 0); __builtin_amdgcn_s_setprio(0); } while (0)
; #define PG8_WAIT_V(n) asm volatile("s_waitcnt vmcnt(" #n ")" ::: "memory")
; #define PG8_WAIT_L(n) asm volatile("s_waitcnt lgkmcnt(" #n ")" ::: "memory")
; #define PG8_BAR __builtin_amdgcn_s_barrier()
; #define PG8_SCHED __builtin_amdgcn_sched_barrier(0)
; template <class Epi, class Sched, bool ALIGN_EPI = false, bool SP2 = false>
; __device__ __forceinline__ void gemm_phase(PG8_LAS unsigned char* lds, const Gemm g, const Sched& S, const Epi& E) {
;     ...
;             PG8_LDA(At, 1, 1); PG8_STAGE(PG8_SB(1, 0), b3, voffB); PG8_STAGE(PG8_SB(1, 1), b3 + hstep, voffB); PG8_STAGE(PG8_SA(1, 0), a3, voffA);
;             PG8_WAIT_V(8); PG8_WAIT_L(0); PG8_BAR; PG8_MMA(1, 0, At, B0); PG8_MMA(1, 1, At, B1); PG8_BAR; PG8_SCHED;
;     ...
;         if constexpr (ALIGN_EPI) { if (wr == 0) PG8_BAR; }
	s_mov_b32 m0, s53
	v_lshl_add_u64 v[160:161], v[160:161], 0, s[18:19]
	ds_read_b128 v[182:185], v143 offset:49152
	ds_read_b128 v[190:193], v143 offset:50176
	ds_read_b128 v[194:197], v143 offset:51200
	ds_read_b128 v[198:201], v143 offset:52224
	ds_read_b128 v[202:205], v143 offset:53248
	ds_read_b128 v[206:209], v143 offset:54272
	ds_read_b128 v[210:213], v143 offset:55296
	ds_read_b128 v[214:217], v143 offset:56320
	global_load_lds_dwordx4 v[160:161], off
	s_mov_b32 m0, s25
	v_lshl_add_u64 v[160:161], v[186:187], 0, s[18:19]
	global_load_lds_dwordx4 v[160:161], off
	s_mov_b32 m0, s27
	v_lshl_add_u64 v[160:161], s[34:35], 0, v[132:133]
	global_load_lds_dwordx4 v[160:161], off
	s_mov_b32 m0, s23
	v_lshl_add_u64 v[160:161], s[34:35], 0, v[130:131]
	global_load_lds_dwordx4 v[160:161], off
	s_mov_b32 m0, s33
	v_lshl_add_u64 v[160:161], v[218:219], 0, s[18:19]
	global_load_lds_dwordx4 v[160:161], off
	s_mov_b32 m0, s48
	v_lshl_add_u64 v[160:161], v[220:221], 0, s[18:19]
	global_load_lds_dwordx4 v[160:161], off
	s_waitcnt vmcnt(8)
	s_waitcnt lgkmcnt(0)
	s_barrier
	s_setprio 1
	s_waitcnt lgkmcnt(0)
	v_mfma_f32_16x16x32_bf16 v[62:65], v[144:147], v[182:185], v[62:65]
	v_mfma_f32_16x16x32_bf16 v[58:61], v[152:155], v[182:185], v[58:61]
	v_mfma_f32_16x16x32_bf16 v[54:57], v[144:147], v[194:197], v[54:57]
	v_mfma_f32_16x16x32_bf16 v[50:53], v[152:155], v[194:197], v[50:53]
	v_mfma_f32_16x16x32_bf16 v[38:41], v[144:147], v[202:205], v[38:41]
	v_mfma_f32_16x16x32_bf16 v[34:37], v[152:155], v[202:205], v[34:37]
	v_mfma_f32_16x16x32_bf16 v[22:25], v[144:147], v[210:213], v[22:25]
	v_mfma_f32_16x16x32_bf16 v[18:21], v[152:155], v[210:213], v[18:21]
	v_mfma_f32_16x16x32_bf16 v[62:65], v[148:151], v[190:193], v[62:65]
	v_mfma_f32_16x16x32_bf16 v[58:61], v[156:159], v[190:193], v[58:61]
	v_mfma_f32_16x16x32_bf16 v[54:57], v[148:151], v[198:201], v[54:57]
	v_mfma_f32_16x16x32_bf16 v[50:53], v[156:159], v[198:201], v[50:53]
	v_mfma_f32_16x16x32_bf16 v[38:41], v[148:151], v[206:209], v[38:41]
	v_mfma_f32_16x16x32_bf16 v[34:37], v[156:159], v[206:209], v[34:37]
	v_mfma_f32_16x16x32_bf16 v[22:25], v[148:151], v[214:217], v[22:25]
	v_mfma_f32_16x16x32_bf16 v[18:21], v[156:159], v[214:217], v[18:21]
	v_mfma_f32_16x16x32_bf16 v[46:49], v[166:169], v[182:185], v[46:49]
	v_mfma_f32_16x16x32_bf16 v[42:45], v[174:177], v[182:185], v[42:45]
	v_mfma_f32_16x16x32_bf16 v[30:33], v[166:169], v[194:197], v[30:33]
	v_mfma_f32_16x16x32_bf16 v[26:29], v[174:177], v[194:197], v[26:29]
	v_mfma_f32_16x16x32_bf16 v[14:17], v[166:169], v[202:205], v[14:17]
	v_mfma_f32_16x16x32_bf16 v[10:13], v[174:177], v[202:205], v[10:13]
	v_mfma_f32_16x16x32_bf16 v[6:9], v[166:169], v[210:213], v[6:9]
	v_mfma_f32_16x16x32_bf16 v[2:5], v[174:177], v[210:213], v[2:5]
	v_mfma_f32_16x16x32_bf16 v[46:49], v[170:173], v[190:193], v[46:49]
	v_mfma_f32_16x16x32_bf16 v[42:45], v[178:181], v[190:193], v[42:45]
	v_mfma_f32_16x16x32_bf16 v[30:33], v[170:173], v[198:201], v[30:33]
	v_mfma_f32_16x16x32_bf16 v[26:29], v[178:181], v[198:201], v[26:29]
	v_mfma_f32_16x16x32_bf16 v[14:17], v[170:173], v[206:209], v[14:17]
	v_mfma_f32_16x16x32_bf16 v[10:13], v[178:181], v[206:209], v[10:13]
	v_mfma_f32_16x16x32_bf16 v[6:9], v[170:173], v[214:217], v[6:9]
	v_mfma_f32_16x16x32_bf16 v[2:5], v[178:181], v[214:217], v[2:5]
	s_setprio 0
	s_barrier
	s_movk_i32 s23, 0x100
	s_andn2_b64 vcc, exec, s[30:31]
	s_mov_b64 s[34:35], -1
	s_mov_b64 s[30:31], 0
	s_cbranch_vccz .LBB0_944
	s_and_b64 vcc, exec, s[20:21]
	s_cbranch_vccz .LBB0_947
	s_barrier

; #define PG8_STAGE(bufoff, gbase, voff) do { _Pragma("unroll") for (int _i = 0; _i < 2; ++_i) \
;         __builtin_amdgcn_global_load_lds((const unsigned*)((const char*)(gbase) + (voff)[_i]), (PG8_LAS unsigned*)(lds + (bufoff) + ldsw + _i * 8192), 16, 0, 0); } while (0)
; #define PG8_LDA(dst, b, h) do { _Pragma("unroll") for (int m = 0; m < 4; ++m) _Pragma("unroll") for (int k = 0; k < 2; ++k) dst[m][k] = *(const PG8_LAS bf16x8*)(lds + PG8_SA(b, h) + aoff + m * 2048 + k * 1024); } while (0)
; #define PG8_LDB(dst, b, h) do { _Pragma("unroll") for (int n = 0; n < 2; ++n) _Pragma("unroll") for (int k = 0; k < 2; ++k) dst[n][k] = *(const PG8_LAS bf16x8*)(lds + PG8_SB(b, h) + boff + n * 2048 + k * 1024); } while (0)
; #define PG8_MMA(ai, bj, At, Bt) do { __builtin_amdgcn_s_setprio(1); _Pragma("unroll") for (int m = 0; m < 4; ++m) _Pragma("unroll") for (int n = 0; n < 2; ++n) _Pragma("unroll") for (int k = 0; k < 2; ++k) \
;         acc[ai][bj][m][n] = __builtin_amdgcn_mfma_f32_16x16x32_bf16(Bt[n][k], At[m][k], acc[ai][bj][m][n], 0, 0, 0); __builtin_amdgcn_s_setprio(0); } while (0)
; #define PG8_WAIT_V(n) asm volatile("s_waitcnt vmcnt(" #n ")" ::: "memory")
; #define PG8_WAIT_L(n) asm volatile("s_waitcnt lgkmcnt(" #n ")" ::: "memory")
; #define PG8_BAR __builtin_amdgcn_s_barrier()
; #define PG8_SCHED __builtin_amdgcn_sched_barrier(0)
; template <class Epi, class Sched, bool ALIGN_EPI = false, bool SP2 = false>
; __device__ __forceinline__ void gemm_phase(PG8_LAS unsigned char* lds, const Gemm g, const Sched& S, const Epi& E) {
;     ...
;         for (int t = 0; t < nt; t += 2) {
;             const bool last = (t == nt - 2);
;             const char* a1 = cA + (size_t)(t + 1) * kstep;
;             const char* a2 = last ? nA : cA + (size_t)(t + 2) * kstep; const char* b2 = last ? nB : cB + (size_t)(t + 2) * kstep;
;             const char* a3 = a2 + kstep; const char* b3 = b2 + kstep;
;             if (last && has_next) S.a_ready(nxt);
;             if constexpr (SP2) {
;             PG8_LDB(B0, 0, 0); PG8_LDB(B1, 0, 1); PG8_SCHED; PG8_LDA(At, 0, 0); PG8_STAGE(PG8_SA(1, 1), a1 + hstep, voffA);
;             PG8_WAIT_V(8); PG8_WAIT_L(0); PG8_BAR; PG8_MMA(0, 0, At, B0); PG8_MMA(0, 1, At, B1); PG8_BAR; PG8_SCHED;
;             PG8_LDA(At, 0, 1); PG8_STAGE(PG8_SB(0, 0), b2, voffB); PG8_STAGE(PG8_SB(0, 1), b2 + hstep, voffB); PG8_STAGE(PG8_SA(0, 0), a2, voffA);
.LBB0_1086:
	ds_read_b128 v[146:149], v153
	ds_read_b128 v[156:159], v153 offset:1024
	ds_read_b128 v[166:169], v153 offset:2048
	ds_read_b128 v[170:173], v153 offset:3072
	ds_read_b128 v[174:177], v154
	ds_read_b128 v[178:181], v154 offset:1024
	ds_read_b128 v[182:185], v154 offset:2048
	ds_read_b128 v[190:193], v154 offset:3072
	s_add_u32 s28, s26, 0xfff80080
	s_addc_u32 s29, s27, -1
	s_cmp_eq_u32 s44, 28
	s_cselect_b32 s31, s19, s29
	s_cselect_b32 s30, s40, s28
	s_cselect_b32 s29, s17, s43
	s_cselect_b32 s28, s41, s42
	v_lshl_add_u64 v[160:161], s[26:27], 0, v[138:139]
	s_add_i32 m0, s4, 0xc000
	ds_read_b128 v[194:197], v155
	ds_read_b128 v[198:201], v155 offset:1024
	ds_read_b128 v[202:205], v155 offset:2048
	ds_read_b128 v[206:209], v155 offset:3072
	ds_read_b128 v[210:213], v155 offset:4096
	ds_read_b128 v[214:217], v155 offset:5120
	ds_read_b128 v[218:221], v155 offset:6144
	ds_read_b128 v[222:225], v155 offset:7168
	global_load_lds_dwordx4 v[160:161], off
	s_add_i32 m0, s4, 0xe000
	v_lshl_add_u64 v[160:161], s[26:27], 0, v[140:141]
	global_load_lds_dwordx4 v[160:161], off
	s_waitcnt vmcnt(8)
	s_waitcnt lgkmcnt(0)
	s_barrier
	s_setprio 1
	s_waitcnt lgkmcnt(0)
	v_mfma_f32_16x16x32_bf16 v[126:129], v[146:149], v[194:197], v[126:129]
	v_mfma_f32_16x16x32_bf16 v[118:121], v[166:169], v[194:197], v[118:121]
	v_mfma_f32_16x16x32_bf16 v[110:113], v[146:149], v[202:205], v[110:113]
	v_mfma_f32_16x16x32_bf16 v[102:105], v[166:169], v[202:205], v[102:105]
	v_mfma_f32_16x16x32_bf16 v[94:97], v[146:149], v[210:213], v[94:97]
	v_mfma_f32_16x16x32_bf16 v[86:89], v[166:169], v[210:213], v[86:89]
	v_mfma_f32_16x16x32_bf16 v[78:81], v[146:149], v[218:221], v[78:81]
	v_mfma_f32_16x16x32_bf16 v[70:73], v[166:169], v[218:221], v[70:73]
	v_mfma_f32_16x16x32_bf16 v[126:129], v[156:159], v[198:201], v[126:129]
	v_mfma_f32_16x16x32_bf16 v[118:121], v[170:173], v[198:201], v[118:121]
	v_mfma_f32_16x16x32_bf16 v[110:113], v[156:159], v[206:209], v[110:113]
	v_mfma_f32_16x16x32_bf16 v[102:105], v[170:173], v[206:209], v[102:105]
	v_mfma_f32_16x16x32_bf16 v[94:97], v[156:159], v[214:217], v[94:97]
	v_mfma_f32_16x16x32_bf16 v[86:89], v[170:173], v[214:217], v[86:89]
	v_mfma_f32_16x16x32_bf16 v[78:81], v[156:159], v[222:225], v[78:81]
	v_mfma_f32_16x16x32_bf16 v[70:73], v[170:173], v[222:225], v[70:73]
	v_mfma_f32_16x16x32_bf16 v[122:125], v[174:177], v[194:197], v[122:125]
	v_mfma_f32_16x16x32_bf16 v[114:117], v[182:185], v[194:197], v[114:117]
	v_mfma_f32_16x16x32_bf16 v[106:109], v[174:177], v[202:205], v[106:109]
	v_mfma_f32_16x16x32_bf16 v[98:101], v[182:185], v[202:205], v[98:101]
	v_mfma_f32_16x16x32_bf16 v[90:93], v[174:177], v[210:213], v[90:93]
	v_mfma_f32_16x16x32_bf16 v[82:85], v[182:185], v[210:213], v[82:85]
	v_mfma_f32_16x16x32_bf16 v[74:77], v[174:177], v[218:221], v[74:77]
	v_mfma_f32_16x16x32_bf16 v[66:69], v[182:185], v[218:221], v[66:69]
	v_mfma_f32_16x16x32_bf16 v[122:125], v[178:181], v[198:201], v[122:125]
	v_mfma_f32_16x16x32_bf16 v[114:117], v[190:193], v[198:201], v[114:117]
	v_mfma_f32_16x16x32_bf16 v[106:109], v[178:181], v[206:209], v[106:109]
	v_mfma_f32_16x16x32_bf16 v[98:101], v[190:193], v[206:209], v[98:101]
	v_mfma_f32_16x16x32_bf16 v[90:93], v[178:181], v[214:217], v[90:93]
	v_mfma_f32_16x16x32_bf16 v[82:85], v[190:193], v[214:217], v[82:85]
	v_mfma_f32_16x16x32_bf16 v[74:77], v[178:181], v[222:225], v[74:77]
	v_mfma_f32_16x16x32_bf16 v[66:69], v[190:193], v[222:225], v[66:69]
	s_setprio 0
	s_barrier
	s_add_i32 s45, s37, s2
	v_lshl_add_u64 v[160:161], s[28:29], 0, v[134:135]
	s_mov_b32 m0, s45
	ds_read_b128 v[194:197], v155 offset:16384
	ds_read_b128 v[198:201], v155 offset:17408
	ds_read_b128 v[202:205], v155 offset:18432
	ds_read_b128 v[206:209], v155 offset:19456
	ds_read_b128 v[210:213], v155 offset:20480
	ds_read_b128 v[214:217], v155 offset:21504
	ds_read_b128 v[218:221], v155 offset:22528
	ds_read_b128 v[222:225], v155 offset:23552
	global_load_lds_dwordx4 v[160:161], off
	s_add_i32 m0, s45, 0x2000
	s_add_u32 s48, s28, 0x80000
	v_lshl_add_u64 v[186:187], s[28:29], 0, v[130:131]
	s_addc_u32 s49, s29, 0
	s_add_i32 s45, s38, s2
	global_load_lds_dwordx4 v[186:187], off
	v_lshl_add_u64 v[226:227], s[48:49], 0, v[134:135]
	s_mov_b32 m0, s45
	v_lshl_add_u64 v[228:229], s[30:31], 0, v[132:133]
	global_load_lds_dwordx4 v[226:227], off
	s_add_i32 m0, s45, 0x2000
	v_lshl_add_u64 v[226:227], s[48:49], 0, v[130:131]
	global_load_lds_dwordx4 v[226:227], off
	s_mov_b32 m0, s4
	v_lshl_add_u64 v[226:227], s[30:31], 0, v[136:137]
	global_load_lds_dwordx4 v[226:227], off
	s_mov_b32 m0, s5
	s_nop 0
	global_load_lds_dwordx4 v[228:229], off
	s_waitcnt vmcnt(8)
	s_waitcnt lgkmcnt(0)
	s_barrier
; #define PG8_STAGE(bufoff, gbase, voff) do { _Pragma("unroll") for (int _i = 0; _i < 2; ++_i) \
;         __builtin_amdgcn_global_load_lds((const unsigned*)((const char*)(gbase) + (voff)[_i]), (PG8_LAS unsigned*)(lds + (bufoff) + ldsw + _i * 8192), 16, 0, 0); } while (0)
; #define PG8_LDA(dst, b, h) do { _Pragma("unroll") for (int m = 0; m < 4; ++m) _Pragma("unroll") for (int k = 0; k < 2; ++k) dst[m][k] = *(const PG8_LAS bf16x8*)(lds + PG8_SA(b, h) + aoff + m * 2048 + k * 1024); } while (0)
; #define PG8_LDB(dst, b, h) do { _Pragma("unroll") for (int n = 0; n < 2; ++n) _Pragma("unroll") for (int k = 0; k < 2; ++k) dst[n][k] = *(const PG8_LAS bf16x8*)(lds + PG8_SB(b, h) + boff + n * 2048 + k * 1024); } while (0)
; #define PG8_MMA(ai, bj, At, Bt) do { __builtin_amdgcn_s_setprio(1); _Pragma("unroll") for (int m = 0; m < 4; ++m) _Pragma("unroll") for (int n = 0; n < 2; ++n) _Pragma("unroll") for (int k = 0; k < 2; ++k) \
;         acc[ai][bj][m][n] = __builtin_amdgcn_mfma_f32_16x16x32_bf16(Bt[n][k], At[m][k], acc[ai][bj][m][n], 0, 0, 0); __builtin_amdgcn_s_setprio(0); } while (0)
; #define PG8_WAIT_V(n) asm volatile("s_waitcnt vmcnt(" #n ")" ::: "memory")
; #define PG8_WAIT_L(n) asm volatile("s_waitcnt lgkmcnt(" #n ")" ::: "memory")
; #define PG8_BAR __builtin_amdgcn_s_barrier()
; #define PG8_SCHED __builtin_amdgcn_sched_barrier(0)
; template <class Epi, class Sched, bool ALIGN_EPI = false, bool SP2 = false>
; __device__ __forceinline__ void gemm_phase(PG8_LAS unsigned char* lds, const Gemm g, const Sched& S, const Epi& E) {
;     ...
;             PG8_WAIT_V(8); PG8_WAIT_L(0); PG8_BAR; PG8_MMA(1, 0, At, B0); PG8_MMA(1, 1, At, B1); PG8_BAR; PG8_SCHED;
;             PG8_LDB(B0, 1, 0); PG8_LDB(B1, 1, 1); PG8_SCHED; PG8_LDA(At, 1, 0); PG8_STAGE(PG8_SA(0, 1), a2 + hstep, voffA);
;             PG8_WAIT_V(8); PG8_WAIT_L(0); PG8_BAR; PG8_MMA(0, 0, At, B0); PG8_MMA(0, 1, At, B1); PG8_BAR; PG8_SCHED;
	s_setprio 1
	s_waitcnt lgkmcnt(0)
	v_mfma_f32_16x16x32_bf16 v[62:65], v[146:149], v[194:197], v[62:65]
	v_mfma_f32_16x16x32_bf16 v[54:57], v[166:169], v[194:197], v[54:57]
	v_mfma_f32_16x16x32_bf16 v[46:49], v[146:149], v[202:205], v[46:49]
	v_mfma_f32_16x16x32_bf16 v[38:41], v[166:169], v[202:205], v[38:41]
	v_mfma_f32_16x16x32_bf16 v[30:33], v[146:149], v[210:213], v[30:33]
	v_mfma_f32_16x16x32_bf16 v[22:25], v[166:169], v[210:213], v[22:25]
	v_mfma_f32_16x16x32_bf16 v[14:17], v[146:149], v[218:221], v[14:17]
	v_mfma_f32_16x16x32_bf16 v[6:9], v[166:169], v[218:221], v[6:9]
	v_mfma_f32_16x16x32_bf16 v[62:65], v[156:159], v[198:201], v[62:65]
	v_mfma_f32_16x16x32_bf16 v[54:57], v[170:173], v[198:201], v[54:57]
	v_mfma_f32_16x16x32_bf16 v[46:49], v[156:159], v[206:209], v[46:49]
	v_mfma_f32_16x16x32_bf16 v[38:41], v[170:173], v[206:209], v[38:41]
	v_mfma_f32_16x16x32_bf16 v[30:33], v[156:159], v[214:217], v[30:33]
	v_mfma_f32_16x16x32_bf16 v[22:25], v[170:173], v[214:217], v[22:25]
	v_mfma_f32_16x16x32_bf16 v[14:17], v[156:159], v[222:225], v[14:17]
	v_mfma_f32_16x16x32_bf16 v[6:9], v[170:173], v[222:225], v[6:9]
	v_mfma_f32_16x16x32_bf16 v[58:61], v[174:177], v[194:197], v[58:61]
	v_mfma_f32_16x16x32_bf16 v[50:53], v[182:185], v[194:197], v[50:53]
	v_mfma_f32_16x16x32_bf16 v[42:45], v[174:177], v[202:205], v[42:45]
	v_mfma_f32_16x16x32_bf16 v[34:37], v[182:185], v[202:205], v[34:37]
	v_mfma_f32_16x16x32_bf16 v[26:29], v[174:177], v[210:213], v[26:29]
	v_mfma_f32_16x16x32_bf16 v[18:21], v[182:185], v[210:213], v[18:21]
	v_mfma_f32_16x16x32_bf16 v[10:13], v[174:177], v[218:221], v[10:13]
	v_mfma_f32_16x16x32_bf16 v[2:5], v[182:185], v[218:221], v[2:5]
	v_mfma_f32_16x16x32_bf16 v[58:61], v[178:181], v[198:201], v[58:61]
	v_mfma_f32_16x16x32_bf16 v[50:53], v[190:193], v[198:201], v[50:53]
	v_mfma_f32_16x16x32_bf16 v[42:45], v[178:181], v[206:209], v[42:45]
	v_mfma_f32_16x16x32_bf16 v[34:37], v[190:193], v[206:209], v[34:37]
	v_mfma_f32_16x16x32_bf16 v[26:29], v[178:181], v[214:217], v[26:29]
	v_mfma_f32_16x16x32_bf16 v[18:21], v[190:193], v[214:217], v[18:21]
	v_mfma_f32_16x16x32_bf16 v[10:13], v[178:181], v[222:225], v[10:13]
	v_mfma_f32_16x16x32_bf16 v[2:5], v[190:193], v[222:225], v[2:5]
	s_setprio 0
	s_barrier
	s_add_i32 s45, 0, 0x18000
	v_add_u32_e32 v162, s45, v151
	s_add_i32 s48, 0, 0x1c000
	ds_read_b128 v[146:149], v162
	ds_read_b128 v[156:159], v162 offset:1024
	ds_read_b128 v[166:169], v162 offset:2048
	ds_read_b128 v[170:173], v162 offset:3072
	v_add_u32_e32 v162, s48, v151
	ds_read_b128 v[174:177], v162
	ds_read_b128 v[178:181], v162 offset:1024
	ds_read_b128 v[182:185], v162 offset:2048
	ds_read_b128 v[190:193], v162 offset:3072
	s_add_u32 s30, s30, 0x80000
	s_addc_u32 s31, s31, 0
	s_mov_b32 m0, s11
	v_lshl_add_u64 v[230:231], s[30:31], 0, v[136:137]
	ds_read_b128 v[194:197], v155 offset:32768
	ds_read_b128 v[198:201], v155 offset:33792
	ds_read_b128 v[202:205], v155 offset:34816
	ds_read_b128 v[206:209], v155 offset:35840
	ds_read_b128 v[210:213], v155 offset:36864
	ds_read_b128 v[214:217], v155 offset:37888
	ds_read_b128 v[218:221], v155 offset:38912
	ds_read_b128 v[222:225], v155 offset:39936
	global_load_lds_dwordx4 v[230:231], off
	s_mov_b32 m0, s33
	v_lshl_add_u64 v[230:231], s[30:31], 0, v[132:133]
	global_load_lds_dwordx4 v[230:231], off
	s_waitcnt vmcnt(8)
	s_waitcnt lgkmcnt(0)
	s_barrier
	s_setprio 1
	s_waitcnt lgkmcnt(0)
	v_mfma_f32_16x16x32_bf16 v[126:129], v[146:149], v[194:197], v[126:129]
	v_mfma_f32_16x16x32_bf16 v[118:121], v[166:169], v[194:197], v[118:121]
	v_mfma_f32_16x16x32_bf16 v[110:113], v[146:149], v[202:205], v[110:113]
	v_mfma_f32_16x16x32_bf16 v[102:105], v[166:169], v[202:205], v[102:105]
	v_mfma_f32_16x16x32_bf16 v[94:97], v[146:149], v[210:213], v[94:97]
	v_mfma_f32_16x16x32_bf16 v[86:89], v[166:169], v[210:213], v[86:89]
	v_mfma_f32_16x16x32_bf16 v[78:81], v[146:149], v[218:221], v[78:81]
	v_mfma_f32_16x16x32_bf16 v[70:73], v[166:169], v[218:221], v[70:73]
	v_mfma_f32_16x16x32_bf16 v[126:129], v[156:159], v[198:201], v[126:129]
	v_mfma_f32_16x16x32_bf16 v[118:121], v[170:173], v[198:201], v[118:121]
	v_mfma_f32_16x16x32_bf16 v[110:113], v[156:159], v[206:209], v[110:113]
	v_mfma_f32_16x16x32_bf16 v[102:105], v[170:173], v[206:209], v[102:105]
	v_mfma_f32_16x16x32_bf16 v[94:97], v[156:159], v[214:217], v[94:97]
	v_mfma_f32_16x16x32_bf16 v[86:89], v[170:173], v[214:217], v[86:89]
	v_mfma_f32_16x16x32_bf16 v[78:81], v[156:159], v[222:225], v[78:81]
	v_mfma_f32_16x16x32_bf16 v[70:73], v[170:173], v[222:225], v[70:73]
	v_mfma_f32_16x16x32_bf16 v[122:125], v[174:177], v[194:197], v[122:125]
	v_mfma_f32_16x16x32_bf16 v[114:117], v[182:185], v[194:197], v[114:117]
	v_mfma_f32_16x16x32_bf16 v[106:109], v[174:177], v[202:205], v[106:109]
	v_mfma_f32_16x16x32_bf16 v[98:101], v[182:185], v[202:205], v[98:101]
	v_mfma_f32_16x16x32_bf16 v[90:93], v[174:177], v[210:213], v[90:93]
	v_mfma_f32_16x16x32_bf16 v[82:85], v[182:185], v[210:213], v[82:85]
	v_mfma_f32_16x16x32_bf16 v[74:77], v[174:177], v[218:221], v[74:77]
	v_mfma_f32_16x16x32_bf16 v[66:69], v[182:185], v[218:221], v[66:69]
	v_mfma_f32_16x16x32_bf16 v[122:125], v[178:181], v[198:201], v[122:125]
	v_mfma_f32_16x16x32_bf16 v[114:117], v[190:193], v[198:201], v[114:117]
	v_mfma_f32_16x16x32_bf16 v[106:109], v[178:181], v[206:209], v[106:109]
	v_mfma_f32_16x16x32_bf16 v[98:101], v[190:193], v[206:209], v[98:101]
	v_mfma_f32_16x16x32_bf16 v[90:93], v[178:181], v[214:217], v[90:93]
	v_mfma_f32_16x16x32_bf16 v[82:85], v[190:193], v[214:217], v[82:85]
	v_mfma_f32_16x16x32_bf16 v[74:77], v[178:181], v[222:225], v[74:77]
	v_mfma_f32_16x16x32_bf16 v[66:69], v[190:193], v[222:225], v[66:69]
	s_setprio 0
	s_barrier
; #define PG8_STAGE(bufoff, gbase, voff) do { _Pragma("unroll") for (int _i = 0; _i < 2; ++_i) \
;         __builtin_amdgcn_global_load_lds((const unsigned*)((const char*)(gbase) + (voff)[_i]), (PG8_LAS unsigned*)(lds + (bufoff) + ldsw + _i * 8192), 16, 0, 0); } while (0)
; #define PG8_LDA(dst, b, h) do { _Pragma("unroll") for (int m = 0; m < 4; ++m) _Pragma("unroll") for (int k = 0; k < 2; ++k) dst[m][k] = *(const PG8_LAS bf16x8*)(lds + PG8_SA(b, h) + aoff + m * 2048 + k * 1024); } while (0)
; #define PG8_MMA(ai, bj, At, Bt) do { __builtin_amdgcn_s_setprio(1); _Pragma("unroll") for (int m = 0; m < 4; ++m) _Pragma("unroll") for (int n = 0; n < 2; ++n) _Pragma("unroll") for (int k = 0; k < 2; ++k) \
;         acc[ai][bj][m][n] = __builtin_amdgcn_mfma_f32_16x16x32_bf16(Bt[n][k], At[m][k], acc[ai][bj][m][n], 0, 0, 0); __builtin_amdgcn_s_setprio(0); } while (0)
; #define PG8_WAIT_V(n) asm volatile("s_waitcnt vmcnt(" #n ")" ::: "memory")
; #define PG8_WAIT_L(n) asm volatile("s_waitcnt lgkmcnt(" #n ")" ::: "memory")
; #define PG8_BAR __builtin_amdgcn_s_barrier()
; #define PG8_SCHED __builtin_amdgcn_sched_barrier(0)
; template <class Epi, class Sched, bool ALIGN_EPI = false, bool SP2 = false>
; __device__ __forceinline__ void gemm_phase(PG8_LAS unsigned char* lds, const Gemm g, const Sched& S, const Epi& E) {
;     ...
;             PG8_LDA(At, 1, 1); PG8_STAGE(PG8_SB(1, 0), b3, voffB); PG8_STAGE(PG8_SB(1, 1), b3 + hstep, voffB); PG8_STAGE(PG8_SA(1, 0), a3, voffA);
;             PG8_WAIT_V(8); PG8_WAIT_L(0); PG8_BAR; PG8_MMA(1, 0, At, B0); PG8_MMA(1, 1, At, B1); PG8_BAR; PG8_SCHED;
;     ...
;         if constexpr (ALIGN_EPI) { if (wr == 0) PG8_BAR; }
	s_add_i32 s30, s45, s2
	v_lshl_add_u64 v[160:161], v[160:161], 0, s[12:13]
	s_mov_b32 m0, s30
	ds_read_b128 v[194:197], v155 offset:49152
	ds_read_b128 v[198:201], v155 offset:50176
	ds_read_b128 v[202:205], v155 offset:51200
	ds_read_b128 v[206:209], v155 offset:52224
	ds_read_b128 v[210:213], v155 offset:53248
	ds_read_b128 v[214:217], v155 offset:54272
	ds_read_b128 v[218:221], v155 offset:55296
	ds_read_b128 v[222:225], v155 offset:56320
	global_load_lds_dwordx4 v[160:161], off
	s_add_i32 m0, s30, 0x2000
	s_add_u32 s28, s28, 0x80080
	v_lshl_add_u64 v[160:161], v[186:187], 0, s[12:13]
	s_addc_u32 s29, s29, 0
	s_add_i32 s30, s48, s2
	global_load_lds_dwordx4 v[160:161], off
	s_mov_b32 m0, s30
	v_lshl_add_u64 v[160:161], s[28:29], 0, v[134:135]
	global_load_lds_dwordx4 v[160:161], off
	s_add_i32 m0, s30, 0x2000
	v_lshl_add_u64 v[160:161], s[28:29], 0, v[130:131]
	global_load_lds_dwordx4 v[160:161], off
	s_mov_b32 m0, s35
	v_lshl_add_u64 v[160:161], v[226:227], 0, s[12:13]
	global_load_lds_dwordx4 v[160:161], off
	s_mov_b32 m0, s36
	v_lshl_add_u64 v[160:161], v[228:229], 0, s[12:13]
	global_load_lds_dwordx4 v[160:161], off
	s_waitcnt vmcnt(8)
	s_waitcnt lgkmcnt(0)
	s_barrier
	s_setprio 1
	s_waitcnt lgkmcnt(0)
	v_mfma_f32_16x16x32_bf16 v[62:65], v[146:149], v[194:197], v[62:65]
	v_mfma_f32_16x16x32_bf16 v[54:57], v[166:169], v[194:197], v[54:57]
	v_mfma_f32_16x16x32_bf16 v[46:49], v[146:149], v[202:205], v[46:49]
	v_mfma_f32_16x16x32_bf16 v[38:41], v[166:169], v[202:205], v[38:41]
	v_mfma_f32_16x16x32_bf16 v[30:33], v[146:149], v[210:213], v[30:33]
	v_mfma_f32_16x16x32_bf16 v[22:25], v[166:169], v[210:213], v[22:25]
	v_mfma_f32_16x16x32_bf16 v[14:17], v[146:149], v[218:221], v[14:17]
	v_mfma_f32_16x16x32_bf16 v[6:9], v[166:169], v[218:221], v[6:9]
	v_mfma_f32_16x16x32_bf16 v[62:65], v[156:159], v[198:201], v[62:65]
	v_mfma_f32_16x16x32_bf16 v[54:57], v[170:173], v[198:201], v[54:57]
	v_mfma_f32_16x16x32_bf16 v[46:49], v[156:159], v[206:209], v[46:49]
	v_mfma_f32_16x16x32_bf16 v[38:41], v[170:173], v[206:209], v[38:41]
	v_mfma_f32_16x16x32_bf16 v[30:33], v[156:159], v[214:217], v[30:33]
	v_mfma_f32_16x16x32_bf16 v[22:25], v[170:173], v[214:217], v[22:25]
	v_mfma_f32_16x16x32_bf16 v[14:17], v[156:159], v[222:225], v[14:17]
	v_mfma_f32_16x16x32_bf16 v[6:9], v[170:173], v[222:225], v[6:9]
	v_mfma_f32_16x16x32_bf16 v[58:61], v[174:177], v[194:197], v[58:61]
	v_mfma_f32_16x16x32_bf16 v[50:53], v[182:185], v[194:197], v[50:53]
	v_mfma_f32_16x16x32_bf16 v[42:45], v[174:177], v[202:205], v[42:45]
	v_mfma_f32_16x16x32_bf16 v[34:37], v[182:185], v[202:205], v[34:37]
	v_mfma_f32_16x16x32_bf16 v[26:29], v[174:177], v[210:213], v[26:29]
	v_mfma_f32_16x16x32_bf16 v[18:21], v[182:185], v[210:213], v[18:21]
	v_mfma_f32_16x16x32_bf16 v[10:13], v[174:177], v[218:221], v[10:13]
	v_mfma_f32_16x16x32_bf16 v[2:5], v[182:185], v[218:221], v[2:5]
	v_mfma_f32_16x16x32_bf16 v[58:61], v[178:181], v[198:201], v[58:61]
	v_mfma_f32_16x16x32_bf16 v[50:53], v[190:193], v[198:201], v[50:53]
	v_mfma_f32_16x16x32_bf16 v[42:45], v[178:181], v[206:209], v[42:45]
	v_mfma_f32_16x16x32_bf16 v[34:37], v[190:193], v[206:209], v[34:37]
	v_mfma_f32_16x16x32_bf16 v[26:29], v[178:181], v[214:217], v[26:29]
	v_mfma_f32_16x16x32_bf16 v[18:21], v[190:193], v[214:217], v[18:21]
	v_mfma_f32_16x16x32_bf16 v[10:13], v[178:181], v[222:225], v[10:13]
	v_mfma_f32_16x16x32_bf16 v[2:5], v[190:193], v[222:225], v[2:5]
	s_setprio 0
	s_barrier
	s_add_i32 s44, s44, 2
	s_add_u32 s26, s26, 0x100
	s_addc_u32 s27, s27, 0
	s_add_u32 s42, s42, 0x100
	s_addc_u32 s43, s43, 0
	s_cmp_gt_u32 s44, 29
	s_cbranch_scc0 .LBB0_1086
	s_and_b64 vcc, exec, s[14:15]
	s_cbranch_vccz .LBB0_1089
	s_barrier

; #define PG8_STAGE(bufoff, gbase, voff) do { _Pragma("unroll") for (int _i = 0; _i < 2; ++_i) \
;         __builtin_amdgcn_global_load_lds((const unsigned*)((const char*)(gbase) + (voff)[_i]), (PG8_LAS unsigned*)(lds + (bufoff) + ldsw + _i * 8192), 16, 0, 0); } while (0)
; #define PG8_LDA(dst, b, h) do { _Pragma("unroll") for (int m = 0; m < 4; ++m) _Pragma("unroll") for (int k = 0; k < 2; ++k) dst[m][k] = *(const PG8_LAS bf16x8*)(lds + PG8_SA(b, h) + aoff + m * 2048 + k * 1024); } while (0)
; #define PG8_LDB(dst, b, h) do { _Pragma("unroll") for (int n = 0; n < 2; ++n) _Pragma("unroll") for (int k = 0; k < 2; ++k) dst[n][k] = *(const PG8_LAS bf16x8*)(lds + PG8_SB(b, h) + boff + n * 2048 + k * 1024); } while (0)
; #define PG8_MMA(ai, bj, At, Bt) do { __builtin_amdgcn_s_setprio(1); _Pragma("unroll") for (int m = 0; m < 4; ++m) _Pragma("unroll") for (int n = 0; n < 2; ++n) _Pragma("unroll") for (int k = 0; k < 2; ++k) \
;         acc[ai][bj][m][n] = __builtin_amdgcn_mfma_f32_16x16x32_bf16(Bt[n][k], At[m][k], acc[ai][bj][m][n], 0, 0, 0); __builtin_amdgcn_s_setprio(0); } while (0)
; #define PG8_WAIT_V(n) asm volatile("s_waitcnt vmcnt(" #n ")" ::: "memory")
; #define PG8_WAIT_L(n) asm volatile("s_waitcnt lgkmcnt(" #n ")" ::: "memory")
; #define PG8_BAR __builtin_amdgcn_s_barrier()
; #define PG8_SCHED __builtin_amdgcn_sched_barrier(0)
; template <class Epi, class Sched, bool ALIGN_EPI = false, bool SP2 = false>
; __device__ __forceinline__ void gemm_phase(PG8_LAS unsigned char* lds, const Gemm g, const Sched& S, const Epi& E) {
;     ...
;         for (int t = 0; t < nt; t += 2) {
;             const bool last = (t == nt - 2);
;             const char* a1 = cA + (size_t)(t + 1) * kstep;
;             const char* a2 = last ? nA : cA + (size_t)(t + 2) * kstep; const char* b2 = last ? nB : cB + (size_t)(t + 2) * kstep;
;             const char* a3 = a2 + kstep; const char* b3 = b2 + kstep;
;             if (last && has_next) S.a_ready(nxt);
;             if constexpr (SP2) {
;             PG8_LDB(B0, 0, 0); PG8_LDB(B1, 0, 1); PG8_SCHED; PG8_LDA(At, 0, 0); PG8_STAGE(PG8_SA(1, 1), a1 + hstep, voffA);
;             PG8_WAIT_V(8); PG8_WAIT_L(0); PG8_BAR; PG8_MMA(0, 0, At, B0); PG8_MMA(0, 1, At, B1); PG8_BAR; PG8_SCHED;
;             PG8_LDA(At, 0, 1); PG8_STAGE(PG8_SB(0, 0), b2, voffB); PG8_STAGE(PG8_SB(0, 1), b2 + hstep, voffB); PG8_STAGE(PG8_SA(0, 0), a2, voffA);
.LBB0_1165:
	ds_read_b128 v[144:147], v155
	ds_read_b128 v[148:151], v155 offset:1024
	ds_read_b128 v[166:169], v155 offset:2048
	ds_read_b128 v[170:173], v155 offset:3072
	ds_read_b128 v[174:177], v156
	ds_read_b128 v[178:181], v156 offset:1024
	ds_read_b128 v[182:185], v156 offset:2048
	ds_read_b128 v[190:193], v156 offset:3072
	s_add_u32 s6, s26, 0x100
	s_addc_u32 s7, s27, 0
	s_cmpk_eq_i32 s48, 0x54
	s_cselect_b32 s31, s23, s7
	s_cselect_b32 s30, s22, s6
	s_cselect_b32 s29, s25, s45
	s_cselect_b32 s28, s24, s44
	v_lshl_add_u64 v[160:161], s[26:27], 0, v[136:137]
	s_add_i32 m0, s3, 0xc000
	ds_read_b128 v[194:197], v157
	ds_read_b128 v[198:201], v157 offset:1024
	ds_read_b128 v[202:205], v157 offset:2048
	ds_read_b128 v[206:209], v157 offset:3072
	ds_read_b128 v[210:213], v157 offset:4096
	ds_read_b128 v[214:217], v157 offset:5120
	ds_read_b128 v[218:221], v157 offset:6144
	ds_read_b128 v[222:225], v157 offset:7168
	global_load_lds_dwordx4 v[160:161], off
	s_add_i32 m0, s3, 0xe000
	v_lshl_add_u64 v[160:161], s[26:27], 0, v[138:139]
	global_load_lds_dwordx4 v[160:161], off
	s_waitcnt vmcnt(8)
	s_waitcnt lgkmcnt(0)
	s_barrier
	s_setprio 1
	s_waitcnt lgkmcnt(0)
	v_mfma_f32_16x16x32_bf16 v[126:129], v[144:147], v[194:197], v[126:129]
	v_mfma_f32_16x16x32_bf16 v[122:125], v[166:169], v[194:197], v[122:125]
	v_mfma_f32_16x16x32_bf16 v[110:113], v[144:147], v[202:205], v[110:113]
	v_mfma_f32_16x16x32_bf16 v[106:109], v[166:169], v[202:205], v[106:109]
	v_mfma_f32_16x16x32_bf16 v[94:97], v[144:147], v[210:213], v[94:97]
	v_mfma_f32_16x16x32_bf16 v[90:93], v[166:169], v[210:213], v[90:93]
	v_mfma_f32_16x16x32_bf16 v[78:81], v[144:147], v[218:221], v[78:81]
	v_mfma_f32_16x16x32_bf16 v[74:77], v[166:169], v[218:221], v[74:77]
	v_mfma_f32_16x16x32_bf16 v[126:129], v[148:151], v[198:201], v[126:129]
	v_mfma_f32_16x16x32_bf16 v[122:125], v[170:173], v[198:201], v[122:125]
	v_mfma_f32_16x16x32_bf16 v[110:113], v[148:151], v[206:209], v[110:113]
	v_mfma_f32_16x16x32_bf16 v[106:109], v[170:173], v[206:209], v[106:109]
	v_mfma_f32_16x16x32_bf16 v[94:97], v[148:151], v[214:217], v[94:97]
	v_mfma_f32_16x16x32_bf16 v[90:93], v[170:173], v[214:217], v[90:93]
	v_mfma_f32_16x16x32_bf16 v[78:81], v[148:151], v[222:225], v[78:81]
	v_mfma_f32_16x16x32_bf16 v[74:77], v[170:173], v[222:225], v[74:77]
	v_mfma_f32_16x16x32_bf16 v[118:121], v[174:177], v[194:197], v[118:121]
	v_mfma_f32_16x16x32_bf16 v[114:117], v[182:185], v[194:197], v[114:117]
	v_mfma_f32_16x16x32_bf16 v[102:105], v[174:177], v[202:205], v[102:105]
	v_mfma_f32_16x16x32_bf16 v[98:101], v[182:185], v[202:205], v[98:101]
	v_mfma_f32_16x16x32_bf16 v[86:89], v[174:177], v[210:213], v[86:89]
	v_mfma_f32_16x16x32_bf16 v[82:85], v[182:185], v[210:213], v[82:85]
	v_mfma_f32_16x16x32_bf16 v[70:73], v[174:177], v[218:221], v[70:73]
	v_mfma_f32_16x16x32_bf16 v[66:69], v[182:185], v[218:221], v[66:69]
	v_mfma_f32_16x16x32_bf16 v[118:121], v[178:181], v[198:201], v[118:121]
	v_mfma_f32_16x16x32_bf16 v[114:117], v[190:193], v[198:201], v[114:117]
	v_mfma_f32_16x16x32_bf16 v[102:105], v[178:181], v[206:209], v[102:105]
	v_mfma_f32_16x16x32_bf16 v[98:101], v[190:193], v[206:209], v[98:101]
	v_mfma_f32_16x16x32_bf16 v[86:89], v[178:181], v[214:217], v[86:89]
	v_mfma_f32_16x16x32_bf16 v[82:85], v[190:193], v[214:217], v[82:85]
	v_mfma_f32_16x16x32_bf16 v[70:73], v[178:181], v[222:225], v[70:73]
	v_mfma_f32_16x16x32_bf16 v[66:69], v[190:193], v[222:225], v[66:69]
	s_setprio 0
	s_barrier
	s_add_i32 s26, s37, s2
	v_lshl_add_u64 v[160:161], s[28:29], 0, v[130:131]
	s_mov_b32 m0, s26
	ds_read_b128 v[194:197], v157 offset:16384
	ds_read_b128 v[198:201], v157 offset:17408
	ds_read_b128 v[202:205], v157 offset:18432
	ds_read_b128 v[206:209], v157 offset:19456
	ds_read_b128 v[210:213], v157 offset:20480
	ds_read_b128 v[214:217], v157 offset:21504
	ds_read_b128 v[218:221], v157 offset:22528
	ds_read_b128 v[222:225], v157 offset:23552
	global_load_lds_dwordx4 v[160:161], off
	s_add_i32 m0, s26, 0x2000
	s_add_u32 s26, s28, 0x160000
	v_lshl_add_u64 v[186:187], s[28:29], 0, v[132:133]
	s_addc_u32 s27, s29, 0
	s_add_i32 s49, s38, s2
	global_load_lds_dwordx4 v[186:187], off
	v_lshl_add_u64 v[226:227], s[26:27], 0, v[130:131]
	s_mov_b32 m0, s49
	v_lshl_add_u64 v[228:229], s[30:31], 0, v[132:133]
	global_load_lds_dwordx4 v[226:227], off
	s_add_i32 m0, s49, 0x2000
	v_lshl_add_u64 v[226:227], s[26:27], 0, v[132:133]
	global_load_lds_dwordx4 v[226:227], off
	s_mov_b32 m0, s3
	v_lshl_add_u64 v[226:227], s[30:31], 0, v[130:131]
	global_load_lds_dwordx4 v[226:227], off
	s_mov_b32 m0, s4
	s_nop 0
	global_load_lds_dwordx4 v[228:229], off
	s_waitcnt vmcnt(8)
	s_waitcnt lgkmcnt(0)
	s_barrier
; #define PG8_STAGE(bufoff, gbase, voff) do { _Pragma("unroll") for (int _i = 0; _i < 2; ++_i) \
;         __builtin_amdgcn_global_load_lds((const unsigned*)((const char*)(gbase) + (voff)[_i]), (PG8_LAS unsigned*)(lds + (bufoff) + ldsw + _i * 8192), 16, 0, 0); } while (0)
; #define PG8_LDA(dst, b, h) do { _Pragma("unroll") for (int m = 0; m < 4; ++m) _Pragma("unroll") for (int k = 0; k < 2; ++k) dst[m][k] = *(const PG8_LAS bf16x8*)(lds + PG8_SA(b, h) + aoff + m * 2048 + k * 1024); } while (0)
; #define PG8_LDB(dst, b, h) do { _Pragma("unroll") for (int n = 0; n < 2; ++n) _Pragma("unroll") for (int k = 0; k < 2; ++k) dst[n][k] = *(const PG8_LAS bf16x8*)(lds + PG8_SB(b, h) + boff + n * 2048 + k * 1024); } while (0)
; #define PG8_MMA(ai, bj, At, Bt) do { __builtin_amdgcn_s_setprio(1); _Pragma("unroll") for (int m = 0; m < 4; ++m) _Pragma("unroll") for (int n = 0; n < 2; ++n) _Pragma("unroll") for (int k = 0; k < 2; ++k) \
;         acc[ai][bj][m][n] = __builtin_amdgcn_mfma_f32_16x16x32_bf16(Bt[n][k], At[m][k], acc[ai][bj][m][n], 0, 0, 0); __builtin_amdgcn_s_setprio(0); } while (0)
; #define PG8_WAIT_V(n) asm volatile("s_waitcnt vmcnt(" #n ")" ::: "memory")
; #define PG8_WAIT_L(n) asm volatile("s_waitcnt lgkmcnt(" #n ")" ::: "memory")
; #define PG8_BAR __builtin_amdgcn_s_barrier()
; #define PG8_SCHED __builtin_amdgcn_sched_barrier(0)
; template <class Epi, class Sched, bool ALIGN_EPI = false, bool SP2 = false>
; __device__ __forceinline__ void gemm_phase(PG8_LAS unsigned char* lds, const Gemm g, const Sched& S, const Epi& E) {
;     ...
;             PG8_WAIT_V(8); PG8_WAIT_L(0); PG8_BAR; PG8_MMA(1, 0, At, B0); PG8_MMA(1, 1, At, B1); PG8_BAR; PG8_SCHED;
;             PG8_LDB(B0, 1, 0); PG8_LDB(B1, 1, 1); PG8_SCHED; PG8_LDA(At, 1, 0); PG8_STAGE(PG8_SA(0, 1), a2 + hstep, voffA);
;             PG8_WAIT_V(8); PG8_WAIT_L(0); PG8_BAR; PG8_MMA(0, 0, At, B0); PG8_MMA(0, 1, At, B1); PG8_BAR; PG8_SCHED;
	s_setprio 1
	s_waitcnt lgkmcnt(0)
	v_mfma_f32_16x16x32_bf16 v[62:65], v[144:147], v[194:197], v[62:65]
	v_mfma_f32_16x16x32_bf16 v[58:61], v[166:169], v[194:197], v[58:61]
	v_mfma_f32_16x16x32_bf16 v[46:49], v[144:147], v[202:205], v[46:49]
	v_mfma_f32_16x16x32_bf16 v[42:45], v[166:169], v[202:205], v[42:45]
	v_mfma_f32_16x16x32_bf16 v[30:33], v[144:147], v[210:213], v[30:33]
	v_mfma_f32_16x16x32_bf16 v[26:29], v[166:169], v[210:213], v[26:29]
	v_mfma_f32_16x16x32_bf16 v[14:17], v[144:147], v[218:221], v[14:17]
	v_mfma_f32_16x16x32_bf16 v[10:13], v[166:169], v[218:221], v[10:13]
	v_mfma_f32_16x16x32_bf16 v[62:65], v[148:151], v[198:201], v[62:65]
	v_mfma_f32_16x16x32_bf16 v[58:61], v[170:173], v[198:201], v[58:61]
	v_mfma_f32_16x16x32_bf16 v[46:49], v[148:151], v[206:209], v[46:49]
	v_mfma_f32_16x16x32_bf16 v[42:45], v[170:173], v[206:209], v[42:45]
	v_mfma_f32_16x16x32_bf16 v[30:33], v[148:151], v[214:217], v[30:33]
	v_mfma_f32_16x16x32_bf16 v[26:29], v[170:173], v[214:217], v[26:29]
	v_mfma_f32_16x16x32_bf16 v[14:17], v[148:151], v[222:225], v[14:17]
	v_mfma_f32_16x16x32_bf16 v[10:13], v[170:173], v[222:225], v[10:13]
	v_mfma_f32_16x16x32_bf16 v[54:57], v[174:177], v[194:197], v[54:57]
	v_mfma_f32_16x16x32_bf16 v[50:53], v[182:185], v[194:197], v[50:53]
	v_mfma_f32_16x16x32_bf16 v[38:41], v[174:177], v[202:205], v[38:41]
	v_mfma_f32_16x16x32_bf16 v[34:37], v[182:185], v[202:205], v[34:37]
	v_mfma_f32_16x16x32_bf16 v[22:25], v[174:177], v[210:213], v[22:25]
	v_mfma_f32_16x16x32_bf16 v[18:21], v[182:185], v[210:213], v[18:21]
	v_mfma_f32_16x16x32_bf16 v[6:9], v[174:177], v[218:221], v[6:9]
	v_mfma_f32_16x16x32_bf16 v[2:5], v[182:185], v[218:221], v[2:5]
	v_mfma_f32_16x16x32_bf16 v[54:57], v[178:181], v[198:201], v[54:57]
	v_mfma_f32_16x16x32_bf16 v[50:53], v[190:193], v[198:201], v[50:53]
	v_mfma_f32_16x16x32_bf16 v[38:41], v[178:181], v[206:209], v[38:41]
	v_mfma_f32_16x16x32_bf16 v[34:37], v[190:193], v[206:209], v[34:37]
	v_mfma_f32_16x16x32_bf16 v[22:25], v[178:181], v[214:217], v[22:25]
	v_mfma_f32_16x16x32_bf16 v[18:21], v[190:193], v[214:217], v[18:21]
	v_mfma_f32_16x16x32_bf16 v[6:9], v[178:181], v[222:225], v[6:9]
	v_mfma_f32_16x16x32_bf16 v[2:5], v[190:193], v[222:225], v[2:5]
	s_setprio 0
	s_barrier
	s_add_i32 s49, 0, 0x18000
	v_add_u32_e32 v134, s49, v153
	s_add_i32 s50, 0, 0x1c000
	ds_read_b128 v[144:147], v134
	ds_read_b128 v[148:151], v134 offset:1024
	ds_read_b128 v[166:169], v134 offset:2048
	ds_read_b128 v[170:173], v134 offset:3072
	v_add_u32_e32 v134, s50, v153
	ds_read_b128 v[174:177], v134
	ds_read_b128 v[178:181], v134 offset:1024
	ds_read_b128 v[182:185], v134 offset:2048
	ds_read_b128 v[190:193], v134 offset:3072
	s_add_u32 s26, s30, 0x160000
	s_addc_u32 s27, s31, 0
	s_mov_b32 m0, s5
	v_lshl_add_u64 v[230:231], s[26:27], 0, v[130:131]
	ds_read_b128 v[194:197], v157 offset:32768
	ds_read_b128 v[198:201], v157 offset:33792
	ds_read_b128 v[202:205], v157 offset:34816
	ds_read_b128 v[206:209], v157 offset:35840
	ds_read_b128 v[210:213], v157 offset:36864
	ds_read_b128 v[214:217], v157 offset:37888
	ds_read_b128 v[218:221], v157 offset:38912
	ds_read_b128 v[222:225], v157 offset:39936
	global_load_lds_dwordx4 v[230:231], off
	s_mov_b32 m0, s11
	v_lshl_add_u64 v[230:231], s[26:27], 0, v[132:133]
	global_load_lds_dwordx4 v[230:231], off
	s_waitcnt vmcnt(8)
	s_waitcnt lgkmcnt(0)
	s_barrier
	s_setprio 1
	s_waitcnt lgkmcnt(0)
	v_mfma_f32_16x16x32_bf16 v[126:129], v[144:147], v[194:197], v[126:129]
	v_mfma_f32_16x16x32_bf16 v[122:125], v[166:169], v[194:197], v[122:125]
	v_mfma_f32_16x16x32_bf16 v[110:113], v[144:147], v[202:205], v[110:113]
	v_mfma_f32_16x16x32_bf16 v[106:109], v[166:169], v[202:205], v[106:109]
	v_mfma_f32_16x16x32_bf16 v[94:97], v[144:147], v[210:213], v[94:97]
	v_mfma_f32_16x16x32_bf16 v[90:93], v[166:169], v[210:213], v[90:93]
	v_mfma_f32_16x16x32_bf16 v[78:81], v[144:147], v[218:221], v[78:81]
	v_mfma_f32_16x16x32_bf16 v[74:77], v[166:169], v[218:221], v[74:77]
	v_mfma_f32_16x16x32_bf16 v[126:129], v[148:151], v[198:201], v[126:129]
	v_mfma_f32_16x16x32_bf16 v[122:125], v[170:173], v[198:201], v[122:125]
	v_mfma_f32_16x16x32_bf16 v[110:113], v[148:151], v[206:209], v[110:113]
	v_mfma_f32_16x16x32_bf16 v[106:109], v[170:173], v[206:209], v[106:109]
	v_mfma_f32_16x16x32_bf16 v[94:97], v[148:151], v[214:217], v[94:97]
	v_mfma_f32_16x16x32_bf16 v[90:93], v[170:173], v[214:217], v[90:93]
	v_mfma_f32_16x16x32_bf16 v[78:81], v[148:151], v[222:225], v[78:81]
	v_mfma_f32_16x16x32_bf16 v[74:77], v[170:173], v[222:225], v[74:77]
	v_mfma_f32_16x16x32_bf16 v[118:121], v[174:177], v[194:197], v[118:121]
	v_mfma_f32_16x16x32_bf16 v[114:117], v[182:185], v[194:197], v[114:117]
	v_mfma_f32_16x16x32_bf16 v[102:105], v[174:177], v[202:205], v[102:105]
	v_mfma_f32_16x16x32_bf16 v[98:101], v[182:185], v[202:205], v[98:101]
	v_mfma_f32_16x16x32_bf16 v[86:89], v[174:177], v[210:213], v[86:89]
	v_mfma_f32_16x16x32_bf16 v[82:85], v[182:185], v[210:213], v[82:85]
	v_mfma_f32_16x16x32_bf16 v[70:73], v[174:177], v[218:221], v[70:73]
	v_mfma_f32_16x16x32_bf16 v[66:69], v[182:185], v[218:221], v[66:69]
	v_mfma_f32_16x16x32_bf16 v[118:121], v[178:181], v[198:201], v[118:121]
	v_mfma_f32_16x16x32_bf16 v[114:117], v[190:193], v[198:201], v[114:117]
	v_mfma_f32_16x16x32_bf16 v[102:105], v[178:181], v[206:209], v[102:105]
	v_mfma_f32_16x16x32_bf16 v[98:101], v[190:193], v[206:209], v[98:101]
	v_mfma_f32_16x16x32_bf16 v[86:89], v[178:181], v[214:217], v[86:89]
	v_mfma_f32_16x16x32_bf16 v[82:85], v[190:193], v[214:217], v[82:85]
	v_mfma_f32_16x16x32_bf16 v[70:73], v[178:181], v[222:225], v[70:73]
	v_mfma_f32_16x16x32_bf16 v[66:69], v[190:193], v[222:225], v[66:69]
	s_setprio 0
	s_barrier
; #define PG8_STAGE(bufoff, gbase, voff) do { _Pragma("unroll") for (int _i = 0; _i < 2; ++_i) \
;         __builtin_amdgcn_global_load_lds((const unsigned*)((const char*)(gbase) + (voff)[_i]), (PG8_LAS unsigned*)(lds + (bufoff) + ldsw + _i * 8192), 16, 0, 0); } while (0)
; #define PG8_LDA(dst, b, h) do { _Pragma("unroll") for (int m = 0; m < 4; ++m) _Pragma("unroll") for (int k = 0; k < 2; ++k) dst[m][k] = *(const PG8_LAS bf16x8*)(lds + PG8_SA(b, h) + aoff + m * 2048 + k * 1024); } while (0)
; #define PG8_MMA(ai, bj, At, Bt) do { __builtin_amdgcn_s_setprio(1); _Pragma("unroll") for (int m = 0; m < 4; ++m) _Pragma("unroll") for (int n = 0; n < 2; ++n) _Pragma("unroll") for (int k = 0; k < 2; ++k) \
;         acc[ai][bj][m][n] = __builtin_amdgcn_mfma_f32_16x16x32_bf16(Bt[n][k], At[m][k], acc[ai][bj][m][n], 0, 0, 0); __builtin_amdgcn_s_setprio(0); } while (0)
; #define PG8_WAIT_V(n) asm volatile("s_waitcnt vmcnt(" #n ")" ::: "memory")
; #define PG8_WAIT_L(n) asm volatile("s_waitcnt lgkmcnt(" #n ")" ::: "memory")
; #define PG8_BAR __builtin_amdgcn_s_barrier()
; #define PG8_SCHED __builtin_amdgcn_sched_barrier(0)
; template <class Epi, class Sched, bool ALIGN_EPI = false, bool SP2 = false>
; __device__ __forceinline__ void gemm_phase(PG8_LAS unsigned char* lds, const Gemm g, const Sched& S, const Epi& E) {
;     ...
;             PG8_LDA(At, 1, 1); PG8_STAGE(PG8_SB(1, 0), b3, voffB); PG8_STAGE(PG8_SB(1, 1), b3 + hstep, voffB); PG8_STAGE(PG8_SA(1, 0), a3, voffA);
;             PG8_WAIT_V(8); PG8_WAIT_L(0); PG8_BAR; PG8_MMA(1, 0, At, B0); PG8_MMA(1, 1, At, B1); PG8_BAR; PG8_SCHED;
;     ...
;         if constexpr (ALIGN_EPI) { if (wr == 0) PG8_BAR; }
	s_add_i32 s26, s49, s2
	v_lshl_add_u64 v[160:161], v[160:161], 0, s[18:19]
	s_mov_b32 m0, s26
	ds_read_b128 v[194:197], v157 offset:49152
	ds_read_b128 v[198:201], v157 offset:50176
	ds_read_b128 v[202:205], v157 offset:51200
	ds_read_b128 v[206:209], v157 offset:52224
	ds_read_b128 v[210:213], v157 offset:53248
	ds_read_b128 v[214:217], v157 offset:54272
	ds_read_b128 v[218:221], v157 offset:55296
	ds_read_b128 v[222:225], v157 offset:56320
	global_load_lds_dwordx4 v[160:161], off
	s_add_i32 m0, s26, 0x2000
	s_add_u32 s26, s28, 0x160080
	v_lshl_add_u64 v[160:161], v[186:187], 0, s[18:19]
	s_addc_u32 s27, s29, 0
	s_add_i32 s28, s50, s2
	global_load_lds_dwordx4 v[160:161], off
	s_mov_b32 m0, s28
	v_lshl_add_u64 v[160:161], s[26:27], 0, v[130:131]
	global_load_lds_dwordx4 v[160:161], off
	s_add_i32 m0, s28, 0x2000
	v_lshl_add_u64 v[160:161], s[26:27], 0, v[132:133]
	global_load_lds_dwordx4 v[160:161], off
	s_mov_b32 m0, s35
	v_lshl_add_u64 v[160:161], v[226:227], 0, s[18:19]
	global_load_lds_dwordx4 v[160:161], off
	s_mov_b32 m0, s36
	v_lshl_add_u64 v[160:161], v[228:229], 0, s[18:19]
	global_load_lds_dwordx4 v[160:161], off
	s_waitcnt vmcnt(8)
	s_waitcnt lgkmcnt(0)
	s_barrier
	s_setprio 1
	s_waitcnt lgkmcnt(0)
	v_mfma_f32_16x16x32_bf16 v[62:65], v[144:147], v[194:197], v[62:65]
	v_mfma_f32_16x16x32_bf16 v[58:61], v[166:169], v[194:197], v[58:61]
	v_mfma_f32_16x16x32_bf16 v[46:49], v[144:147], v[202:205], v[46:49]
	v_mfma_f32_16x16x32_bf16 v[42:45], v[166:169], v[202:205], v[42:45]
	v_mfma_f32_16x16x32_bf16 v[30:33], v[144:147], v[210:213], v[30:33]
	v_mfma_f32_16x16x32_bf16 v[26:29], v[166:169], v[210:213], v[26:29]
	v_mfma_f32_16x16x32_bf16 v[14:17], v[144:147], v[218:221], v[14:17]
	v_mfma_f32_16x16x32_bf16 v[10:13], v[166:169], v[218:221], v[10:13]
	v_mfma_f32_16x16x32_bf16 v[62:65], v[148:151], v[198:201], v[62:65]
	v_mfma_f32_16x16x32_bf16 v[58:61], v[170:173], v[198:201], v[58:61]
	v_mfma_f32_16x16x32_bf16 v[46:49], v[148:151], v[206:209], v[46:49]
	v_mfma_f32_16x16x32_bf16 v[42:45], v[170:173], v[206:209], v[42:45]
	v_mfma_f32_16x16x32_bf16 v[30:33], v[148:151], v[214:217], v[30:33]
	v_mfma_f32_16x16x32_bf16 v[26:29], v[170:173], v[214:217], v[26:29]
	v_mfma_f32_16x16x32_bf16 v[14:17], v[148:151], v[222:225], v[14:17]
	v_mfma_f32_16x16x32_bf16 v[10:13], v[170:173], v[222:225], v[10:13]
	v_mfma_f32_16x16x32_bf16 v[54:57], v[174:177], v[194:197], v[54:57]
	v_mfma_f32_16x16x32_bf16 v[50:53], v[182:185], v[194:197], v[50:53]
	v_mfma_f32_16x16x32_bf16 v[38:41], v[174:177], v[202:205], v[38:41]
	v_mfma_f32_16x16x32_bf16 v[34:37], v[182:185], v[202:205], v[34:37]
	v_mfma_f32_16x16x32_bf16 v[22:25], v[174:177], v[210:213], v[22:25]
	v_mfma_f32_16x16x32_bf16 v[18:21], v[182:185], v[210:213], v[18:21]
	v_mfma_f32_16x16x32_bf16 v[6:9], v[174:177], v[218:221], v[6:9]
	v_mfma_f32_16x16x32_bf16 v[2:5], v[182:185], v[218:221], v[2:5]
	v_mfma_f32_16x16x32_bf16 v[54:57], v[178:181], v[198:201], v[54:57]
	v_mfma_f32_16x16x32_bf16 v[50:53], v[190:193], v[198:201], v[50:53]
	v_mfma_f32_16x16x32_bf16 v[38:41], v[178:181], v[206:209], v[38:41]
	v_mfma_f32_16x16x32_bf16 v[34:37], v[190:193], v[206:209], v[34:37]
	v_mfma_f32_16x16x32_bf16 v[22:25], v[178:181], v[214:217], v[22:25]
	v_mfma_f32_16x16x32_bf16 v[18:21], v[190:193], v[214:217], v[18:21]
	v_mfma_f32_16x16x32_bf16 v[6:9], v[178:181], v[222:225], v[6:9]
	v_mfma_f32_16x16x32_bf16 v[2:5], v[190:193], v[222:225], v[2:5]
	s_setprio 0
	s_barrier
	s_add_i32 s48, s48, 2
	s_add_u32 s44, s44, 0x100
	s_addc_u32 s45, s45, 0
	s_cmpk_gt_u32 s48, 0x55
	s_mov_b64 s[26:27], s[6:7]
	s_cbranch_scc0 .LBB0_1165
	s_and_b64 vcc, exec, s[20:21]
	s_cbranch_vccz .LBB0_1168
	s_barrier

; #define PG8_STAGE(bufoff, gbase, voff) do { _Pragma("unroll") for (int _i = 0; _i < 2; ++_i) \
;         __builtin_amdgcn_global_load_lds((const unsigned*)((const char*)(gbase) + (voff)[_i]), (PG8_LAS unsigned*)(lds + (bufoff) + ldsw + _i * 8192), 16, 0, 0); } while (0)
; #define PG8_LDA(dst, b, h) do { _Pragma("unroll") for (int m = 0; m < 4; ++m) _Pragma("unroll") for (int k = 0; k < 2; ++k) dst[m][k] = *(const PG8_LAS bf16x8*)(lds + PG8_SA(b, h) + aoff + m * 2048 + k * 1024); } while (0)
; #define PG8_LDB(dst, b, h) do { _Pragma("unroll") for (int n = 0; n < 2; ++n) _Pragma("unroll") for (int k = 0; k < 2; ++k) dst[n][k] = *(const PG8_LAS bf16x8*)(lds + PG8_SB(b, h) + boff + n * 2048 + k * 1024); } while (0)
; #define PG8_MMA(ai, bj, At, Bt) do { __builtin_amdgcn_s_setprio(1); _Pragma("unroll") for (int m = 0; m < 4; ++m) _Pragma("unroll") for (int n = 0; n < 2; ++n) _Pragma("unroll") for (int k = 0; k < 2; ++k) \
;         acc[ai][bj][m][n] = __builtin_amdgcn_mfma_f32_16x16x32_bf16(Bt[n][k], At[m][k], acc[ai][bj][m][n], 0, 0, 0); __builtin_amdgcn_s_setprio(0); } while (0)
; #define PG8_WAIT_V(n) asm volatile("s_waitcnt vmcnt(" #n ")" ::: "memory")
; #define PG8_WAIT_L(n) asm volatile("s_waitcnt lgkmcnt(" #n ")" ::: "memory")
; #define PG8_BAR __builtin_amdgcn_s_barrier()
; #define PG8_SCHED __builtin_amdgcn_sched_barrier(0)
; template <class Epi, class Sched, bool ALIGN_EPI = false, bool SP2 = false>
; __device__ __forceinline__ void gemm_phase(PG8_LAS unsigned char* lds, const Gemm g, const Sched& S, const Epi& E) {
;     ...
;         for (int t = 0; t < nt; t += 2) {
;             const bool last = (t == nt - 2);
;             const char* a1 = cA + (size_t)(t + 1) * kstep;
;             const char* a2 = last ? nA : cA + (size_t)(t + 2) * kstep; const char* b2 = last ? nB : cB + (size_t)(t + 2) * kstep;
;             const char* a3 = a2 + kstep; const char* b3 = b2 + kstep;
;             if (last && has_next) S.a_ready(nxt);
;             if constexpr (SP2) {
;             PG8_LDB(B0, 0, 0); PG8_LDB(B1, 0, 1); PG8_SCHED; PG8_LDA(At, 0, 0); PG8_STAGE(PG8_SA(1, 1), a1 + hstep, voffA);
;             PG8_WAIT_V(8); PG8_WAIT_L(0); PG8_BAR; PG8_MMA(0, 0, At, B0); PG8_MMA(0, 1, At, B1); PG8_BAR; PG8_SCHED;
;             PG8_LDA(At, 0, 1); PG8_STAGE(PG8_SB(0, 0), b2, voffB); PG8_STAGE(PG8_SB(0, 1), b2 + hstep, voffB); PG8_STAGE(PG8_SA(0, 0), a2, voffA);
.LBB0_1217:
	ds_read_b128 v[148:151], v145
	ds_read_b128 v[152:155], v145 offset:1024
	ds_read_b128 v[156:159], v145 offset:2048
	ds_read_b128 v[166:169], v145 offset:3072
	ds_read_b128 v[170:173], v146
	ds_read_b128 v[174:177], v146 offset:1024
	ds_read_b128 v[178:181], v146 offset:2048
	ds_read_b128 v[182:185], v146 offset:3072
	s_add_u32 s28, s26, 0x100
	s_addc_u32 s29, s27, 0
	s_cmp_eq_u32 s42, 4
	s_cselect_b32 s35, s7, s29
	s_cselect_b32 s34, s6, s28
	s_cselect_b32 s31, s25, s41
	s_cselect_b32 s30, s24, s23
	v_lshl_add_u64 v[160:161], s[26:27], 0, v[134:135]
	s_add_i32 m0, s3, 0xc000
	ds_read_b128 v[190:193], v147
	ds_read_b128 v[194:197], v147 offset:1024
	ds_read_b128 v[198:201], v147 offset:2048
	ds_read_b128 v[202:205], v147 offset:3072
	ds_read_b128 v[206:209], v147 offset:4096
	ds_read_b128 v[210:213], v147 offset:5120
	ds_read_b128 v[214:217], v147 offset:6144
	ds_read_b128 v[218:221], v147 offset:7168
	global_load_lds_dwordx4 v[160:161], off
	s_add_i32 m0, s3, 0xe000
	v_lshl_add_u64 v[160:161], s[26:27], 0, v[136:137]
	global_load_lds_dwordx4 v[160:161], off
	s_waitcnt vmcnt(8)
	s_waitcnt lgkmcnt(0)
	s_barrier
	s_setprio 1
	s_waitcnt lgkmcnt(0)
	v_mfma_f32_16x16x32_bf16 v[126:129], v[148:151], v[190:193], v[126:129]
	v_mfma_f32_16x16x32_bf16 v[122:125], v[156:159], v[190:193], v[122:125]
	v_mfma_f32_16x16x32_bf16 v[118:121], v[148:151], v[198:201], v[118:121]
	v_mfma_f32_16x16x32_bf16 v[114:117], v[156:159], v[198:201], v[114:117]
	v_mfma_f32_16x16x32_bf16 v[106:109], v[148:151], v[206:209], v[106:109]
	v_mfma_f32_16x16x32_bf16 v[98:101], v[156:159], v[206:209], v[98:101]
	v_mfma_f32_16x16x32_bf16 v[90:93], v[148:151], v[214:217], v[90:93]
	v_mfma_f32_16x16x32_bf16 v[82:85], v[156:159], v[214:217], v[82:85]
	v_mfma_f32_16x16x32_bf16 v[126:129], v[152:155], v[194:197], v[126:129]
	v_mfma_f32_16x16x32_bf16 v[122:125], v[166:169], v[194:197], v[122:125]
	v_mfma_f32_16x16x32_bf16 v[118:121], v[152:155], v[202:205], v[118:121]
	v_mfma_f32_16x16x32_bf16 v[114:117], v[166:169], v[202:205], v[114:117]
	v_mfma_f32_16x16x32_bf16 v[106:109], v[152:155], v[210:213], v[106:109]
	v_mfma_f32_16x16x32_bf16 v[98:101], v[166:169], v[210:213], v[98:101]
	v_mfma_f32_16x16x32_bf16 v[90:93], v[152:155], v[218:221], v[90:93]
	v_mfma_f32_16x16x32_bf16 v[82:85], v[166:169], v[218:221], v[82:85]
	v_mfma_f32_16x16x32_bf16 v[110:113], v[170:173], v[190:193], v[110:113]
	v_mfma_f32_16x16x32_bf16 v[102:105], v[178:181], v[190:193], v[102:105]
	v_mfma_f32_16x16x32_bf16 v[94:97], v[170:173], v[198:201], v[94:97]
	v_mfma_f32_16x16x32_bf16 v[86:89], v[178:181], v[198:201], v[86:89]
	v_mfma_f32_16x16x32_bf16 v[78:81], v[170:173], v[206:209], v[78:81]
	v_mfma_f32_16x16x32_bf16 v[74:77], v[178:181], v[206:209], v[74:77]
	v_mfma_f32_16x16x32_bf16 v[70:73], v[170:173], v[214:217], v[70:73]
	v_mfma_f32_16x16x32_bf16 v[66:69], v[178:181], v[214:217], v[66:69]
	v_mfma_f32_16x16x32_bf16 v[110:113], v[174:177], v[194:197], v[110:113]
	v_mfma_f32_16x16x32_bf16 v[102:105], v[182:185], v[194:197], v[102:105]
	v_mfma_f32_16x16x32_bf16 v[94:97], v[174:177], v[202:205], v[94:97]
	v_mfma_f32_16x16x32_bf16 v[86:89], v[182:185], v[202:205], v[86:89]
	v_mfma_f32_16x16x32_bf16 v[78:81], v[174:177], v[210:213], v[78:81]
	v_mfma_f32_16x16x32_bf16 v[74:77], v[182:185], v[210:213], v[74:77]
	v_mfma_f32_16x16x32_bf16 v[70:73], v[174:177], v[218:221], v[70:73]
	v_mfma_f32_16x16x32_bf16 v[66:69], v[182:185], v[218:221], v[66:69]
	s_setprio 0
	s_barrier
	s_add_i32 s26, s37, s2
	v_lshl_add_u64 v[160:161], s[30:31], 0, v[132:133]
	s_mov_b32 m0, s26
	ds_read_b128 v[190:193], v147 offset:16384
	ds_read_b128 v[194:197], v147 offset:17408
	ds_read_b128 v[198:201], v147 offset:18432
	ds_read_b128 v[202:205], v147 offset:19456
	ds_read_b128 v[206:209], v147 offset:20480
	ds_read_b128 v[210:213], v147 offset:21504
	ds_read_b128 v[214:217], v147 offset:22528
	ds_read_b128 v[218:221], v147 offset:23552
	global_load_lds_dwordx4 v[160:161], off
	s_add_i32 m0, s26, 0x2000
	s_add_u32 s26, s30, 0x160000
	v_lshl_add_u64 v[186:187], s[30:31], 0, v[130:131]
	s_addc_u32 s27, s31, 0
	s_add_i32 s43, s38, s2
	global_load_lds_dwordx4 v[186:187], off
	v_lshl_add_u64 v[222:223], s[26:27], 0, v[132:133]
	s_mov_b32 m0, s43
	v_lshl_add_u64 v[224:225], s[34:35], 0, v[130:131]
	global_load_lds_dwordx4 v[222:223], off
	s_add_i32 m0, s43, 0x2000
	v_lshl_add_u64 v[222:223], s[26:27], 0, v[130:131]
	global_load_lds_dwordx4 v[222:223], off
	s_mov_b32 m0, s3
	v_lshl_add_u64 v[222:223], s[34:35], 0, v[132:133]
	global_load_lds_dwordx4 v[222:223], off
	s_mov_b32 m0, s4
	s_nop 0
	global_load_lds_dwordx4 v[224:225], off
	s_waitcnt vmcnt(8)
	s_waitcnt lgkmcnt(0)
	s_barrier
; #define PG8_STAGE(bufoff, gbase, voff) do { _Pragma("unroll") for (int _i = 0; _i < 2; ++_i) \
;         __builtin_amdgcn_global_load_lds((const unsigned*)((const char*)(gbase) + (voff)[_i]), (PG8_LAS unsigned*)(lds + (bufoff) + ldsw + _i * 8192), 16, 0, 0); } while (0)
; #define PG8_LDA(dst, b, h) do { _Pragma("unroll") for (int m = 0; m < 4; ++m) _Pragma("unroll") for (int k = 0; k < 2; ++k) dst[m][k] = *(const PG8_LAS bf16x8*)(lds + PG8_SA(b, h) + aoff + m * 2048 + k * 1024); } while (0)
; #define PG8_LDB(dst, b, h) do { _Pragma("unroll") for (int n = 0; n < 2; ++n) _Pragma("unroll") for (int k = 0; k < 2; ++k) dst[n][k] = *(const PG8_LAS bf16x8*)(lds + PG8_SB(b, h) + boff + n * 2048 + k * 1024); } while (0)
; #define PG8_MMA(ai, bj, At, Bt) do { __builtin_amdgcn_s_setprio(1); _Pragma("unroll") for (int m = 0; m < 4; ++m) _Pragma("unroll") for (int n = 0; n < 2; ++n) _Pragma("unroll") for (int k = 0; k < 2; ++k) \
;         acc[ai][bj][m][n] = __builtin_amdgcn_mfma_f32_16x16x32_bf16(Bt[n][k], At[m][k], acc[ai][bj][m][n], 0, 0, 0); __builtin_amdgcn_s_setprio(0); } while (0)
; #define PG8_WAIT_V(n) asm volatile("s_waitcnt vmcnt(" #n ")" ::: "memory")
; #define PG8_WAIT_L(n) asm volatile("s_waitcnt lgkmcnt(" #n ")" ::: "memory")
; #define PG8_BAR __builtin_amdgcn_s_barrier()
; #define PG8_SCHED __builtin_amdgcn_sched_barrier(0)
; template <class Epi, class Sched, bool ALIGN_EPI = false, bool SP2 = false>
; __device__ __forceinline__ void gemm_phase(PG8_LAS unsigned char* lds, const Gemm g, const Sched& S, const Epi& E) {
;     ...
;             PG8_WAIT_V(8); PG8_WAIT_L(0); PG8_BAR; PG8_MMA(1, 0, At, B0); PG8_MMA(1, 1, At, B1); PG8_BAR; PG8_SCHED;
;             PG8_LDB(B0, 1, 0); PG8_LDB(B1, 1, 1); PG8_SCHED; PG8_LDA(At, 1, 0); PG8_STAGE(PG8_SA(0, 1), a2 + hstep, voffA);
;             PG8_WAIT_V(8); PG8_WAIT_L(0); PG8_BAR; PG8_MMA(0, 0, At, B0); PG8_MMA(0, 1, At, B1); PG8_BAR; PG8_SCHED;
	s_setprio 1
	s_waitcnt lgkmcnt(0)
	v_mfma_f32_16x16x32_bf16 v[62:65], v[148:151], v[190:193], v[62:65]
	v_mfma_f32_16x16x32_bf16 v[58:61], v[156:159], v[190:193], v[58:61]
	v_mfma_f32_16x16x32_bf16 v[54:57], v[148:151], v[198:201], v[54:57]
	v_mfma_f32_16x16x32_bf16 v[50:53], v[156:159], v[198:201], v[50:53]
	v_mfma_f32_16x16x32_bf16 v[38:41], v[148:151], v[206:209], v[38:41]
	v_mfma_f32_16x16x32_bf16 v[34:37], v[156:159], v[206:209], v[34:37]
	v_mfma_f32_16x16x32_bf16 v[22:25], v[148:151], v[214:217], v[22:25]
	v_mfma_f32_16x16x32_bf16 v[18:21], v[156:159], v[214:217], v[18:21]
	v_mfma_f32_16x16x32_bf16 v[62:65], v[152:155], v[194:197], v[62:65]
	v_mfma_f32_16x16x32_bf16 v[58:61], v[166:169], v[194:197], v[58:61]
	v_mfma_f32_16x16x32_bf16 v[54:57], v[152:155], v[202:205], v[54:57]
	v_mfma_f32_16x16x32_bf16 v[50:53], v[166:169], v[202:205], v[50:53]
	v_mfma_f32_16x16x32_bf16 v[38:41], v[152:155], v[210:213], v[38:41]
	v_mfma_f32_16x16x32_bf16 v[34:37], v[166:169], v[210:213], v[34:37]
	v_mfma_f32_16x16x32_bf16 v[22:25], v[152:155], v[218:221], v[22:25]
	v_mfma_f32_16x16x32_bf16 v[18:21], v[166:169], v[218:221], v[18:21]
	v_mfma_f32_16x16x32_bf16 v[46:49], v[170:173], v[190:193], v[46:49]
	v_mfma_f32_16x16x32_bf16 v[42:45], v[178:181], v[190:193], v[42:45]
	v_mfma_f32_16x16x32_bf16 v[30:33], v[170:173], v[198:201], v[30:33]
	v_mfma_f32_16x16x32_bf16 v[26:29], v[178:181], v[198:201], v[26:29]
	v_mfma_f32_16x16x32_bf16 v[14:17], v[170:173], v[206:209], v[14:17]
	v_mfma_f32_16x16x32_bf16 v[10:13], v[178:181], v[206:209], v[10:13]
	v_mfma_f32_16x16x32_bf16 v[6:9], v[170:173], v[214:217], v[6:9]
	v_mfma_f32_16x16x32_bf16 v[2:5], v[178:181], v[214:217], v[2:5]
	v_mfma_f32_16x16x32_bf16 v[46:49], v[174:177], v[194:197], v[46:49]
	v_mfma_f32_16x16x32_bf16 v[42:45], v[182:185], v[194:197], v[42:45]
	v_mfma_f32_16x16x32_bf16 v[30:33], v[174:177], v[202:205], v[30:33]
	v_mfma_f32_16x16x32_bf16 v[26:29], v[182:185], v[202:205], v[26:29]
	v_mfma_f32_16x16x32_bf16 v[14:17], v[174:177], v[210:213], v[14:17]
	v_mfma_f32_16x16x32_bf16 v[10:13], v[182:185], v[210:213], v[10:13]
	v_mfma_f32_16x16x32_bf16 v[6:9], v[174:177], v[218:221], v[6:9]
	v_mfma_f32_16x16x32_bf16 v[2:5], v[182:185], v[218:221], v[2:5]
	s_setprio 0
	s_barrier
	s_add_i32 s43, 0, 0x18000
	v_add_u32_e32 v162, s43, v142
	s_add_i32 s44, 0, 0x1c000
	ds_read_b128 v[148:151], v162
	ds_read_b128 v[152:155], v162 offset:1024
	ds_read_b128 v[156:159], v162 offset:2048
	ds_read_b128 v[166:169], v162 offset:3072
	v_add_u32_e32 v162, s44, v142
	ds_read_b128 v[170:173], v162
	ds_read_b128 v[174:177], v162 offset:1024
	ds_read_b128 v[178:181], v162 offset:2048
	ds_read_b128 v[182:185], v162 offset:3072
	s_add_u32 s26, s34, 0x160000
	s_addc_u32 s27, s35, 0
	s_mov_b32 m0, s5
	v_lshl_add_u64 v[226:227], s[26:27], 0, v[132:133]
	ds_read_b128 v[190:193], v147 offset:32768
	ds_read_b128 v[194:197], v147 offset:33792
	ds_read_b128 v[198:201], v147 offset:34816
	ds_read_b128 v[202:205], v147 offset:35840
	ds_read_b128 v[206:209], v147 offset:36864
	ds_read_b128 v[210:213], v147 offset:37888
	ds_read_b128 v[214:217], v147 offset:38912
	ds_read_b128 v[218:221], v147 offset:39936
	global_load_lds_dwordx4 v[226:227], off
	s_mov_b32 m0, s11
	v_lshl_add_u64 v[226:227], s[26:27], 0, v[130:131]
	global_load_lds_dwordx4 v[226:227], off
	s_waitcnt vmcnt(8)
	s_waitcnt lgkmcnt(0)
	s_barrier
	s_setprio 1
	s_waitcnt lgkmcnt(0)
	v_mfma_f32_16x16x32_bf16 v[126:129], v[148:151], v[190:193], v[126:129]
	v_mfma_f32_16x16x32_bf16 v[122:125], v[156:159], v[190:193], v[122:125]
	v_mfma_f32_16x16x32_bf16 v[118:121], v[148:151], v[198:201], v[118:121]
	v_mfma_f32_16x16x32_bf16 v[114:117], v[156:159], v[198:201], v[114:117]
	v_mfma_f32_16x16x32_bf16 v[106:109], v[148:151], v[206:209], v[106:109]
	v_mfma_f32_16x16x32_bf16 v[98:101], v[156:159], v[206:209], v[98:101]
	v_mfma_f32_16x16x32_bf16 v[90:93], v[148:151], v[214:217], v[90:93]
	v_mfma_f32_16x16x32_bf16 v[82:85], v[156:159], v[214:217], v[82:85]
	v_mfma_f32_16x16x32_bf16 v[126:129], v[152:155], v[194:197], v[126:129]
	v_mfma_f32_16x16x32_bf16 v[122:125], v[166:169], v[194:197], v[122:125]
	v_mfma_f32_16x16x32_bf16 v[118:121], v[152:155], v[202:205], v[118:121]
	v_mfma_f32_16x16x32_bf16 v[114:117], v[166:169], v[202:205], v[114:117]
	v_mfma_f32_16x16x32_bf16 v[106:109], v[152:155], v[210:213], v[106:109]
	v_mfma_f32_16x16x32_bf16 v[98:101], v[166:169], v[210:213], v[98:101]
	v_mfma_f32_16x16x32_bf16 v[90:93], v[152:155], v[218:221], v[90:93]
	v_mfma_f32_16x16x32_bf16 v[82:85], v[166:169], v[218:221], v[82:85]
	v_mfma_f32_16x16x32_bf16 v[110:113], v[170:173], v[190:193], v[110:113]
	v_mfma_f32_16x16x32_bf16 v[102:105], v[178:181], v[190:193], v[102:105]
	v_mfma_f32_16x16x32_bf16 v[94:97], v[170:173], v[198:201], v[94:97]
	v_mfma_f32_16x16x32_bf16 v[86:89], v[178:181], v[198:201], v[86:89]
	v_mfma_f32_16x16x32_bf16 v[78:81], v[170:173], v[206:209], v[78:81]
	v_mfma_f32_16x16x32_bf16 v[74:77], v[178:181], v[206:209], v[74:77]
	v_mfma_f32_16x16x32_bf16 v[70:73], v[170:173], v[214:217], v[70:73]
	v_mfma_f32_16x16x32_bf16 v[66:69], v[178:181], v[214:217], v[66:69]
	v_mfma_f32_16x16x32_bf16 v[110:113], v[174:177], v[194:197], v[110:113]
	v_mfma_f32_16x16x32_bf16 v[102:105], v[182:185], v[194:197], v[102:105]
	v_mfma_f32_16x16x32_bf16 v[94:97], v[174:177], v[202:205], v[94:97]
	v_mfma_f32_16x16x32_bf16 v[86:89], v[182:185], v[202:205], v[86:89]
	v_mfma_f32_16x16x32_bf16 v[78:81], v[174:177], v[210:213], v[78:81]
	v_mfma_f32_16x16x32_bf16 v[74:77], v[182:185], v[210:213], v[74:77]
	v_mfma_f32_16x16x32_bf16 v[70:73], v[174:177], v[218:221], v[70:73]
	v_mfma_f32_16x16x32_bf16 v[66:69], v[182:185], v[218:221], v[66:69]
	s_setprio 0
	s_barrier
; #define PG8_STAGE(bufoff, gbase, voff) do { _Pragma("unroll") for (int _i = 0; _i < 2; ++_i) \
;         __builtin_amdgcn_global_load_lds((const unsigned*)((const char*)(gbase) + (voff)[_i]), (PG8_LAS unsigned*)(lds + (bufoff) + ldsw + _i * 8192), 16, 0, 0); } while (0)
; #define PG8_LDA(dst, b, h) do { _Pragma("unroll") for (int m = 0; m < 4; ++m) _Pragma("unroll") for (int k = 0; k < 2; ++k) dst[m][k] = *(const PG8_LAS bf16x8*)(lds + PG8_SA(b, h) + aoff + m * 2048 + k * 1024); } while (0)
; #define PG8_MMA(ai, bj, At, Bt) do { __builtin_amdgcn_s_setprio(1); _Pragma("unroll") for (int m = 0; m < 4; ++m) _Pragma("unroll") for (int n = 0; n < 2; ++n) _Pragma("unroll") for (int k = 0; k < 2; ++k) \
;         acc[ai][bj][m][n] = __builtin_amdgcn_mfma_f32_16x16x32_bf16(Bt[n][k], At[m][k], acc[ai][bj][m][n], 0, 0, 0); __builtin_amdgcn_s_setprio(0); } while (0)
; #define PG8_WAIT_V(n) asm volatile("s_waitcnt vmcnt(" #n ")" ::: "memory")
; #define PG8_WAIT_L(n) asm volatile("s_waitcnt lgkmcnt(" #n ")" ::: "memory")
; #define PG8_BAR __builtin_amdgcn_s_barrier()
; #define PG8_SCHED __builtin_amdgcn_sched_barrier(0)
; template <class Epi, class Sched, bool ALIGN_EPI = false, bool SP2 = false>
; __device__ __forceinline__ void gemm_phase(PG8_LAS unsigned char* lds, const Gemm g, const Sched& S, const Epi& E) {
;     ...
;             PG8_LDA(At, 1, 1); PG8_STAGE(PG8_SB(1, 0), b3, voffB); PG8_STAGE(PG8_SB(1, 1), b3 + hstep, voffB); PG8_STAGE(PG8_SA(1, 0), a3, voffA);
;             PG8_WAIT_V(8); PG8_WAIT_L(0); PG8_BAR; PG8_MMA(1, 0, At, B0); PG8_MMA(1, 1, At, B1); PG8_BAR; PG8_SCHED;
;     ...
;         if constexpr (ALIGN_EPI) { if (wr == 0) PG8_BAR; }
	s_add_i32 s26, s43, s2
	v_lshl_add_u64 v[160:161], v[160:161], 0, s[18:19]
	s_mov_b32 m0, s26
	ds_read_b128 v[190:193], v147 offset:49152
	ds_read_b128 v[194:197], v147 offset:50176
	ds_read_b128 v[198:201], v147 offset:51200
	ds_read_b128 v[202:205], v147 offset:52224
	ds_read_b128 v[206:209], v147 offset:53248
	ds_read_b128 v[210:213], v147 offset:54272
	ds_read_b128 v[214:217], v147 offset:55296
	ds_read_b128 v[218:221], v147 offset:56320
	global_load_lds_dwordx4 v[160:161], off
	s_add_i32 m0, s26, 0x2000
	s_add_u32 s26, s30, 0x160080
	v_lshl_add_u64 v[160:161], v[186:187], 0, s[18:19]
	s_addc_u32 s27, s31, 0
	s_add_i32 s30, s44, s2
	global_load_lds_dwordx4 v[160:161], off
	s_mov_b32 m0, s30
	v_lshl_add_u64 v[160:161], s[26:27], 0, v[132:133]
	global_load_lds_dwordx4 v[160:161], off
	s_add_i32 m0, s30, 0x2000
	v_lshl_add_u64 v[160:161], s[26:27], 0, v[130:131]
	global_load_lds_dwordx4 v[160:161], off
	s_mov_b32 m0, s33
	v_lshl_add_u64 v[160:161], v[222:223], 0, s[18:19]
	global_load_lds_dwordx4 v[160:161], off
	s_mov_b32 m0, s36
	v_lshl_add_u64 v[160:161], v[224:225], 0, s[18:19]
	global_load_lds_dwordx4 v[160:161], off
	s_waitcnt vmcnt(8)
	s_waitcnt lgkmcnt(0)
	s_barrier
	s_setprio 1
	s_waitcnt lgkmcnt(0)
	v_mfma_f32_16x16x32_bf16 v[62:65], v[148:151], v[190:193], v[62:65]
	v_mfma_f32_16x16x32_bf16 v[58:61], v[156:159], v[190:193], v[58:61]
	v_mfma_f32_16x16x32_bf16 v[54:57], v[148:151], v[198:201], v[54:57]
	v_mfma_f32_16x16x32_bf16 v[50:53], v[156:159], v[198:201], v[50:53]
	v_mfma_f32_16x16x32_bf16 v[38:41], v[148:151], v[206:209], v[38:41]
	v_mfma_f32_16x16x32_bf16 v[34:37], v[156:159], v[206:209], v[34:37]
	v_mfma_f32_16x16x32_bf16 v[22:25], v[148:151], v[214:217], v[22:25]
	v_mfma_f32_16x16x32_bf16 v[18:21], v[156:159], v[214:217], v[18:21]
	v_mfma_f32_16x16x32_bf16 v[62:65], v[152:155], v[194:197], v[62:65]
	v_mfma_f32_16x16x32_bf16 v[58:61], v[166:169], v[194:197], v[58:61]
	v_mfma_f32_16x16x32_bf16 v[54:57], v[152:155], v[202:205], v[54:57]
	v_mfma_f32_16x16x32_bf16 v[50:53], v[166:169], v[202:205], v[50:53]
	v_mfma_f32_16x16x32_bf16 v[38:41], v[152:155], v[210:213], v[38:41]
	v_mfma_f32_16x16x32_bf16 v[34:37], v[166:169], v[210:213], v[34:37]
	v_mfma_f32_16x16x32_bf16 v[22:25], v[152:155], v[218:221], v[22:25]
	v_mfma_f32_16x16x32_bf16 v[18:21], v[166:169], v[218:221], v[18:21]
	v_mfma_f32_16x16x32_bf16 v[46:49], v[170:173], v[190:193], v[46:49]
	v_mfma_f32_16x16x32_bf16 v[42:45], v[178:181], v[190:193], v[42:45]
	v_mfma_f32_16x16x32_bf16 v[30:33], v[170:173], v[198:201], v[30:33]
	v_mfma_f32_16x16x32_bf16 v[26:29], v[178:181], v[198:201], v[26:29]
	v_mfma_f32_16x16x32_bf16 v[14:17], v[170:173], v[206:209], v[14:17]
	v_mfma_f32_16x16x32_bf16 v[10:13], v[178:181], v[206:209], v[10:13]
	v_mfma_f32_16x16x32_bf16 v[6:9], v[170:173], v[214:217], v[6:9]
	v_mfma_f32_16x16x32_bf16 v[2:5], v[178:181], v[214:217], v[2:5]
	v_mfma_f32_16x16x32_bf16 v[46:49], v[174:177], v[194:197], v[46:49]
	v_mfma_f32_16x16x32_bf16 v[42:45], v[182:185], v[194:197], v[42:45]
	v_mfma_f32_16x16x32_bf16 v[30:33], v[174:177], v[202:205], v[30:33]
	v_mfma_f32_16x16x32_bf16 v[26:29], v[182:185], v[202:205], v[26:29]
	v_mfma_f32_16x16x32_bf16 v[14:17], v[174:177], v[210:213], v[14:17]
	v_mfma_f32_16x16x32_bf16 v[10:13], v[182:185], v[210:213], v[10:13]
	v_mfma_f32_16x16x32_bf16 v[6:9], v[174:177], v[218:221], v[6:9]
	v_mfma_f32_16x16x32_bf16 v[2:5], v[182:185], v[218:221], v[2:5]
	s_setprio 0
	s_barrier
	s_add_i32 s42, s42, 2
	s_add_u32 s23, s23, 0x100
	s_addc_u32 s41, s41, 0
	s_cmp_gt_u32 s42, 5
	s_mov_b64 s[26:27], s[28:29]
	s_cbranch_scc0 .LBB0_1217
	s_and_b64 vcc, exec, s[20:21]
	s_cbranch_vccz .LBB0_1220
	s_barrier

; #define PG8_STAGE(bufoff, gbase, voff) do { _Pragma("unroll") for (int _i = 0; _i < 2; ++_i) \
;         __builtin_amdgcn_global_load_lds((const unsigned*)((const char*)(gbase) + (voff)[_i]), (PG8_LAS unsigned*)(lds + (bufoff) + ldsw + _i * 8192), 16, 0, 0); } while (0)
; #define PG8_LDA(dst, b, h) do { _Pragma("unroll") for (int m = 0; m < 4; ++m) _Pragma("unroll") for (int k = 0; k < 2; ++k) dst[m][k] = *(const PG8_LAS bf16x8*)(lds + PG8_SA(b, h) + aoff + m * 2048 + k * 1024); } while (0)
; #define PG8_LDB(dst, b, h) do { _Pragma("unroll") for (int n = 0; n < 2; ++n) _Pragma("unroll") for (int k = 0; k < 2; ++k) dst[n][k] = *(const PG8_LAS bf16x8*)(lds + PG8_SB(b, h) + boff + n * 2048 + k * 1024); } while (0)
; #define PG8_MMA(ai, bj, At, Bt) do { __builtin_amdgcn_s_setprio(1); _Pragma("unroll") for (int m = 0; m < 4; ++m) _Pragma("unroll") for (int n = 0; n < 2; ++n) _Pragma("unroll") for (int k = 0; k < 2; ++k) \
;         acc[ai][bj][m][n] = __builtin_amdgcn_mfma_f32_16x16x32_bf16(Bt[n][k], At[m][k], acc[ai][bj][m][n], 0, 0, 0); __builtin_amdgcn_s_setprio(0); } while (0)
; #define PG8_WAIT_V(n) asm volatile("s_waitcnt vmcnt(" #n ")" ::: "memory")
; #define PG8_WAIT_L(n) asm volatile("s_waitcnt lgkmcnt(" #n ")" ::: "memory")
; #define PG8_BAR __builtin_amdgcn_s_barrier()
; #define PG8_SCHED __builtin_amdgcn_sched_barrier(0)
; template <class Epi, class Sched, bool ALIGN_EPI = false, bool SP2 = false>
; __device__ __forceinline__ void gemm_phase(PG8_LAS unsigned char* lds, const Gemm g, const Sched& S, const Epi& E) {
;     ...
;         for (int t = 0; t < nt; t += 2) {
;             const bool last = (t == nt - 2);
;             const char* a1 = cA + (size_t)(t + 1) * kstep;
;             const char* a2 = last ? nA : cA + (size_t)(t + 2) * kstep; const char* b2 = last ? nB : cB + (size_t)(t + 2) * kstep;
;             const char* a3 = a2 + kstep; const char* b3 = b2 + kstep;
;             if (last && has_next) S.a_ready(nxt);
;             if constexpr (SP2) {
;             PG8_LDB(B0, 0, 0); PG8_LDB(B1, 0, 1); PG8_SCHED; PG8_LDA(At, 0, 0); PG8_STAGE(PG8_SA(1, 1), a1 + hstep, voffA);
;             PG8_WAIT_V(8); PG8_WAIT_L(0); PG8_BAR; PG8_MMA(0, 0, At, B0); PG8_MMA(0, 1, At, B1); PG8_BAR; PG8_SCHED;
;             PG8_LDA(At, 0, 1); PG8_STAGE(PG8_SB(0, 0), b2, voffB); PG8_STAGE(PG8_SB(0, 1), b2 + hstep, voffB); PG8_STAGE(PG8_SA(0, 0), a2, voffA);
.LBB0_1350:
	ds_read_b128 v[148:151], v159
	ds_read_b128 v[152:155], v159 offset:1024
	ds_read_b128 v[166:169], v159 offset:2048
	ds_read_b128 v[170:173], v159 offset:3072
	ds_read_b128 v[174:177], v160
	ds_read_b128 v[178:181], v160 offset:1024
	ds_read_b128 v[182:185], v160 offset:2048
	ds_read_b128 v[190:193], v160 offset:3072
	s_add_u32 s28, s26, 0xfff80080
	s_addc_u32 s29, s27, -1
	s_cmp_eq_u32 s42, 28
	s_cselect_b32 s31, s7, s29
	s_cselect_b32 s30, s21, s28
	s_cselect_b32 s29, s19, s41
	s_cselect_b32 s28, s39, s40
	v_lshl_add_u64 v[186:187], s[26:27], 0, v[140:141]
	s_add_i32 m0, s3, 0xc000
	ds_read_b128 v[194:197], v161
	ds_read_b128 v[198:201], v161 offset:1024
	ds_read_b128 v[202:205], v161 offset:2048
	ds_read_b128 v[206:209], v161 offset:3072
	ds_read_b128 v[210:213], v161 offset:4096
	ds_read_b128 v[214:217], v161 offset:5120
	ds_read_b128 v[218:221], v161 offset:6144
	ds_read_b128 v[222:225], v161 offset:7168
	global_load_lds_dwordx4 v[186:187], off
	s_add_i32 m0, s3, 0xe000
	v_lshl_add_u64 v[186:187], s[26:27], 0, v[142:143]
	global_load_lds_dwordx4 v[186:187], off
	s_waitcnt vmcnt(8)
	s_waitcnt lgkmcnt(0)
	s_barrier
	s_setprio 1
	s_waitcnt lgkmcnt(0)
	v_mfma_f32_16x16x32_bf16 v[126:129], v[148:151], v[194:197], v[126:129]
	v_mfma_f32_16x16x32_bf16 v[122:125], v[166:169], v[194:197], v[122:125]
	v_mfma_f32_16x16x32_bf16 v[110:113], v[148:151], v[202:205], v[110:113]
	v_mfma_f32_16x16x32_bf16 v[106:109], v[166:169], v[202:205], v[106:109]
	v_mfma_f32_16x16x32_bf16 v[94:97], v[148:151], v[210:213], v[94:97]
	v_mfma_f32_16x16x32_bf16 v[90:93], v[166:169], v[210:213], v[90:93]
	v_mfma_f32_16x16x32_bf16 v[78:81], v[148:151], v[218:221], v[78:81]
	v_mfma_f32_16x16x32_bf16 v[74:77], v[166:169], v[218:221], v[74:77]
	v_mfma_f32_16x16x32_bf16 v[126:129], v[152:155], v[198:201], v[126:129]
	v_mfma_f32_16x16x32_bf16 v[122:125], v[170:173], v[198:201], v[122:125]
	v_mfma_f32_16x16x32_bf16 v[110:113], v[152:155], v[206:209], v[110:113]
	v_mfma_f32_16x16x32_bf16 v[106:109], v[170:173], v[206:209], v[106:109]
	v_mfma_f32_16x16x32_bf16 v[94:97], v[152:155], v[214:217], v[94:97]
	v_mfma_f32_16x16x32_bf16 v[90:93], v[170:173], v[214:217], v[90:93]
	v_mfma_f32_16x16x32_bf16 v[78:81], v[152:155], v[222:225], v[78:81]
	v_mfma_f32_16x16x32_bf16 v[74:77], v[170:173], v[222:225], v[74:77]
	v_mfma_f32_16x16x32_bf16 v[118:121], v[174:177], v[194:197], v[118:121]
	v_mfma_f32_16x16x32_bf16 v[114:117], v[182:185], v[194:197], v[114:117]
	v_mfma_f32_16x16x32_bf16 v[102:105], v[174:177], v[202:205], v[102:105]
	v_mfma_f32_16x16x32_bf16 v[98:101], v[182:185], v[202:205], v[98:101]
	v_mfma_f32_16x16x32_bf16 v[86:89], v[174:177], v[210:213], v[86:89]
	v_mfma_f32_16x16x32_bf16 v[82:85], v[182:185], v[210:213], v[82:85]
	v_mfma_f32_16x16x32_bf16 v[70:73], v[174:177], v[218:221], v[70:73]
	v_mfma_f32_16x16x32_bf16 v[66:69], v[182:185], v[218:221], v[66:69]
	v_mfma_f32_16x16x32_bf16 v[118:121], v[178:181], v[198:201], v[118:121]
	v_mfma_f32_16x16x32_bf16 v[114:117], v[190:193], v[198:201], v[114:117]
	v_mfma_f32_16x16x32_bf16 v[102:105], v[178:181], v[206:209], v[102:105]
	v_mfma_f32_16x16x32_bf16 v[98:101], v[190:193], v[206:209], v[98:101]
	v_mfma_f32_16x16x32_bf16 v[86:89], v[178:181], v[214:217], v[86:89]
	v_mfma_f32_16x16x32_bf16 v[82:85], v[190:193], v[214:217], v[82:85]
	v_mfma_f32_16x16x32_bf16 v[70:73], v[178:181], v[222:225], v[70:73]
	v_mfma_f32_16x16x32_bf16 v[66:69], v[190:193], v[222:225], v[66:69]
	s_setprio 0
	s_barrier
	s_add_i32 s43, s36, s2
	v_lshl_add_u64 v[186:187], s[28:29], 0, v[132:133]
	s_mov_b32 m0, s43
	ds_read_b128 v[194:197], v161 offset:16384
	ds_read_b128 v[198:201], v161 offset:17408
	ds_read_b128 v[202:205], v161 offset:18432
	ds_read_b128 v[206:209], v161 offset:19456
	ds_read_b128 v[210:213], v161 offset:20480
	ds_read_b128 v[214:217], v161 offset:21504
	ds_read_b128 v[218:221], v161 offset:22528
	ds_read_b128 v[222:225], v161 offset:23552
	global_load_lds_dwordx4 v[186:187], off
	s_add_i32 m0, s43, 0x2000
	s_add_u32 s44, s28, 0x80000
	v_lshl_add_u64 v[226:227], s[28:29], 0, v[136:137]
	s_addc_u32 s45, s29, 0
	s_add_i32 s43, s37, s2
	global_load_lds_dwordx4 v[226:227], off
	v_lshl_add_u64 v[228:229], s[44:45], 0, v[132:133]
	s_mov_b32 m0, s43
	v_lshl_add_u64 v[230:231], s[30:31], 0, v[134:135]
	global_load_lds_dwordx4 v[228:229], off
	s_add_i32 m0, s43, 0x2000
	v_lshl_add_u64 v[228:229], s[44:45], 0, v[136:137]
	global_load_lds_dwordx4 v[228:229], off
	s_mov_b32 m0, s3
	v_lshl_add_u64 v[228:229], s[30:31], 0, v[130:131]
	global_load_lds_dwordx4 v[228:229], off
	s_mov_b32 m0, s4
	s_nop 0
	global_load_lds_dwordx4 v[230:231], off
	s_waitcnt vmcnt(8)
	s_waitcnt lgkmcnt(0)
	s_barrier
; #define PG8_STAGE(bufoff, gbase, voff) do { _Pragma("unroll") for (int _i = 0; _i < 2; ++_i) \
;         __builtin_amdgcn_global_load_lds((const unsigned*)((const char*)(gbase) + (voff)[_i]), (PG8_LAS unsigned*)(lds + (bufoff) + ldsw + _i * 8192), 16, 0, 0); } while (0)
; #define PG8_LDA(dst, b, h) do { _Pragma("unroll") for (int m = 0; m < 4; ++m) _Pragma("unroll") for (int k = 0; k < 2; ++k) dst[m][k] = *(const PG8_LAS bf16x8*)(lds + PG8_SA(b, h) + aoff + m * 2048 + k * 1024); } while (0)
; #define PG8_LDB(dst, b, h) do { _Pragma("unroll") for (int n = 0; n < 2; ++n) _Pragma("unroll") for (int k = 0; k < 2; ++k) dst[n][k] = *(const PG8_LAS bf16x8*)(lds + PG8_SB(b, h) + boff + n * 2048 + k * 1024); } while (0)
; #define PG8_MMA(ai, bj, At, Bt) do { __builtin_amdgcn_s_setprio(1); _Pragma("unroll") for (int m = 0; m < 4; ++m) _Pragma("unroll") for (int n = 0; n < 2; ++n) _Pragma("unroll") for (int k = 0; k < 2; ++k) \
;         acc[ai][bj][m][n] = __builtin_amdgcn_mfma_f32_16x16x32_bf16(Bt[n][k], At[m][k], acc[ai][bj][m][n], 0, 0, 0); __builtin_amdgcn_s_setprio(0); } while (0)
; #define PG8_WAIT_V(n) asm volatile("s_waitcnt vmcnt(" #n ")" ::: "memory")
; #define PG8_WAIT_L(n) asm volatile("s_waitcnt lgkmcnt(" #n ")" ::: "memory")
; #define PG8_BAR __builtin_amdgcn_s_barrier()
; #define PG8_SCHED __builtin_amdgcn_sched_barrier(0)
; template <class Epi, class Sched, bool ALIGN_EPI = false, bool SP2 = false>
; __device__ __forceinline__ void gemm_phase(PG8_LAS unsigned char* lds, const Gemm g, const Sched& S, const Epi& E) {
;     ...
;             PG8_WAIT_V(8); PG8_WAIT_L(0); PG8_BAR; PG8_MMA(1, 0, At, B0); PG8_MMA(1, 1, At, B1); PG8_BAR; PG8_SCHED;
;             PG8_LDB(B0, 1, 0); PG8_LDB(B1, 1, 1); PG8_SCHED; PG8_LDA(At, 1, 0); PG8_STAGE(PG8_SA(0, 1), a2 + hstep, voffA);
;             PG8_WAIT_V(8); PG8_WAIT_L(0); PG8_BAR; PG8_MMA(0, 0, At, B0); PG8_MMA(0, 1, At, B1); PG8_BAR; PG8_SCHED;
	s_setprio 1
	s_waitcnt lgkmcnt(0)
	v_mfma_f32_16x16x32_bf16 v[62:65], v[148:151], v[194:197], v[62:65]
	v_mfma_f32_16x16x32_bf16 v[58:61], v[166:169], v[194:197], v[58:61]
	v_mfma_f32_16x16x32_bf16 v[46:49], v[148:151], v[202:205], v[46:49]
	v_mfma_f32_16x16x32_bf16 v[42:45], v[166:169], v[202:205], v[42:45]
	v_mfma_f32_16x16x32_bf16 v[30:33], v[148:151], v[210:213], v[30:33]
	v_mfma_f32_16x16x32_bf16 v[26:29], v[166:169], v[210:213], v[26:29]
	v_mfma_f32_16x16x32_bf16 v[14:17], v[148:151], v[218:221], v[14:17]
	v_mfma_f32_16x16x32_bf16 v[10:13], v[166:169], v[218:221], v[10:13]
	v_mfma_f32_16x16x32_bf16 v[62:65], v[152:155], v[198:201], v[62:65]
	v_mfma_f32_16x16x32_bf16 v[58:61], v[170:173], v[198:201], v[58:61]
	v_mfma_f32_16x16x32_bf16 v[46:49], v[152:155], v[206:209], v[46:49]
	v_mfma_f32_16x16x32_bf16 v[42:45], v[170:173], v[206:209], v[42:45]
	v_mfma_f32_16x16x32_bf16 v[30:33], v[152:155], v[214:217], v[30:33]
	v_mfma_f32_16x16x32_bf16 v[26:29], v[170:173], v[214:217], v[26:29]
	v_mfma_f32_16x16x32_bf16 v[14:17], v[152:155], v[222:225], v[14:17]
	v_mfma_f32_16x16x32_bf16 v[10:13], v[170:173], v[222:225], v[10:13]
	v_mfma_f32_16x16x32_bf16 v[54:57], v[174:177], v[194:197], v[54:57]
	v_mfma_f32_16x16x32_bf16 v[50:53], v[182:185], v[194:197], v[50:53]
	v_mfma_f32_16x16x32_bf16 v[38:41], v[174:177], v[202:205], v[38:41]
	v_mfma_f32_16x16x32_bf16 v[34:37], v[182:185], v[202:205], v[34:37]
	v_mfma_f32_16x16x32_bf16 v[22:25], v[174:177], v[210:213], v[22:25]
	v_mfma_f32_16x16x32_bf16 v[18:21], v[182:185], v[210:213], v[18:21]
	v_mfma_f32_16x16x32_bf16 v[6:9], v[174:177], v[218:221], v[6:9]
	v_mfma_f32_16x16x32_bf16 v[2:5], v[182:185], v[218:221], v[2:5]
	v_mfma_f32_16x16x32_bf16 v[54:57], v[178:181], v[198:201], v[54:57]
	v_mfma_f32_16x16x32_bf16 v[50:53], v[190:193], v[198:201], v[50:53]
	v_mfma_f32_16x16x32_bf16 v[38:41], v[178:181], v[206:209], v[38:41]
	v_mfma_f32_16x16x32_bf16 v[34:37], v[190:193], v[206:209], v[34:37]
	v_mfma_f32_16x16x32_bf16 v[22:25], v[178:181], v[214:217], v[22:25]
	v_mfma_f32_16x16x32_bf16 v[18:21], v[190:193], v[214:217], v[18:21]
	v_mfma_f32_16x16x32_bf16 v[6:9], v[178:181], v[222:225], v[6:9]
	v_mfma_f32_16x16x32_bf16 v[2:5], v[190:193], v[222:225], v[2:5]
	s_setprio 0
	s_barrier
	s_add_i32 s43, 0, 0x18000
	v_add_u32_e32 v162, s43, v157
	s_add_i32 s44, 0, 0x1c000
	ds_read_b128 v[148:151], v162
	ds_read_b128 v[152:155], v162 offset:1024
	ds_read_b128 v[166:169], v162 offset:2048
	ds_read_b128 v[170:173], v162 offset:3072
	v_add_u32_e32 v162, s44, v157
	ds_read_b128 v[174:177], v162
	ds_read_b128 v[178:181], v162 offset:1024
	ds_read_b128 v[182:185], v162 offset:2048
	ds_read_b128 v[190:193], v162 offset:3072
	s_add_u32 s30, s30, 0x80000
	s_addc_u32 s31, s31, 0
	s_mov_b32 m0, s5
	v_lshl_add_u64 v[232:233], s[30:31], 0, v[130:131]
	ds_read_b128 v[194:197], v161 offset:32768
	ds_read_b128 v[198:201], v161 offset:33792
	ds_read_b128 v[202:205], v161 offset:34816
	ds_read_b128 v[206:209], v161 offset:35840
	ds_read_b128 v[210:213], v161 offset:36864
	ds_read_b128 v[214:217], v161 offset:37888
	ds_read_b128 v[218:221], v161 offset:38912
	ds_read_b128 v[222:225], v161 offset:39936
	global_load_lds_dwordx4 v[232:233], off
	s_mov_b32 m0, s17
	v_lshl_add_u64 v[232:233], s[30:31], 0, v[134:135]
	global_load_lds_dwordx4 v[232:233], off
	s_waitcnt vmcnt(8)
	s_waitcnt lgkmcnt(0)
	s_barrier
	s_setprio 1
	s_waitcnt lgkmcnt(0)
	v_mfma_f32_16x16x32_bf16 v[126:129], v[148:151], v[194:197], v[126:129]
	v_mfma_f32_16x16x32_bf16 v[122:125], v[166:169], v[194:197], v[122:125]
	v_mfma_f32_16x16x32_bf16 v[110:113], v[148:151], v[202:205], v[110:113]
	v_mfma_f32_16x16x32_bf16 v[106:109], v[166:169], v[202:205], v[106:109]
	v_mfma_f32_16x16x32_bf16 v[94:97], v[148:151], v[210:213], v[94:97]
	v_mfma_f32_16x16x32_bf16 v[90:93], v[166:169], v[210:213], v[90:93]
	v_mfma_f32_16x16x32_bf16 v[78:81], v[148:151], v[218:221], v[78:81]
	v_mfma_f32_16x16x32_bf16 v[74:77], v[166:169], v[218:221], v[74:77]
	v_mfma_f32_16x16x32_bf16 v[126:129], v[152:155], v[198:201], v[126:129]
	v_mfma_f32_16x16x32_bf16 v[122:125], v[170:173], v[198:201], v[122:125]
	v_mfma_f32_16x16x32_bf16 v[110:113], v[152:155], v[206:209], v[110:113]
	v_mfma_f32_16x16x32_bf16 v[106:109], v[170:173], v[206:209], v[106:109]
	v_mfma_f32_16x16x32_bf16 v[94:97], v[152:155], v[214:217], v[94:97]
	v_mfma_f32_16x16x32_bf16 v[90:93], v[170:173], v[214:217], v[90:93]
	v_mfma_f32_16x16x32_bf16 v[78:81], v[152:155], v[222:225], v[78:81]
	v_mfma_f32_16x16x32_bf16 v[74:77], v[170:173], v[222:225], v[74:77]
	v_mfma_f32_16x16x32_bf16 v[118:121], v[174:177], v[194:197], v[118:121]
	v_mfma_f32_16x16x32_bf16 v[114:117], v[182:185], v[194:197], v[114:117]
	v_mfma_f32_16x16x32_bf16 v[102:105], v[174:177], v[202:205], v[102:105]
	v_mfma_f32_16x16x32_bf16 v[98:101], v[182:185], v[202:205], v[98:101]
	v_mfma_f32_16x16x32_bf16 v[86:89], v[174:177], v[210:213], v[86:89]
	v_mfma_f32_16x16x32_bf16 v[82:85], v[182:185], v[210:213], v[82:85]
	v_mfma_f32_16x16x32_bf16 v[70:73], v[174:177], v[218:221], v[70:73]
	v_mfma_f32_16x16x32_bf16 v[66:69], v[182:185], v[218:221], v[66:69]
	v_mfma_f32_16x16x32_bf16 v[118:121], v[178:181], v[198:201], v[118:121]
	v_mfma_f32_16x16x32_bf16 v[114:117], v[190:193], v[198:201], v[114:117]
	v_mfma_f32_16x16x32_bf16 v[102:105], v[178:181], v[206:209], v[102:105]
	v_mfma_f32_16x16x32_bf16 v[98:101], v[190:193], v[206:209], v[98:101]
	v_mfma_f32_16x16x32_bf16 v[86:89], v[178:181], v[214:217], v[86:89]
	v_mfma_f32_16x16x32_bf16 v[82:85], v[190:193], v[214:217], v[82:85]
	v_mfma_f32_16x16x32_bf16 v[70:73], v[178:181], v[222:225], v[70:73]
	v_mfma_f32_16x16x32_bf16 v[66:69], v[190:193], v[222:225], v[66:69]
	s_setprio 0
	s_barrier
; #define PG8_STAGE(bufoff, gbase, voff) do { _Pragma("unroll") for (int _i = 0; _i < 2; ++_i) \
;         __builtin_amdgcn_global_load_lds((const unsigned*)((const char*)(gbase) + (voff)[_i]), (PG8_LAS unsigned*)(lds + (bufoff) + ldsw + _i * 8192), 16, 0, 0); } while (0)
; #define PG8_LDA(dst, b, h) do { _Pragma("unroll") for (int m = 0; m < 4; ++m) _Pragma("unroll") for (int k = 0; k < 2; ++k) dst[m][k] = *(const PG8_LAS bf16x8*)(lds + PG8_SA(b, h) + aoff + m * 2048 + k * 1024); } while (0)
; #define PG8_MMA(ai, bj, At, Bt) do { __builtin_amdgcn_s_setprio(1); _Pragma("unroll") for (int m = 0; m < 4; ++m) _Pragma("unroll") for (int n = 0; n < 2; ++n) _Pragma("unroll") for (int k = 0; k < 2; ++k) \
;         acc[ai][bj][m][n] = __builtin_amdgcn_mfma_f32_16x16x32_bf16(Bt[n][k], At[m][k], acc[ai][bj][m][n], 0, 0, 0); __builtin_amdgcn_s_setprio(0); } while (0)
; #define PG8_WAIT_V(n) asm volatile("s_waitcnt vmcnt(" #n ")" ::: "memory")
; #define PG8_WAIT_L(n) asm volatile("s_waitcnt lgkmcnt(" #n ")" ::: "memory")
; #define PG8_BAR __builtin_amdgcn_s_barrier()
; #define PG8_SCHED __builtin_amdgcn_sched_barrier(0)
; template <class Epi, class Sched, bool ALIGN_EPI = false, bool SP2 = false>
; __device__ __forceinline__ void gemm_phase(PG8_LAS unsigned char* lds, const Gemm g, const Sched& S, const Epi& E) {
;     ...
;             PG8_LDA(At, 1, 1); PG8_STAGE(PG8_SB(1, 0), b3, voffB); PG8_STAGE(PG8_SB(1, 1), b3 + hstep, voffB); PG8_STAGE(PG8_SA(1, 0), a3, voffA);
;             PG8_WAIT_V(8); PG8_WAIT_L(0); PG8_BAR; PG8_MMA(1, 0, At, B0); PG8_MMA(1, 1, At, B1); PG8_BAR; PG8_SCHED;
;     ...
;         if constexpr (ALIGN_EPI) { if (wr == 0) PG8_BAR; }
	s_add_i32 s30, s43, s2
	v_lshl_add_u64 v[186:187], v[186:187], 0, s[12:13]
	s_mov_b32 m0, s30
	ds_read_b128 v[194:197], v161 offset:49152
	ds_read_b128 v[198:201], v161 offset:50176
	ds_read_b128 v[202:205], v161 offset:51200
	ds_read_b128 v[206:209], v161 offset:52224
	ds_read_b128 v[210:213], v161 offset:53248
	ds_read_b128 v[214:217], v161 offset:54272
	ds_read_b128 v[218:221], v161 offset:55296
	ds_read_b128 v[222:225], v161 offset:56320
	global_load_lds_dwordx4 v[186:187], off
	s_add_i32 m0, s30, 0x2000
	s_add_u32 s28, s28, 0x80080
	v_lshl_add_u64 v[186:187], v[226:227], 0, s[12:13]
	s_addc_u32 s29, s29, 0
	s_add_i32 s30, s44, s2
	global_load_lds_dwordx4 v[186:187], off
	s_mov_b32 m0, s30
	v_lshl_add_u64 v[186:187], s[28:29], 0, v[132:133]
	global_load_lds_dwordx4 v[186:187], off
	s_add_i32 m0, s30, 0x2000
	v_lshl_add_u64 v[186:187], s[28:29], 0, v[136:137]
	global_load_lds_dwordx4 v[186:187], off
	s_mov_b32 m0, s34
	v_lshl_add_u64 v[186:187], v[228:229], 0, s[12:13]
	global_load_lds_dwordx4 v[186:187], off
	s_mov_b32 m0, s35
	v_lshl_add_u64 v[186:187], v[230:231], 0, s[12:13]
	global_load_lds_dwordx4 v[186:187], off
	s_waitcnt vmcnt(8)
	s_waitcnt lgkmcnt(0)
	s_barrier
	s_setprio 1
	s_waitcnt lgkmcnt(0)
	v_mfma_f32_16x16x32_bf16 v[62:65], v[148:151], v[194:197], v[62:65]
	v_mfma_f32_16x16x32_bf16 v[58:61], v[166:169], v[194:197], v[58:61]
	v_mfma_f32_16x16x32_bf16 v[46:49], v[148:151], v[202:205], v[46:49]
	v_mfma_f32_16x16x32_bf16 v[42:45], v[166:169], v[202:205], v[42:45]
	v_mfma_f32_16x16x32_bf16 v[30:33], v[148:151], v[210:213], v[30:33]
	v_mfma_f32_16x16x32_bf16 v[26:29], v[166:169], v[210:213], v[26:29]
	v_mfma_f32_16x16x32_bf16 v[14:17], v[148:151], v[218:221], v[14:17]
	v_mfma_f32_16x16x32_bf16 v[10:13], v[166:169], v[218:221], v[10:13]
	v_mfma_f32_16x16x32_bf16 v[62:65], v[152:155], v[198:201], v[62:65]
	v_mfma_f32_16x16x32_bf16 v[58:61], v[170:173], v[198:201], v[58:61]
	v_mfma_f32_16x16x32_bf16 v[46:49], v[152:155], v[206:209], v[46:49]
	v_mfma_f32_16x16x32_bf16 v[42:45], v[170:173], v[206:209], v[42:45]
	v_mfma_f32_16x16x32_bf16 v[30:33], v[152:155], v[214:217], v[30:33]
	v_mfma_f32_16x16x32_bf16 v[26:29], v[170:173], v[214:217], v[26:29]
	v_mfma_f32_16x16x32_bf16 v[14:17], v[152:155], v[222:225], v[14:17]
	v_mfma_f32_16x16x32_bf16 v[10:13], v[170:173], v[222:225], v[10:13]
	v_mfma_f32_16x16x32_bf16 v[54:57], v[174:177], v[194:197], v[54:57]
	v_mfma_f32_16x16x32_bf16 v[50:53], v[182:185], v[194:197], v[50:53]
	v_mfma_f32_16x16x32_bf16 v[38:41], v[174:177], v[202:205], v[38:41]
	v_mfma_f32_16x16x32_bf16 v[34:37], v[182:185], v[202:205], v[34:37]
	v_mfma_f32_16x16x32_bf16 v[22:25], v[174:177], v[210:213], v[22:25]
	v_mfma_f32_16x16x32_bf16 v[18:21], v[182:185], v[210:213], v[18:21]
	v_mfma_f32_16x16x32_bf16 v[6:9], v[174:177], v[218:221], v[6:9]
	v_mfma_f32_16x16x32_bf16 v[2:5], v[182:185], v[218:221], v[2:5]
	v_mfma_f32_16x16x32_bf16 v[54:57], v[178:181], v[198:201], v[54:57]
	v_mfma_f32_16x16x32_bf16 v[50:53], v[190:193], v[198:201], v[50:53]
	v_mfma_f32_16x16x32_bf16 v[38:41], v[178:181], v[206:209], v[38:41]
	v_mfma_f32_16x16x32_bf16 v[34:37], v[190:193], v[206:209], v[34:37]
	v_mfma_f32_16x16x32_bf16 v[22:25], v[178:181], v[214:217], v[22:25]
	v_mfma_f32_16x16x32_bf16 v[18:21], v[190:193], v[214:217], v[18:21]
	v_mfma_f32_16x16x32_bf16 v[6:9], v[178:181], v[222:225], v[6:9]
	v_mfma_f32_16x16x32_bf16 v[2:5], v[190:193], v[222:225], v[2:5]
	s_setprio 0
	s_barrier
	s_add_i32 s42, s42, 2
	s_add_u32 s26, s26, 0x100
	s_addc_u32 s27, s27, 0
	s_add_u32 s40, s40, 0x100
	s_addc_u32 s41, s41, 0
	s_cmp_gt_u32 s42, 29
	s_cbranch_scc0 .LBB0_1350
	s_and_b64 vcc, exec, s[14:15]
	s_cbranch_vccz .LBB0_1353
	s_barrier

; #define PG8_STAGE(bufoff, gbase, voff) do { _Pragma("unroll") for (int _i = 0; _i < 2; ++_i) \
;         __builtin_amdgcn_global_load_lds((const unsigned*)((const char*)(gbase) + (voff)[_i]), (PG8_LAS unsigned*)(lds + (bufoff) + ldsw + _i * 8192), 16, 0, 0); } while (0)
; #define PG8_LDA(dst, b, h) do { _Pragma("unroll") for (int m = 0; m < 4; ++m) _Pragma("unroll") for (int k = 0; k < 2; ++k) dst[m][k] = *(const PG8_LAS bf16x8*)(lds + PG8_SA(b, h) + aoff + m * 2048 + k * 1024); } while (0)
; #define PG8_LDB(dst, b, h) do { _Pragma("unroll") for (int n = 0; n < 2; ++n) _Pragma("unroll") for (int k = 0; k < 2; ++k) dst[n][k] = *(const PG8_LAS bf16x8*)(lds + PG8_SB(b, h) + boff + n * 2048 + k * 1024); } while (0)
; #define PG8_MMA(ai, bj, At, Bt) do { __builtin_amdgcn_s_setprio(1); _Pragma("unroll") for (int m = 0; m < 4; ++m) _Pragma("unroll") for (int n = 0; n < 2; ++n) _Pragma("unroll") for (int k = 0; k < 2; ++k) \
;         acc[ai][bj][m][n] = __builtin_amdgcn_mfma_f32_16x16x32_bf16(Bt[n][k], At[m][k], acc[ai][bj][m][n], 0, 0, 0); __builtin_amdgcn_s_setprio(0); } while (0)
; #define PG8_WAIT_V(n) asm volatile("s_waitcnt vmcnt(" #n ")" ::: "memory")
; #define PG8_WAIT_L(n) asm volatile("s_waitcnt lgkmcnt(" #n ")" ::: "memory")
; #define PG8_BAR __builtin_amdgcn_s_barrier()
; #define PG8_SCHED __builtin_amdgcn_sched_barrier(0)
; template <class Epi, class Sched, bool ALIGN_EPI = false, bool SP2 = false>
; __device__ __forceinline__ void gemm_phase(PG8_LAS unsigned char* lds, const Gemm g, const Sched& S, const Epi& E) {
;     ...
;         for (int t = 0; t < nt; t += 2) {
;             const bool last = (t == nt - 2);
;             const char* a1 = cA + (size_t)(t + 1) * kstep;
;             const char* a2 = last ? nA : cA + (size_t)(t + 2) * kstep; const char* b2 = last ? nB : cB + (size_t)(t + 2) * kstep;
;             const char* a3 = a2 + kstep; const char* b3 = b2 + kstep;
;             if (last && has_next) S.a_ready(nxt);
;             if constexpr (SP2) {
;             PG8_LDB(B0, 0, 0); PG8_LDB(B1, 0, 1); PG8_SCHED; PG8_LDA(At, 0, 0); PG8_STAGE(PG8_SA(1, 1), a1 + hstep, voffA);
;             PG8_WAIT_V(8); PG8_WAIT_L(0); PG8_BAR; PG8_MMA(0, 0, At, B0); PG8_MMA(0, 1, At, B1); PG8_BAR; PG8_SCHED;
;             PG8_LDA(At, 0, 1); PG8_STAGE(PG8_SB(0, 0), b2, voffB); PG8_STAGE(PG8_SB(0, 1), b2 + hstep, voffB); PG8_STAGE(PG8_SA(0, 0), a2, voffA);
.LBB0_1828:
	ds_read_b128 v[144:147], v155
	ds_read_b128 v[148:151], v155 offset:1024
	ds_read_b128 v[166:169], v155 offset:2048
	ds_read_b128 v[170:173], v155 offset:3072
	ds_read_b128 v[174:177], v156
	ds_read_b128 v[178:181], v156 offset:1024
	ds_read_b128 v[182:185], v156 offset:2048
	ds_read_b128 v[190:193], v156 offset:3072
	s_add_u32 s28, s4, 0x100
	s_addc_u32 s29, s5, 0
	s_cmp_eq_u32 s47, 28
	s_cselect_b32 s35, s19, s29
	s_cselect_b32 s34, s43, s28
	s_cselect_b32 s31, s17, s46
	s_cselect_b32 s30, s44, s45
	v_lshl_add_u64 v[160:161], s[4:5], 0, v[136:137]
	s_add_i32 m0, s3, 0xc000
	ds_read_b128 v[194:197], v157
	ds_read_b128 v[198:201], v157 offset:1024
	ds_read_b128 v[202:205], v157 offset:2048
	ds_read_b128 v[206:209], v157 offset:3072
	ds_read_b128 v[210:213], v157 offset:4096
	ds_read_b128 v[214:217], v157 offset:5120
	ds_read_b128 v[218:221], v157 offset:6144
	ds_read_b128 v[222:225], v157 offset:7168
	global_load_lds_dwordx4 v[160:161], off
	s_add_i32 m0, s3, 0xe000
	v_lshl_add_u64 v[160:161], s[4:5], 0, v[138:139]
	global_load_lds_dwordx4 v[160:161], off
	s_waitcnt vmcnt(8)
	s_waitcnt lgkmcnt(0)
	s_barrier
	s_setprio 1
	s_waitcnt lgkmcnt(0)
	v_mfma_f32_16x16x32_bf16 v[126:129], v[144:147], v[194:197], v[126:129]
	v_mfma_f32_16x16x32_bf16 v[122:125], v[166:169], v[194:197], v[122:125]
	v_mfma_f32_16x16x32_bf16 v[110:113], v[144:147], v[202:205], v[110:113]
	v_mfma_f32_16x16x32_bf16 v[106:109], v[166:169], v[202:205], v[106:109]
	v_mfma_f32_16x16x32_bf16 v[94:97], v[144:147], v[210:213], v[94:97]
	v_mfma_f32_16x16x32_bf16 v[90:93], v[166:169], v[210:213], v[90:93]
	v_mfma_f32_16x16x32_bf16 v[78:81], v[144:147], v[218:221], v[78:81]
	v_mfma_f32_16x16x32_bf16 v[74:77], v[166:169], v[218:221], v[74:77]
	v_mfma_f32_16x16x32_bf16 v[126:129], v[148:151], v[198:201], v[126:129]
	v_mfma_f32_16x16x32_bf16 v[122:125], v[170:173], v[198:201], v[122:125]
	v_mfma_f32_16x16x32_bf16 v[110:113], v[148:151], v[206:209], v[110:113]
	v_mfma_f32_16x16x32_bf16 v[106:109], v[170:173], v[206:209], v[106:109]
	v_mfma_f32_16x16x32_bf16 v[94:97], v[148:151], v[214:217], v[94:97]
	v_mfma_f32_16x16x32_bf16 v[90:93], v[170:173], v[214:217], v[90:93]
	v_mfma_f32_16x16x32_bf16 v[78:81], v[148:151], v[222:225], v[78:81]
	v_mfma_f32_16x16x32_bf16 v[74:77], v[170:173], v[222:225], v[74:77]
	v_mfma_f32_16x16x32_bf16 v[118:121], v[174:177], v[194:197], v[118:121]
	v_mfma_f32_16x16x32_bf16 v[114:117], v[182:185], v[194:197], v[114:117]
	v_mfma_f32_16x16x32_bf16 v[102:105], v[174:177], v[202:205], v[102:105]
	v_mfma_f32_16x16x32_bf16 v[98:101], v[182:185], v[202:205], v[98:101]
	v_mfma_f32_16x16x32_bf16 v[86:89], v[174:177], v[210:213], v[86:89]
	v_mfma_f32_16x16x32_bf16 v[82:85], v[182:185], v[210:213], v[82:85]
	v_mfma_f32_16x16x32_bf16 v[70:73], v[174:177], v[218:221], v[70:73]
	v_mfma_f32_16x16x32_bf16 v[66:69], v[182:185], v[218:221], v[66:69]
	v_mfma_f32_16x16x32_bf16 v[118:121], v[178:181], v[198:201], v[118:121]
	v_mfma_f32_16x16x32_bf16 v[114:117], v[190:193], v[198:201], v[114:117]
	v_mfma_f32_16x16x32_bf16 v[102:105], v[178:181], v[206:209], v[102:105]
	v_mfma_f32_16x16x32_bf16 v[98:101], v[190:193], v[206:209], v[98:101]
	v_mfma_f32_16x16x32_bf16 v[86:89], v[178:181], v[214:217], v[86:89]
	v_mfma_f32_16x16x32_bf16 v[82:85], v[190:193], v[214:217], v[82:85]
	v_mfma_f32_16x16x32_bf16 v[70:73], v[178:181], v[222:225], v[70:73]
	v_mfma_f32_16x16x32_bf16 v[66:69], v[190:193], v[222:225], v[66:69]
	s_setprio 0
	s_barrier
	s_add_i32 s4, s40, s2
	v_lshl_add_u64 v[160:161], s[30:31], 0, v[130:131]
	s_mov_b32 m0, s4
	ds_read_b128 v[194:197], v157 offset:16384
	ds_read_b128 v[198:201], v157 offset:17408
	ds_read_b128 v[202:205], v157 offset:18432
	ds_read_b128 v[206:209], v157 offset:19456
	ds_read_b128 v[210:213], v157 offset:20480
	ds_read_b128 v[214:217], v157 offset:21504
	ds_read_b128 v[218:221], v157 offset:22528
	ds_read_b128 v[222:225], v157 offset:23552
	global_load_lds_dwordx4 v[160:161], off
	s_add_i32 m0, s4, 0x2000
	s_add_u32 s4, s30, 0x80000
	v_lshl_add_u64 v[186:187], s[30:31], 0, v[132:133]
	s_addc_u32 s5, s31, 0
	s_add_i32 s48, s41, s2
	global_load_lds_dwordx4 v[186:187], off
	v_lshl_add_u64 v[226:227], s[4:5], 0, v[130:131]
	s_mov_b32 m0, s48
	v_lshl_add_u64 v[228:229], s[34:35], 0, v[132:133]
	global_load_lds_dwordx4 v[226:227], off
	s_add_i32 m0, s48, 0x2000
	v_lshl_add_u64 v[226:227], s[4:5], 0, v[132:133]
	global_load_lds_dwordx4 v[226:227], off
	s_mov_b32 m0, s3
	v_lshl_add_u64 v[226:227], s[34:35], 0, v[130:131]
	global_load_lds_dwordx4 v[226:227], off
	s_mov_b32 m0, s25
	s_nop 0
	global_load_lds_dwordx4 v[228:229], off
	s_waitcnt vmcnt(8)
	s_waitcnt lgkmcnt(0)
	s_barrier
; #define PG8_STAGE(bufoff, gbase, voff) do { _Pragma("unroll") for (int _i = 0; _i < 2; ++_i) \
;         __builtin_amdgcn_global_load_lds((const unsigned*)((const char*)(gbase) + (voff)[_i]), (PG8_LAS unsigned*)(lds + (bufoff) + ldsw + _i * 8192), 16, 0, 0); } while (0)
; #define PG8_LDA(dst, b, h) do { _Pragma("unroll") for (int m = 0; m < 4; ++m) _Pragma("unroll") for (int k = 0; k < 2; ++k) dst[m][k] = *(const PG8_LAS bf16x8*)(lds + PG8_SA(b, h) + aoff + m * 2048 + k * 1024); } while (0)
; #define PG8_LDB(dst, b, h) do { _Pragma("unroll") for (int n = 0; n < 2; ++n) _Pragma("unroll") for (int k = 0; k < 2; ++k) dst[n][k] = *(const PG8_LAS bf16x8*)(lds + PG8_SB(b, h) + boff + n * 2048 + k * 1024); } while (0)
; #define PG8_MMA(ai, bj, At, Bt) do { __builtin_amdgcn_s_setprio(1); _Pragma("unroll") for (int m = 0; m < 4; ++m) _Pragma("unroll") for (int n = 0; n < 2; ++n) _Pragma("unroll") for (int k = 0; k < 2; ++k) \
;         acc[ai][bj][m][n] = __builtin_amdgcn_mfma_f32_16x16x32_bf16(Bt[n][k], At[m][k], acc[ai][bj][m][n], 0, 0, 0); __builtin_amdgcn_s_setprio(0); } while (0)
; #define PG8_WAIT_V(n) asm volatile("s_waitcnt vmcnt(" #n ")" ::: "memory")
; #define PG8_WAIT_L(n) asm volatile("s_waitcnt lgkmcnt(" #n ")" ::: "memory")
; #define PG8_BAR __builtin_amdgcn_s_barrier()
; #define PG8_SCHED __builtin_amdgcn_sched_barrier(0)
; template <class Epi, class Sched, bool ALIGN_EPI = false, bool SP2 = false>
; __device__ __forceinline__ void gemm_phase(PG8_LAS unsigned char* lds, const Gemm g, const Sched& S, const Epi& E) {
;     ...
;             PG8_WAIT_V(8); PG8_WAIT_L(0); PG8_BAR; PG8_MMA(1, 0, At, B0); PG8_MMA(1, 1, At, B1); PG8_BAR; PG8_SCHED;
;             PG8_LDB(B0, 1, 0); PG8_LDB(B1, 1, 1); PG8_SCHED; PG8_LDA(At, 1, 0); PG8_STAGE(PG8_SA(0, 1), a2 + hstep, voffA);
;             PG8_WAIT_V(8); PG8_WAIT_L(0); PG8_BAR; PG8_MMA(0, 0, At, B0); PG8_MMA(0, 1, At, B1); PG8_BAR; PG8_SCHED;
	s_setprio 1
	s_waitcnt lgkmcnt(0)
	v_mfma_f32_16x16x32_bf16 v[62:65], v[144:147], v[194:197], v[62:65]
	v_mfma_f32_16x16x32_bf16 v[58:61], v[166:169], v[194:197], v[58:61]
	v_mfma_f32_16x16x32_bf16 v[46:49], v[144:147], v[202:205], v[46:49]
	v_mfma_f32_16x16x32_bf16 v[42:45], v[166:169], v[202:205], v[42:45]
	v_mfma_f32_16x16x32_bf16 v[30:33], v[144:147], v[210:213], v[30:33]
	v_mfma_f32_16x16x32_bf16 v[26:29], v[166:169], v[210:213], v[26:29]
	v_mfma_f32_16x16x32_bf16 v[14:17], v[144:147], v[218:221], v[14:17]
	v_mfma_f32_16x16x32_bf16 v[10:13], v[166:169], v[218:221], v[10:13]
	v_mfma_f32_16x16x32_bf16 v[62:65], v[148:151], v[198:201], v[62:65]
	v_mfma_f32_16x16x32_bf16 v[58:61], v[170:173], v[198:201], v[58:61]
	v_mfma_f32_16x16x32_bf16 v[46:49], v[148:151], v[206:209], v[46:49]
	v_mfma_f32_16x16x32_bf16 v[42:45], v[170:173], v[206:209], v[42:45]
	v_mfma_f32_16x16x32_bf16 v[30:33], v[148:151], v[214:217], v[30:33]
	v_mfma_f32_16x16x32_bf16 v[26:29], v[170:173], v[214:217], v[26:29]
	v_mfma_f32_16x16x32_bf16 v[14:17], v[148:151], v[222:225], v[14:17]
	v_mfma_f32_16x16x32_bf16 v[10:13], v[170:173], v[222:225], v[10:13]
	v_mfma_f32_16x16x32_bf16 v[54:57], v[174:177], v[194:197], v[54:57]
	v_mfma_f32_16x16x32_bf16 v[50:53], v[182:185], v[194:197], v[50:53]
	v_mfma_f32_16x16x32_bf16 v[38:41], v[174:177], v[202:205], v[38:41]
	v_mfma_f32_16x16x32_bf16 v[34:37], v[182:185], v[202:205], v[34:37]
	v_mfma_f32_16x16x32_bf16 v[22:25], v[174:177], v[210:213], v[22:25]
	v_mfma_f32_16x16x32_bf16 v[18:21], v[182:185], v[210:213], v[18:21]
	v_mfma_f32_16x16x32_bf16 v[6:9], v[174:177], v[218:221], v[6:9]
	v_mfma_f32_16x16x32_bf16 v[2:5], v[182:185], v[218:221], v[2:5]
	v_mfma_f32_16x16x32_bf16 v[54:57], v[178:181], v[198:201], v[54:57]
	v_mfma_f32_16x16x32_bf16 v[50:53], v[190:193], v[198:201], v[50:53]
	v_mfma_f32_16x16x32_bf16 v[38:41], v[178:181], v[206:209], v[38:41]
	v_mfma_f32_16x16x32_bf16 v[34:37], v[190:193], v[206:209], v[34:37]
	v_mfma_f32_16x16x32_bf16 v[22:25], v[178:181], v[214:217], v[22:25]
	v_mfma_f32_16x16x32_bf16 v[18:21], v[190:193], v[214:217], v[18:21]
	v_mfma_f32_16x16x32_bf16 v[6:9], v[178:181], v[222:225], v[6:9]
	v_mfma_f32_16x16x32_bf16 v[2:5], v[190:193], v[222:225], v[2:5]
	s_setprio 0
	s_barrier
	s_add_i32 s48, 0, 0x18000
	v_add_u32_e32 v134, s48, v153
	s_add_i32 s49, 0, 0x1c000
	ds_read_b128 v[144:147], v134
	ds_read_b128 v[148:151], v134 offset:1024
	ds_read_b128 v[166:169], v134 offset:2048
	ds_read_b128 v[170:173], v134 offset:3072
	v_add_u32_e32 v134, s49, v153
	ds_read_b128 v[174:177], v134
	ds_read_b128 v[178:181], v134 offset:1024
	ds_read_b128 v[182:185], v134 offset:2048
	ds_read_b128 v[190:193], v134 offset:3072
	s_add_u32 s4, s34, 0x80000
	s_addc_u32 s5, s35, 0
	s_mov_b32 m0, s27
	v_lshl_add_u64 v[230:231], s[4:5], 0, v[130:131]
	ds_read_b128 v[194:197], v157 offset:32768
	ds_read_b128 v[198:201], v157 offset:33792
	ds_read_b128 v[202:205], v157 offset:34816
	ds_read_b128 v[206:209], v157 offset:35840
	ds_read_b128 v[210:213], v157 offset:36864
	ds_read_b128 v[214:217], v157 offset:37888
	ds_read_b128 v[218:221], v157 offset:38912
	ds_read_b128 v[222:225], v157 offset:39936
	global_load_lds_dwordx4 v[230:231], off
	s_mov_b32 m0, s33
	v_lshl_add_u64 v[230:231], s[4:5], 0, v[132:133]
	global_load_lds_dwordx4 v[230:231], off
	s_waitcnt vmcnt(8)
	s_waitcnt lgkmcnt(0)
	s_barrier
	s_setprio 1
	s_waitcnt lgkmcnt(0)
	v_mfma_f32_16x16x32_bf16 v[126:129], v[144:147], v[194:197], v[126:129]
	v_mfma_f32_16x16x32_bf16 v[122:125], v[166:169], v[194:197], v[122:125]
	v_mfma_f32_16x16x32_bf16 v[110:113], v[144:147], v[202:205], v[110:113]
	v_mfma_f32_16x16x32_bf16 v[106:109], v[166:169], v[202:205], v[106:109]
	v_mfma_f32_16x16x32_bf16 v[94:97], v[144:147], v[210:213], v[94:97]
	v_mfma_f32_16x16x32_bf16 v[90:93], v[166:169], v[210:213], v[90:93]
	v_mfma_f32_16x16x32_bf16 v[78:81], v[144:147], v[218:221], v[78:81]
	v_mfma_f32_16x16x32_bf16 v[74:77], v[166:169], v[218:221], v[74:77]
	v_mfma_f32_16x16x32_bf16 v[126:129], v[148:151], v[198:201], v[126:129]
	v_mfma_f32_16x16x32_bf16 v[122:125], v[170:173], v[198:201], v[122:125]
	v_mfma_f32_16x16x32_bf16 v[110:113], v[148:151], v[206:209], v[110:113]
	v_mfma_f32_16x16x32_bf16 v[106:109], v[170:173], v[206:209], v[106:109]
	v_mfma_f32_16x16x32_bf16 v[94:97], v[148:151], v[214:217], v[94:97]
	v_mfma_f32_16x16x32_bf16 v[90:93], v[170:173], v[214:217], v[90:93]
	v_mfma_f32_16x16x32_bf16 v[78:81], v[148:151], v[222:225], v[78:81]
	v_mfma_f32_16x16x32_bf16 v[74:77], v[170:173], v[222:225], v[74:77]
	v_mfma_f32_16x16x32_bf16 v[118:121], v[174:177], v[194:197], v[118:121]
	v_mfma_f32_16x16x32_bf16 v[114:117], v[182:185], v[194:197], v[114:117]
	v_mfma_f32_16x16x32_bf16 v[102:105], v[174:177], v[202:205], v[102:105]
	v_mfma_f32_16x16x32_bf16 v[98:101], v[182:185], v[202:205], v[98:101]
	v_mfma_f32_16x16x32_bf16 v[86:89], v[174:177], v[210:213], v[86:89]
	v_mfma_f32_16x16x32_bf16 v[82:85], v[182:185], v[210:213], v[82:85]
	v_mfma_f32_16x16x32_bf16 v[70:73], v[174:177], v[218:221], v[70:73]
	v_mfma_f32_16x16x32_bf16 v[66:69], v[182:185], v[218:221], v[66:69]
	v_mfma_f32_16x16x32_bf16 v[118:121], v[178:181], v[198:201], v[118:121]
	v_mfma_f32_16x16x32_bf16 v[114:117], v[190:193], v[198:201], v[114:117]
	v_mfma_f32_16x16x32_bf16 v[102:105], v[178:181], v[206:209], v[102:105]
	v_mfma_f32_16x16x32_bf16 v[98:101], v[190:193], v[206:209], v[98:101]
	v_mfma_f32_16x16x32_bf16 v[86:89], v[178:181], v[214:217], v[86:89]
	v_mfma_f32_16x16x32_bf16 v[82:85], v[190:193], v[214:217], v[82:85]
	v_mfma_f32_16x16x32_bf16 v[70:73], v[178:181], v[222:225], v[70:73]
	v_mfma_f32_16x16x32_bf16 v[66:69], v[190:193], v[222:225], v[66:69]
	s_setprio 0
	s_barrier
; #define PG8_STAGE(bufoff, gbase, voff) do { _Pragma("unroll") for (int _i = 0; _i < 2; ++_i) \
;         __builtin_amdgcn_global_load_lds((const unsigned*)((const char*)(gbase) + (voff)[_i]), (PG8_LAS unsigned*)(lds + (bufoff) + ldsw + _i * 8192), 16, 0, 0); } while (0)
; #define PG8_LDA(dst, b, h) do { _Pragma("unroll") for (int m = 0; m < 4; ++m) _Pragma("unroll") for (int k = 0; k < 2; ++k) dst[m][k] = *(const PG8_LAS bf16x8*)(lds + PG8_SA(b, h) + aoff + m * 2048 + k * 1024); } while (0)
; #define PG8_MMA(ai, bj, At, Bt) do { __builtin_amdgcn_s_setprio(1); _Pragma("unroll") for (int m = 0; m < 4; ++m) _Pragma("unroll") for (int n = 0; n < 2; ++n) _Pragma("unroll") for (int k = 0; k < 2; ++k) \
;         acc[ai][bj][m][n] = __builtin_amdgcn_mfma_f32_16x16x32_bf16(Bt[n][k], At[m][k], acc[ai][bj][m][n], 0, 0, 0); __builtin_amdgcn_s_setprio(0); } while (0)
; #define PG8_WAIT_V(n) asm volatile("s_waitcnt vmcnt(" #n ")" ::: "memory")
; #define PG8_WAIT_L(n) asm volatile("s_waitcnt lgkmcnt(" #n ")" ::: "memory")
; #define PG8_BAR __builtin_amdgcn_s_barrier()
; #define PG8_SCHED __builtin_amdgcn_sched_barrier(0)
; template <class Epi, class Sched, bool ALIGN_EPI = false, bool SP2 = false>
; __device__ __forceinline__ void gemm_phase(PG8_LAS unsigned char* lds, const Gemm g, const Sched& S, const Epi& E) {
;     ...
;             PG8_LDA(At, 1, 1); PG8_STAGE(PG8_SB(1, 0), b3, voffB); PG8_STAGE(PG8_SB(1, 1), b3 + hstep, voffB); PG8_STAGE(PG8_SA(1, 0), a3, voffA);
;             PG8_WAIT_V(8); PG8_WAIT_L(0); PG8_BAR; PG8_MMA(1, 0, At, B0); PG8_MMA(1, 1, At, B1); PG8_BAR; PG8_SCHED;
;     ...
;         if constexpr (ALIGN_EPI) { if (wr == 0) PG8_BAR; }
	s_add_i32 s4, s48, s2
	v_lshl_add_u64 v[160:161], v[160:161], 0, s[12:13]
	s_mov_b32 m0, s4
	ds_read_b128 v[194:197], v157 offset:49152
	ds_read_b128 v[198:201], v157 offset:50176
	ds_read_b128 v[202:205], v157 offset:51200
	ds_read_b128 v[206:209], v157 offset:52224
	ds_read_b128 v[210:213], v157 offset:53248
	ds_read_b128 v[214:217], v157 offset:54272
	ds_read_b128 v[218:221], v157 offset:55296
	ds_read_b128 v[222:225], v157 offset:56320
	global_load_lds_dwordx4 v[160:161], off
	s_add_i32 m0, s4, 0x2000
	s_add_u32 s4, s30, 0x80080
	v_lshl_add_u64 v[160:161], v[186:187], 0, s[12:13]
	s_addc_u32 s5, s31, 0
	s_add_i32 s30, s49, s2
	global_load_lds_dwordx4 v[160:161], off
	s_mov_b32 m0, s30
	v_lshl_add_u64 v[160:161], s[4:5], 0, v[130:131]
	global_load_lds_dwordx4 v[160:161], off
	s_add_i32 m0, s30, 0x2000
	v_lshl_add_u64 v[160:161], s[4:5], 0, v[132:133]
	global_load_lds_dwordx4 v[160:161], off
	s_mov_b32 m0, s38
	v_lshl_add_u64 v[160:161], v[226:227], 0, s[12:13]
	global_load_lds_dwordx4 v[160:161], off
	s_mov_b32 m0, s39
	v_lshl_add_u64 v[160:161], v[228:229], 0, s[12:13]
	global_load_lds_dwordx4 v[160:161], off
	s_waitcnt vmcnt(8)
	s_waitcnt lgkmcnt(0)
	s_barrier
	s_setprio 1
	s_waitcnt lgkmcnt(0)
	v_mfma_f32_16x16x32_bf16 v[62:65], v[144:147], v[194:197], v[62:65]
	v_mfma_f32_16x16x32_bf16 v[58:61], v[166:169], v[194:197], v[58:61]
	v_mfma_f32_16x16x32_bf16 v[46:49], v[144:147], v[202:205], v[46:49]
	v_mfma_f32_16x16x32_bf16 v[42:45], v[166:169], v[202:205], v[42:45]
	v_mfma_f32_16x16x32_bf16 v[30:33], v[144:147], v[210:213], v[30:33]
	v_mfma_f32_16x16x32_bf16 v[26:29], v[166:169], v[210:213], v[26:29]
	v_mfma_f32_16x16x32_bf16 v[14:17], v[144:147], v[218:221], v[14:17]
	v_mfma_f32_16x16x32_bf16 v[10:13], v[166:169], v[218:221], v[10:13]
	v_mfma_f32_16x16x32_bf16 v[62:65], v[148:151], v[198:201], v[62:65]
	v_mfma_f32_16x16x32_bf16 v[58:61], v[170:173], v[198:201], v[58:61]
	v_mfma_f32_16x16x32_bf16 v[46:49], v[148:151], v[206:209], v[46:49]
	v_mfma_f32_16x16x32_bf16 v[42:45], v[170:173], v[206:209], v[42:45]
	v_mfma_f32_16x16x32_bf16 v[30:33], v[148:151], v[214:217], v[30:33]
	v_mfma_f32_16x16x32_bf16 v[26:29], v[170:173], v[214:217], v[26:29]
	v_mfma_f32_16x16x32_bf16 v[14:17], v[148:151], v[222:225], v[14:17]
	v_mfma_f32_16x16x32_bf16 v[10:13], v[170:173], v[222:225], v[10:13]
	v_mfma_f32_16x16x32_bf16 v[54:57], v[174:177], v[194:197], v[54:57]
	v_mfma_f32_16x16x32_bf16 v[50:53], v[182:185], v[194:197], v[50:53]
	v_mfma_f32_16x16x32_bf16 v[38:41], v[174:177], v[202:205], v[38:41]
	v_mfma_f32_16x16x32_bf16 v[34:37], v[182:185], v[202:205], v[34:37]
	v_mfma_f32_16x16x32_bf16 v[22:25], v[174:177], v[210:213], v[22:25]
	v_mfma_f32_16x16x32_bf16 v[18:21], v[182:185], v[210:213], v[18:21]
	v_mfma_f32_16x16x32_bf16 v[6:9], v[174:177], v[218:221], v[6:9]
	v_mfma_f32_16x16x32_bf16 v[2:5], v[182:185], v[218:221], v[2:5]
	v_mfma_f32_16x16x32_bf16 v[54:57], v[178:181], v[198:201], v[54:57]
	v_mfma_f32_16x16x32_bf16 v[50:53], v[190:193], v[198:201], v[50:53]
	v_mfma_f32_16x16x32_bf16 v[38:41], v[178:181], v[206:209], v[38:41]
	v_mfma_f32_16x16x32_bf16 v[34:37], v[190:193], v[206:209], v[34:37]
	v_mfma_f32_16x16x32_bf16 v[22:25], v[178:181], v[214:217], v[22:25]
	v_mfma_f32_16x16x32_bf16 v[18:21], v[190:193], v[214:217], v[18:21]
	v_mfma_f32_16x16x32_bf16 v[6:9], v[178:181], v[222:225], v[6:9]
	v_mfma_f32_16x16x32_bf16 v[2:5], v[190:193], v[222:225], v[2:5]
	s_setprio 0
	s_barrier
	s_add_i32 s47, s47, 2
	s_add_u32 s45, s45, 0x100
	s_addc_u32 s46, s46, 0
	s_cmp_gt_u32 s47, 29
	s_mov_b64 s[4:5], s[28:29]
	s_cbranch_scc0 .LBB0_1828
	s_and_b64 vcc, exec, s[14:15]
	s_cbranch_vccz .LBB0_1831
	s_barrier

; #define PG8_STAGE(bufoff, gbase, voff) do { _Pragma("unroll") for (int _i = 0; _i < 2; ++_i) \
;         __builtin_amdgcn_global_load_lds((const unsigned*)((const char*)(gbase) + (voff)[_i]), (PG8_LAS unsigned*)(lds + (bufoff) + ldsw + _i * 8192), 16, 0, 0); } while (0)
; #define PG8_LDA(dst, b, h) do { _Pragma("unroll") for (int m = 0; m < 4; ++m) _Pragma("unroll") for (int k = 0; k < 2; ++k) dst[m][k] = *(const PG8_LAS bf16x8*)(lds + PG8_SA(b, h) + aoff + m * 2048 + k * 1024); } while (0)
; #define PG8_LDB(dst, b, h) do { _Pragma("unroll") for (int n = 0; n < 2; ++n) _Pragma("unroll") for (int k = 0; k < 2; ++k) dst[n][k] = *(const PG8_LAS bf16x8*)(lds + PG8_SB(b, h) + boff + n * 2048 + k * 1024); } while (0)
; #define PG8_MMA(ai, bj, At, Bt) do { __builtin_amdgcn_s_setprio(1); _Pragma("unroll") for (int m = 0; m < 4; ++m) _Pragma("unroll") for (int n = 0; n < 2; ++n) _Pragma("unroll") for (int k = 0; k < 2; ++k) \
;         acc[ai][bj][m][n] = __builtin_amdgcn_mfma_f32_16x16x32_bf16(Bt[n][k], At[m][k], acc[ai][bj][m][n], 0, 0, 0); __builtin_amdgcn_s_setprio(0); } while (0)
; #define PG8_BAR __builtin_amdgcn_s_barrier()
; template <class Epi, class Sched, bool ALIGN_EPI = false, bool SP2 = false>
; __device__ __forceinline__ void gemm_phase(PG8_LAS unsigned char* lds, const Gemm g, const Sched& S, const Epi& E) {
;     ...
;         const char* nA = has_next ? (const char*)g.A + (size_t)nxt.pm * tstep + (size_t)nxt.k0 * 2 : cA; const char* nB = has_next ? (const char*)g.Bt + (size_t)nxt.pn * tstep + (size_t)nxt.k0 * 2 : cB;
;         for (int t = 0; t < nt; t += 2) {
;             const bool last = (t == nt - 2);
;             const char* a1 = cA + (size_t)(t + 1) * kstep;
;             const char* a2 = last ? nA : cA + (size_t)(t + 2) * kstep; const char* b2 = last ? nB : cB + (size_t)(t + 2) * kstep;
;             const char* a3 = a2 + kstep; const char* b3 = b2 + kstep;
;             if (last && has_next) S.a_ready(nxt);
;             if constexpr (SP2) {
;             PG8_LDB(B0, 0, 0); PG8_LDB(B1, 0, 1); PG8_SCHED; PG8_LDA(At, 0, 0); PG8_STAGE(PG8_SA(1, 1), a1 + hstep, voffA);
;             PG8_WAIT_V(8); PG8_WAIT_L(0); PG8_BAR; PG8_MMA(0, 0, At, B0); PG8_MMA(0, 1, At, B1); PG8_BAR; PG8_SCHED;
;             PG8_LDA(At, 0, 1); PG8_STAGE(PG8_SB(0, 0), b2, voffB); PG8_STAGE(PG8_SB(0, 1), b2 + hstep, voffB); PG8_STAGE(PG8_SA(0, 0), a2, voffA);
.LBB0_2172:
	ds_read_b128 v[144:147], v150
	ds_read_b128 v[154:157], v150 offset:1024
	ds_read_b128 v[158:161], v150 offset:2048
	ds_read_b128 v[162:165], v150 offset:3072
	ds_read_b128 v[166:169], v151
	ds_read_b128 v[170:173], v151 offset:1024
	ds_read_b128 v[174:177], v151 offset:2048
	ds_read_b128 v[178:181], v151 offset:3072
	s_add_u32 s24, s22, 0xfff80080
	s_addc_u32 s25, s23, -1
	s_cmp_eq_u32 s45, 28
	s_cselect_b32 s27, s11, s25
	s_cselect_b32 s26, s41, s24
	s_cselect_b32 s25, s13, s44
	s_cselect_b32 s24, s42, s43
	v_lshl_add_u64 v[214:215], s[22:23], 0, v[138:139]
	s_add_i32 m0, s19, 0xc000
	ds_read_b128 v[182:185], v152
	ds_read_b128 v[186:189], v152 offset:1024
	ds_read_b128 v[190:193], v152 offset:2048
	ds_read_b128 v[194:197], v152 offset:3072
	ds_read_b128 v[198:201], v152 offset:4096
	ds_read_b128 v[202:205], v152 offset:5120
	ds_read_b128 v[206:209], v152 offset:6144
	ds_read_b128 v[210:213], v152 offset:7168
	global_load_lds_dwordx4 v[214:215], off
	s_add_i32 m0, s19, 0xe000
	v_lshl_add_u64 v[214:215], s[22:23], 0, v[140:141]
	global_load_lds_dwordx4 v[214:215], off
	s_waitcnt vmcnt(8)
	s_waitcnt lgkmcnt(0)
	s_barrier
	s_setprio 1
	s_waitcnt lgkmcnt(0)
	v_mfma_f32_16x16x32_bf16 v[126:129], v[144:147], v[182:185], v[126:129]
	v_mfma_f32_16x16x32_bf16 v[118:121], v[158:161], v[182:185], v[118:121]
	v_mfma_f32_16x16x32_bf16 v[110:113], v[144:147], v[190:193], v[110:113]
	v_mfma_f32_16x16x32_bf16 v[102:105], v[158:161], v[190:193], v[102:105]
	v_mfma_f32_16x16x32_bf16 v[94:97], v[144:147], v[198:201], v[94:97]
	v_mfma_f32_16x16x32_bf16 v[86:89], v[158:161], v[198:201], v[86:89]
	v_mfma_f32_16x16x32_bf16 v[78:81], v[144:147], v[206:209], v[78:81]
	v_mfma_f32_16x16x32_bf16 v[70:73], v[158:161], v[206:209], v[70:73]
	v_mfma_f32_16x16x32_bf16 v[126:129], v[154:157], v[186:189], v[126:129]
	v_mfma_f32_16x16x32_bf16 v[118:121], v[162:165], v[186:189], v[118:121]
	v_mfma_f32_16x16x32_bf16 v[110:113], v[154:157], v[194:197], v[110:113]
	v_mfma_f32_16x16x32_bf16 v[102:105], v[162:165], v[194:197], v[102:105]
	v_mfma_f32_16x16x32_bf16 v[94:97], v[154:157], v[202:205], v[94:97]
	v_mfma_f32_16x16x32_bf16 v[86:89], v[162:165], v[202:205], v[86:89]
	v_mfma_f32_16x16x32_bf16 v[78:81], v[154:157], v[210:213], v[78:81]
	v_mfma_f32_16x16x32_bf16 v[70:73], v[162:165], v[210:213], v[70:73]
	v_mfma_f32_16x16x32_bf16 v[122:125], v[166:169], v[182:185], v[122:125]
	v_mfma_f32_16x16x32_bf16 v[114:117], v[174:177], v[182:185], v[114:117]
	v_mfma_f32_16x16x32_bf16 v[106:109], v[166:169], v[190:193], v[106:109]
	v_mfma_f32_16x16x32_bf16 v[98:101], v[174:177], v[190:193], v[98:101]
	v_mfma_f32_16x16x32_bf16 v[90:93], v[166:169], v[198:201], v[90:93]
	v_mfma_f32_16x16x32_bf16 v[82:85], v[174:177], v[198:201], v[82:85]
	v_mfma_f32_16x16x32_bf16 v[74:77], v[166:169], v[206:209], v[74:77]
	v_mfma_f32_16x16x32_bf16 v[66:69], v[174:177], v[206:209], v[66:69]
	v_mfma_f32_16x16x32_bf16 v[122:125], v[170:173], v[186:189], v[122:125]
	v_mfma_f32_16x16x32_bf16 v[114:117], v[178:181], v[186:189], v[114:117]
	v_mfma_f32_16x16x32_bf16 v[106:109], v[170:173], v[194:197], v[106:109]
	v_mfma_f32_16x16x32_bf16 v[98:101], v[178:181], v[194:197], v[98:101]
	v_mfma_f32_16x16x32_bf16 v[90:93], v[170:173], v[202:205], v[90:93]
	v_mfma_f32_16x16x32_bf16 v[82:85], v[178:181], v[202:205], v[82:85]
	v_mfma_f32_16x16x32_bf16 v[74:77], v[170:173], v[210:213], v[74:77]
	v_mfma_f32_16x16x32_bf16 v[66:69], v[178:181], v[210:213], v[66:69]
	s_setprio 0
	s_barrier
	s_add_i32 s46, s38, s3
	v_lshl_add_u64 v[214:215], s[24:25], 0, v[130:131]
	s_mov_b32 m0, s46
	ds_read_b128 v[182:185], v152 offset:16384
	ds_read_b128 v[186:189], v152 offset:17408
	ds_read_b128 v[190:193], v152 offset:18432
	ds_read_b128 v[194:197], v152 offset:19456
	ds_read_b128 v[198:201], v152 offset:20480
	ds_read_b128 v[202:205], v152 offset:21504
	ds_read_b128 v[206:209], v152 offset:22528
	ds_read_b128 v[210:213], v152 offset:23552
	global_load_lds_dwordx4 v[214:215], off
	s_add_i32 m0, s46, 0x2000
	s_add_u32 s46, s24, 0x80000
	v_lshl_add_u64 v[216:217], s[24:25], 0, v[134:135]
	s_addc_u32 s47, s25, 0
	s_add_i32 s48, s39, s3
	global_load_lds_dwordx4 v[216:217], off
	v_lshl_add_u64 v[218:219], s[46:47], 0, v[130:131]
	s_mov_b32 m0, s48
	v_lshl_add_u64 v[220:221], s[26:27], 0, v[136:137]
	global_load_lds_dwordx4 v[218:219], off
	s_add_i32 m0, s48, 0x2000
	v_lshl_add_u64 v[218:219], s[46:47], 0, v[134:135]
	global_load_lds_dwordx4 v[218:219], off
	s_mov_b32 m0, s19
	v_lshl_add_u64 v[218:219], s[26:27], 0, v[132:133]
	global_load_lds_dwordx4 v[218:219], off
	s_mov_b32 m0, s21
	s_nop 0
	global_load_lds_dwordx4 v[220:221], off
	s_waitcnt vmcnt(8)
	s_waitcnt lgkmcnt(0)
	s_barrier
; #define PG8_STAGE(bufoff, gbase, voff) do { _Pragma("unroll") for (int _i = 0; _i < 2; ++_i) \
;         __builtin_amdgcn_global_load_lds((const unsigned*)((const char*)(gbase) + (voff)[_i]), (PG8_LAS unsigned*)(lds + (bufoff) + ldsw + _i * 8192), 16, 0, 0); } while (0)
; #define PG8_LDA(dst, b, h) do { _Pragma("unroll") for (int m = 0; m < 4; ++m) _Pragma("unroll") for (int k = 0; k < 2; ++k) dst[m][k] = *(const PG8_LAS bf16x8*)(lds + PG8_SA(b, h) + aoff + m * 2048 + k * 1024); } while (0)
; #define PG8_LDB(dst, b, h) do { _Pragma("unroll") for (int n = 0; n < 2; ++n) _Pragma("unroll") for (int k = 0; k < 2; ++k) dst[n][k] = *(const PG8_LAS bf16x8*)(lds + PG8_SB(b, h) + boff + n * 2048 + k * 1024); } while (0)
; #define PG8_MMA(ai, bj, At, Bt) do { __builtin_amdgcn_s_setprio(1); _Pragma("unroll") for (int m = 0; m < 4; ++m) _Pragma("unroll") for (int n = 0; n < 2; ++n) _Pragma("unroll") for (int k = 0; k < 2; ++k) \
;         acc[ai][bj][m][n] = __builtin_amdgcn_mfma_f32_16x16x32_bf16(Bt[n][k], At[m][k], acc[ai][bj][m][n], 0, 0, 0); __builtin_amdgcn_s_setprio(0); } while (0)
; #define PG8_WAIT_V(n) asm volatile("s_waitcnt vmcnt(" #n ")" ::: "memory")
; #define PG8_WAIT_L(n) asm volatile("s_waitcnt lgkmcnt(" #n ")" ::: "memory")
; #define PG8_BAR __builtin_amdgcn_s_barrier()
; #define PG8_SCHED __builtin_amdgcn_sched_barrier(0)
; template <class Epi, class Sched, bool ALIGN_EPI = false, bool SP2 = false>
; __device__ __forceinline__ void gemm_phase(PG8_LAS unsigned char* lds, const Gemm g, const Sched& S, const Epi& E) {
;     ...
;             PG8_WAIT_V(8); PG8_WAIT_L(0); PG8_BAR; PG8_MMA(1, 0, At, B0); PG8_MMA(1, 1, At, B1); PG8_BAR; PG8_SCHED;
;             PG8_LDB(B0, 1, 0); PG8_LDB(B1, 1, 1); PG8_SCHED; PG8_LDA(At, 1, 0); PG8_STAGE(PG8_SA(0, 1), a2 + hstep, voffA);
;             PG8_WAIT_V(8); PG8_WAIT_L(0); PG8_BAR; PG8_MMA(0, 0, At, B0); PG8_MMA(0, 1, At, B1); PG8_BAR; PG8_SCHED;
	s_setprio 1
	s_waitcnt lgkmcnt(0)
	v_mfma_f32_16x16x32_bf16 v[62:65], v[144:147], v[182:185], v[62:65]
	v_mfma_f32_16x16x32_bf16 v[54:57], v[158:161], v[182:185], v[54:57]
	v_mfma_f32_16x16x32_bf16 v[46:49], v[144:147], v[190:193], v[46:49]
	v_mfma_f32_16x16x32_bf16 v[38:41], v[158:161], v[190:193], v[38:41]
	v_mfma_f32_16x16x32_bf16 v[30:33], v[144:147], v[198:201], v[30:33]
	v_mfma_f32_16x16x32_bf16 v[22:25], v[158:161], v[198:201], v[22:25]
	v_mfma_f32_16x16x32_bf16 v[14:17], v[144:147], v[206:209], v[14:17]
	v_mfma_f32_16x16x32_bf16 v[6:9], v[158:161], v[206:209], v[6:9]
	v_mfma_f32_16x16x32_bf16 v[62:65], v[154:157], v[186:189], v[62:65]
	v_mfma_f32_16x16x32_bf16 v[54:57], v[162:165], v[186:189], v[54:57]
	v_mfma_f32_16x16x32_bf16 v[46:49], v[154:157], v[194:197], v[46:49]
	v_mfma_f32_16x16x32_bf16 v[38:41], v[162:165], v[194:197], v[38:41]
	v_mfma_f32_16x16x32_bf16 v[30:33], v[154:157], v[202:205], v[30:33]
	v_mfma_f32_16x16x32_bf16 v[22:25], v[162:165], v[202:205], v[22:25]
	v_mfma_f32_16x16x32_bf16 v[14:17], v[154:157], v[210:213], v[14:17]
	v_mfma_f32_16x16x32_bf16 v[6:9], v[162:165], v[210:213], v[6:9]
	v_mfma_f32_16x16x32_bf16 v[58:61], v[166:169], v[182:185], v[58:61]
	v_mfma_f32_16x16x32_bf16 v[50:53], v[174:177], v[182:185], v[50:53]
	v_mfma_f32_16x16x32_bf16 v[42:45], v[166:169], v[190:193], v[42:45]
	v_mfma_f32_16x16x32_bf16 v[34:37], v[174:177], v[190:193], v[34:37]
	v_mfma_f32_16x16x32_bf16 v[26:29], v[166:169], v[198:201], v[26:29]
	v_mfma_f32_16x16x32_bf16 v[18:21], v[174:177], v[198:201], v[18:21]
	v_mfma_f32_16x16x32_bf16 v[10:13], v[166:169], v[206:209], v[10:13]
	v_mfma_f32_16x16x32_bf16 v[2:5], v[174:177], v[206:209], v[2:5]
	v_mfma_f32_16x16x32_bf16 v[58:61], v[170:173], v[186:189], v[58:61]
	v_mfma_f32_16x16x32_bf16 v[50:53], v[178:181], v[186:189], v[50:53]
	v_mfma_f32_16x16x32_bf16 v[42:45], v[170:173], v[194:197], v[42:45]
	v_mfma_f32_16x16x32_bf16 v[34:37], v[178:181], v[194:197], v[34:37]
	v_mfma_f32_16x16x32_bf16 v[26:29], v[170:173], v[202:205], v[26:29]
	v_mfma_f32_16x16x32_bf16 v[18:21], v[178:181], v[202:205], v[18:21]
	v_mfma_f32_16x16x32_bf16 v[10:13], v[170:173], v[210:213], v[10:13]
	v_mfma_f32_16x16x32_bf16 v[2:5], v[178:181], v[210:213], v[2:5]
	s_setprio 0
	s_barrier
	s_add_i32 s46, 0, 0x18000
	v_add_u32_e32 v153, s46, v148
	s_add_i32 s47, 0, 0x1c000
	ds_read_b128 v[144:147], v153
	ds_read_b128 v[154:157], v153 offset:1024
	ds_read_b128 v[158:161], v153 offset:2048
	ds_read_b128 v[162:165], v153 offset:3072
	v_add_u32_e32 v153, s47, v148
	ds_read_b128 v[166:169], v153
	ds_read_b128 v[170:173], v153 offset:1024
	ds_read_b128 v[174:177], v153 offset:2048
	ds_read_b128 v[178:181], v153 offset:3072
	s_add_u32 s26, s26, 0x80000
	s_addc_u32 s27, s27, 0
	s_mov_b32 m0, s33
	v_lshl_add_u64 v[222:223], s[26:27], 0, v[132:133]
	ds_read_b128 v[182:185], v152 offset:32768
	ds_read_b128 v[186:189], v152 offset:33792
	ds_read_b128 v[190:193], v152 offset:34816
	ds_read_b128 v[194:197], v152 offset:35840
	ds_read_b128 v[198:201], v152 offset:36864
	ds_read_b128 v[202:205], v152 offset:37888
	ds_read_b128 v[206:209], v152 offset:38912
	ds_read_b128 v[210:213], v152 offset:39936
	global_load_lds_dwordx4 v[222:223], off
	s_mov_b32 m0, s34
	v_lshl_add_u64 v[222:223], s[26:27], 0, v[136:137]
	global_load_lds_dwordx4 v[222:223], off
	s_waitcnt vmcnt(8)
	s_waitcnt lgkmcnt(0)
	s_barrier
	s_setprio 1
	s_waitcnt lgkmcnt(0)
	v_mfma_f32_16x16x32_bf16 v[126:129], v[144:147], v[182:185], v[126:129]
	v_mfma_f32_16x16x32_bf16 v[118:121], v[158:161], v[182:185], v[118:121]
	v_mfma_f32_16x16x32_bf16 v[110:113], v[144:147], v[190:193], v[110:113]
	v_mfma_f32_16x16x32_bf16 v[102:105], v[158:161], v[190:193], v[102:105]
	v_mfma_f32_16x16x32_bf16 v[94:97], v[144:147], v[198:201], v[94:97]
	v_mfma_f32_16x16x32_bf16 v[86:89], v[158:161], v[198:201], v[86:89]
	v_mfma_f32_16x16x32_bf16 v[78:81], v[144:147], v[206:209], v[78:81]
	v_mfma_f32_16x16x32_bf16 v[70:73], v[158:161], v[206:209], v[70:73]
	v_mfma_f32_16x16x32_bf16 v[126:129], v[154:157], v[186:189], v[126:129]
	v_mfma_f32_16x16x32_bf16 v[118:121], v[162:165], v[186:189], v[118:121]
	v_mfma_f32_16x16x32_bf16 v[110:113], v[154:157], v[194:197], v[110:113]
	v_mfma_f32_16x16x32_bf16 v[102:105], v[162:165], v[194:197], v[102:105]
	v_mfma_f32_16x16x32_bf16 v[94:97], v[154:157], v[202:205], v[94:97]
	v_mfma_f32_16x16x32_bf16 v[86:89], v[162:165], v[202:205], v[86:89]
	v_mfma_f32_16x16x32_bf16 v[78:81], v[154:157], v[210:213], v[78:81]
	v_mfma_f32_16x16x32_bf16 v[70:73], v[162:165], v[210:213], v[70:73]
	v_mfma_f32_16x16x32_bf16 v[122:125], v[166:169], v[182:185], v[122:125]
	v_mfma_f32_16x16x32_bf16 v[114:117], v[174:177], v[182:185], v[114:117]
	v_mfma_f32_16x16x32_bf16 v[106:109], v[166:169], v[190:193], v[106:109]
	v_mfma_f32_16x16x32_bf16 v[98:101], v[174:177], v[190:193], v[98:101]
	v_mfma_f32_16x16x32_bf16 v[90:93], v[166:169], v[198:201], v[90:93]
	v_mfma_f32_16x16x32_bf16 v[82:85], v[174:177], v[198:201], v[82:85]
	v_mfma_f32_16x16x32_bf16 v[74:77], v[166:169], v[206:209], v[74:77]
	v_mfma_f32_16x16x32_bf16 v[66:69], v[174:177], v[206:209], v[66:69]
	v_mfma_f32_16x16x32_bf16 v[122:125], v[170:173], v[186:189], v[122:125]
	v_mfma_f32_16x16x32_bf16 v[114:117], v[178:181], v[186:189], v[114:117]
	v_mfma_f32_16x16x32_bf16 v[106:109], v[170:173], v[194:197], v[106:109]
	v_mfma_f32_16x16x32_bf16 v[98:101], v[178:181], v[194:197], v[98:101]
	v_mfma_f32_16x16x32_bf16 v[90:93], v[170:173], v[202:205], v[90:93]
	v_mfma_f32_16x16x32_bf16 v[82:85], v[178:181], v[202:205], v[82:85]
	v_mfma_f32_16x16x32_bf16 v[74:77], v[170:173], v[210:213], v[74:77]
	v_mfma_f32_16x16x32_bf16 v[66:69], v[178:181], v[210:213], v[66:69]
	s_setprio 0
	s_barrier
; #define PG8_STAGE(bufoff, gbase, voff) do { _Pragma("unroll") for (int _i = 0; _i < 2; ++_i) \
;         __builtin_amdgcn_global_load_lds((const unsigned*)((const char*)(gbase) + (voff)[_i]), (PG8_LAS unsigned*)(lds + (bufoff) + ldsw + _i * 8192), 16, 0, 0); } while (0)
; #define PG8_LDA(dst, b, h) do { _Pragma("unroll") for (int m = 0; m < 4; ++m) _Pragma("unroll") for (int k = 0; k < 2; ++k) dst[m][k] = *(const PG8_LAS bf16x8*)(lds + PG8_SA(b, h) + aoff + m * 2048 + k * 1024); } while (0)
; #define PG8_MMA(ai, bj, At, Bt) do { __builtin_amdgcn_s_setprio(1); _Pragma("unroll") for (int m = 0; m < 4; ++m) _Pragma("unroll") for (int n = 0; n < 2; ++n) _Pragma("unroll") for (int k = 0; k < 2; ++k) \
;         acc[ai][bj][m][n] = __builtin_amdgcn_mfma_f32_16x16x32_bf16(Bt[n][k], At[m][k], acc[ai][bj][m][n], 0, 0, 0); __builtin_amdgcn_s_setprio(0); } while (0)
; #define PG8_WAIT_V(n) asm volatile("s_waitcnt vmcnt(" #n ")" ::: "memory")
; #define PG8_WAIT_L(n) asm volatile("s_waitcnt lgkmcnt(" #n ")" ::: "memory")
; #define PG8_BAR __builtin_amdgcn_s_barrier()
; #define PG8_SCHED __builtin_amdgcn_sched_barrier(0)
; template <class Epi, class Sched, bool ALIGN_EPI = false, bool SP2 = false>
; __device__ __forceinline__ void gemm_phase(PG8_LAS unsigned char* lds, const Gemm g, const Sched& S, const Epi& E) {
;     ...
;             PG8_LDA(At, 1, 1); PG8_STAGE(PG8_SB(1, 0), b3, voffB); PG8_STAGE(PG8_SB(1, 1), b3 + hstep, voffB); PG8_STAGE(PG8_SA(1, 0), a3, voffA);
;             PG8_WAIT_V(8); PG8_WAIT_L(0); PG8_BAR; PG8_MMA(1, 0, At, B0); PG8_MMA(1, 1, At, B1); PG8_BAR; PG8_SCHED;
	s_add_i32 s26, s46, s3
	v_lshl_add_u64 v[214:215], v[214:215], 0, s[6:7]
	s_mov_b32 m0, s26
	ds_read_b128 v[182:185], v152 offset:49152
	ds_read_b128 v[186:189], v152 offset:50176
	ds_read_b128 v[190:193], v152 offset:51200
	ds_read_b128 v[194:197], v152 offset:52224
	ds_read_b128 v[198:201], v152 offset:53248
	ds_read_b128 v[202:205], v152 offset:54272
	ds_read_b128 v[206:209], v152 offset:55296
	ds_read_b128 v[210:213], v152 offset:56320
	global_load_lds_dwordx4 v[214:215], off
	s_add_i32 m0, s26, 0x2000
	s_add_u32 s24, s24, 0x80080
	v_lshl_add_u64 v[214:215], v[216:217], 0, s[6:7]
	s_addc_u32 s25, s25, 0
	s_add_i32 s26, s47, s3
	global_load_lds_dwordx4 v[214:215], off
	s_mov_b32 m0, s26
	v_lshl_add_u64 v[214:215], s[24:25], 0, v[130:131]
	global_load_lds_dwordx4 v[214:215], off
	s_add_i32 m0, s26, 0x2000
	v_lshl_add_u64 v[214:215], s[24:25], 0, v[134:135]
	global_load_lds_dwordx4 v[214:215], off
	s_mov_b32 m0, s36
	v_lshl_add_u64 v[214:215], v[218:219], 0, s[6:7]
	global_load_lds_dwordx4 v[214:215], off
	s_mov_b32 m0, s37
	v_lshl_add_u64 v[214:215], v[220:221], 0, s[6:7]
	global_load_lds_dwordx4 v[214:215], off
	s_waitcnt vmcnt(8)
	s_waitcnt lgkmcnt(0)
	s_barrier
	s_setprio 1
	s_waitcnt lgkmcnt(0)
	v_mfma_f32_16x16x32_bf16 v[62:65], v[144:147], v[182:185], v[62:65]
	v_mfma_f32_16x16x32_bf16 v[54:57], v[158:161], v[182:185], v[54:57]
	v_mfma_f32_16x16x32_bf16 v[46:49], v[144:147], v[190:193], v[46:49]
	v_mfma_f32_16x16x32_bf16 v[38:41], v[158:161], v[190:193], v[38:41]
	v_mfma_f32_16x16x32_bf16 v[30:33], v[144:147], v[198:201], v[30:33]
	v_mfma_f32_16x16x32_bf16 v[22:25], v[158:161], v[198:201], v[22:25]
	v_mfma_f32_16x16x32_bf16 v[14:17], v[144:147], v[206:209], v[14:17]
	v_mfma_f32_16x16x32_bf16 v[6:9], v[158:161], v[206:209], v[6:9]
	v_mfma_f32_16x16x32_bf16 v[62:65], v[154:157], v[186:189], v[62:65]
	v_mfma_f32_16x16x32_bf16 v[54:57], v[162:165], v[186:189], v[54:57]
	v_mfma_f32_16x16x32_bf16 v[46:49], v[154:157], v[194:197], v[46:49]
	v_mfma_f32_16x16x32_bf16 v[38:41], v[162:165], v[194:197], v[38:41]
	v_mfma_f32_16x16x32_bf16 v[30:33], v[154:157], v[202:205], v[30:33]
	v_mfma_f32_16x16x32_bf16 v[22:25], v[162:165], v[202:205], v[22:25]
	v_mfma_f32_16x16x32_bf16 v[14:17], v[154:157], v[210:213], v[14:17]
	v_mfma_f32_16x16x32_bf16 v[6:9], v[162:165], v[210:213], v[6:9]
	v_mfma_f32_16x16x32_bf16 v[58:61], v[166:169], v[182:185], v[58:61]
	v_mfma_f32_16x16x32_bf16 v[50:53], v[174:177], v[182:185], v[50:53]
	v_mfma_f32_16x16x32_bf16 v[42:45], v[166:169], v[190:193], v[42:45]
	v_mfma_f32_16x16x32_bf16 v[34:37], v[174:177], v[190:193], v[34:37]
	v_mfma_f32_16x16x32_bf16 v[26:29], v[166:169], v[198:201], v[26:29]
	v_mfma_f32_16x16x32_bf16 v[18:21], v[174:177], v[198:201], v[18:21]
	v_mfma_f32_16x16x32_bf16 v[10:13], v[166:169], v[206:209], v[10:13]
	v_mfma_f32_16x16x32_bf16 v[2:5], v[174:177], v[206:209], v[2:5]
	v_mfma_f32_16x16x32_bf16 v[58:61], v[170:173], v[186:189], v[58:61]
	v_mfma_f32_16x16x32_bf16 v[50:53], v[178:181], v[186:189], v[50:53]
	v_mfma_f32_16x16x32_bf16 v[42:45], v[170:173], v[194:197], v[42:45]
	v_mfma_f32_16x16x32_bf16 v[34:37], v[178:181], v[194:197], v[34:37]
	v_mfma_f32_16x16x32_bf16 v[26:29], v[170:173], v[202:205], v[26:29]
	v_mfma_f32_16x16x32_bf16 v[18:21], v[178:181], v[202:205], v[18:21]
	v_mfma_f32_16x16x32_bf16 v[10:13], v[170:173], v[210:213], v[10:13]
	v_mfma_f32_16x16x32_bf16 v[2:5], v[178:181], v[210:213], v[2:5]
	s_setprio 0
	s_barrier
	s_add_i32 s45, s45, 2
	s_add_u32 s22, s22, 0x100
	s_addc_u32 s23, s23, 0
	s_add_u32 s43, s43, 0x100
	s_addc_u32 s44, s44, 0
	s_cmp_gt_u32 s45, 29
	s_cbranch_scc0 .LBB0_2172
	s_and_b64 vcc, exec, s[8:9]
	s_cbranch_vccz .LBB0_2175
	s_barrier

; #define PG8_STAGE(bufoff, gbase, voff) do { _Pragma("unroll") for (int _i = 0; _i < 2; ++_i) \
;         __builtin_amdgcn_global_load_lds((const unsigned*)((const char*)(gbase) + (voff)[_i]), (PG8_LAS unsigned*)(lds + (bufoff) + ldsw + _i * 8192), 16, 0, 0); } while (0)
; #define PG8_LDA(dst, b, h) do { _Pragma("unroll") for (int m = 0; m < 4; ++m) _Pragma("unroll") for (int k = 0; k < 2; ++k) dst[m][k] = *(const PG8_LAS bf16x8*)(lds + PG8_SA(b, h) + aoff + m * 2048 + k * 1024); } while (0)
; #define PG8_LDB(dst, b, h) do { _Pragma("unroll") for (int n = 0; n < 2; ++n) _Pragma("unroll") for (int k = 0; k < 2; ++k) dst[n][k] = *(const PG8_LAS bf16x8*)(lds + PG8_SB(b, h) + boff + n * 2048 + k * 1024); } while (0)
; #define PG8_MMA(ai, bj, At, Bt) do { __builtin_amdgcn_s_setprio(1); _Pragma("unroll") for (int m = 0; m < 4; ++m) _Pragma("unroll") for (int n = 0; n < 2; ++n) _Pragma("unroll") for (int k = 0; k < 2; ++k) \
;         acc[ai][bj][m][n] = __builtin_amdgcn_mfma_f32_16x16x32_bf16(Bt[n][k], At[m][k], acc[ai][bj][m][n], 0, 0, 0); __builtin_amdgcn_s_setprio(0); } while (0)
; #define PG8_BAR __builtin_amdgcn_s_barrier()
; template <class Epi, class Sched, bool ALIGN_EPI = false, bool SP2 = false>
; __device__ __forceinline__ void gemm_phase(PG8_LAS unsigned char* lds, const Gemm g, const Sched& S, const Epi& E) {
;     ...
;         const char* nA = has_next ? (const char*)g.A + (size_t)nxt.pm * tstep + (size_t)nxt.k0 * 2 : cA; const char* nB = has_next ? (const char*)g.Bt + (size_t)nxt.pn * tstep + (size_t)nxt.k0 * 2 : cB;
;         for (int t = 0; t < nt; t += 2) {
;             const bool last = (t == nt - 2);
;             const char* a1 = cA + (size_t)(t + 1) * kstep;
;             const char* a2 = last ? nA : cA + (size_t)(t + 2) * kstep; const char* b2 = last ? nB : cB + (size_t)(t + 2) * kstep;
;             const char* a3 = a2 + kstep; const char* b3 = b2 + kstep;
;             if (last && has_next) S.a_ready(nxt);
;             if constexpr (SP2) {
;             PG8_LDB(B0, 0, 0); PG8_LDB(B1, 0, 1); PG8_SCHED; PG8_LDA(At, 0, 0); PG8_STAGE(PG8_SA(1, 1), a1 + hstep, voffA);
;             PG8_WAIT_V(8); PG8_WAIT_L(0); PG8_BAR; PG8_MMA(0, 0, At, B0); PG8_MMA(0, 1, At, B1); PG8_BAR; PG8_SCHED;
;             PG8_LDA(At, 0, 1); PG8_STAGE(PG8_SB(0, 0), b2, voffB); PG8_STAGE(PG8_SB(0, 1), b2 + hstep, voffB); PG8_STAGE(PG8_SA(0, 0), a2, voffA);
.LBB0_2253:
	ds_read_b128 v[150:153], v146
	ds_read_b128 v[154:157], v146 offset:1024
	ds_read_b128 v[158:161], v146 offset:2048
	ds_read_b128 v[162:165], v146 offset:3072
	ds_read_b128 v[166:169], v147
	ds_read_b128 v[170:173], v147 offset:1024
	ds_read_b128 v[174:177], v147 offset:2048
	ds_read_b128 v[178:181], v147 offset:3072
	s_add_u32 s38, s36, 0x100
	s_addc_u32 s39, s37, 0
	s_cmpk_eq_i32 s65, 0x6c
	s_cselect_b32 s43, s7, s39
	s_cselect_b32 s42, s6, s38
	s_cselect_b32 s41, s35, s64
	s_cselect_b32 s40, s34, s63
	v_lshl_add_u64 v[214:215], s[36:37], 0, v[138:139]
	s_add_i32 m0, s21, 0xc000
	ds_read_b128 v[182:185], v148
	ds_read_b128 v[186:189], v148 offset:1024
	ds_read_b128 v[190:193], v148 offset:2048
	ds_read_b128 v[194:197], v148 offset:3072
	ds_read_b128 v[198:201], v148 offset:4096
	ds_read_b128 v[202:205], v148 offset:5120
	ds_read_b128 v[206:209], v148 offset:6144
	ds_read_b128 v[210:213], v148 offset:7168
	global_load_lds_dwordx4 v[214:215], off
	s_add_i32 m0, s21, 0xe000
	v_lshl_add_u64 v[214:215], s[36:37], 0, v[140:141]
	global_load_lds_dwordx4 v[214:215], off
	s_waitcnt vmcnt(8)
	s_waitcnt lgkmcnt(0)
	s_barrier
	s_setprio 1
	s_waitcnt lgkmcnt(0)
	v_mfma_f32_16x16x32_bf16 v[126:129], v[150:153], v[182:185], v[126:129]
	v_mfma_f32_16x16x32_bf16 v[122:125], v[158:161], v[182:185], v[122:125]
	v_mfma_f32_16x16x32_bf16 v[118:121], v[150:153], v[190:193], v[118:121]
	v_mfma_f32_16x16x32_bf16 v[114:117], v[158:161], v[190:193], v[114:117]
	v_mfma_f32_16x16x32_bf16 v[102:105], v[150:153], v[198:201], v[102:105]
	v_mfma_f32_16x16x32_bf16 v[98:101], v[158:161], v[198:201], v[98:101]
	v_mfma_f32_16x16x32_bf16 v[86:89], v[150:153], v[206:209], v[86:89]
	v_mfma_f32_16x16x32_bf16 v[82:85], v[158:161], v[206:209], v[82:85]
	v_mfma_f32_16x16x32_bf16 v[126:129], v[154:157], v[186:189], v[126:129]
	v_mfma_f32_16x16x32_bf16 v[122:125], v[162:165], v[186:189], v[122:125]
	v_mfma_f32_16x16x32_bf16 v[118:121], v[154:157], v[194:197], v[118:121]
	v_mfma_f32_16x16x32_bf16 v[114:117], v[162:165], v[194:197], v[114:117]
	v_mfma_f32_16x16x32_bf16 v[102:105], v[154:157], v[202:205], v[102:105]
	v_mfma_f32_16x16x32_bf16 v[98:101], v[162:165], v[202:205], v[98:101]
	v_mfma_f32_16x16x32_bf16 v[86:89], v[154:157], v[210:213], v[86:89]
	v_mfma_f32_16x16x32_bf16 v[82:85], v[162:165], v[210:213], v[82:85]
	v_mfma_f32_16x16x32_bf16 v[110:113], v[166:169], v[182:185], v[110:113]
	v_mfma_f32_16x16x32_bf16 v[106:109], v[174:177], v[182:185], v[106:109]
	v_mfma_f32_16x16x32_bf16 v[94:97], v[166:169], v[190:193], v[94:97]
	v_mfma_f32_16x16x32_bf16 v[90:93], v[174:177], v[190:193], v[90:93]
	v_mfma_f32_16x16x32_bf16 v[78:81], v[166:169], v[198:201], v[78:81]
	v_mfma_f32_16x16x32_bf16 v[74:77], v[174:177], v[198:201], v[74:77]
	v_mfma_f32_16x16x32_bf16 v[70:73], v[166:169], v[206:209], v[70:73]
	v_mfma_f32_16x16x32_bf16 v[66:69], v[174:177], v[206:209], v[66:69]
	v_mfma_f32_16x16x32_bf16 v[110:113], v[170:173], v[186:189], v[110:113]
	v_mfma_f32_16x16x32_bf16 v[106:109], v[178:181], v[186:189], v[106:109]
	v_mfma_f32_16x16x32_bf16 v[94:97], v[170:173], v[194:197], v[94:97]
	v_mfma_f32_16x16x32_bf16 v[90:93], v[178:181], v[194:197], v[90:93]
	v_mfma_f32_16x16x32_bf16 v[78:81], v[170:173], v[202:205], v[78:81]
	v_mfma_f32_16x16x32_bf16 v[74:77], v[178:181], v[202:205], v[74:77]
	v_mfma_f32_16x16x32_bf16 v[70:73], v[170:173], v[210:213], v[70:73]
	v_mfma_f32_16x16x32_bf16 v[66:69], v[178:181], v[210:213], v[66:69]
	s_setprio 0
	s_barrier
	s_add_i32 s36, s11, s49
	v_lshl_add_u64 v[214:215], s[40:41], 0, v[130:131]
	s_mov_b32 m0, s36
	ds_read_b128 v[182:185], v148 offset:16384
	ds_read_b128 v[186:189], v148 offset:17408
	ds_read_b128 v[190:193], v148 offset:18432
	ds_read_b128 v[194:197], v148 offset:19456
	ds_read_b128 v[198:201], v148 offset:20480
	ds_read_b128 v[202:205], v148 offset:21504
	ds_read_b128 v[206:209], v148 offset:22528
	ds_read_b128 v[210:213], v148 offset:23552
	global_load_lds_dwordx4 v[214:215], off
	s_add_i32 m0, s36, 0x2000
	s_add_u32 s36, s40, 0x1c0000
	v_lshl_add_u64 v[216:217], s[40:41], 0, v[136:137]
	s_addc_u32 s37, s41, 0
	s_add_i32 s66, s57, s49
	global_load_lds_dwordx4 v[216:217], off
	v_lshl_add_u64 v[218:219], s[36:37], 0, v[130:131]
	s_mov_b32 m0, s66
	v_lshl_add_u64 v[220:221], s[42:43], 0, v[134:135]
	global_load_lds_dwordx4 v[218:219], off
	s_add_i32 m0, s66, 0x2000
	v_lshl_add_u64 v[218:219], s[36:37], 0, v[136:137]
	global_load_lds_dwordx4 v[218:219], off
	s_mov_b32 m0, s21
	v_lshl_add_u64 v[218:219], s[42:43], 0, v[132:133]
	global_load_lds_dwordx4 v[218:219], off
	s_mov_b32 m0, s51
	s_nop 0
	global_load_lds_dwordx4 v[220:221], off
	s_waitcnt vmcnt(8)
	s_waitcnt lgkmcnt(0)
	s_barrier
; #define PG8_STAGE(bufoff, gbase, voff) do { _Pragma("unroll") for (int _i = 0; _i < 2; ++_i) \
;         __builtin_amdgcn_global_load_lds((const unsigned*)((const char*)(gbase) + (voff)[_i]), (PG8_LAS unsigned*)(lds + (bufoff) + ldsw + _i * 8192), 16, 0, 0); } while (0)
; #define PG8_LDA(dst, b, h) do { _Pragma("unroll") for (int m = 0; m < 4; ++m) _Pragma("unroll") for (int k = 0; k < 2; ++k) dst[m][k] = *(const PG8_LAS bf16x8*)(lds + PG8_SA(b, h) + aoff + m * 2048 + k * 1024); } while (0)
; #define PG8_LDB(dst, b, h) do { _Pragma("unroll") for (int n = 0; n < 2; ++n) _Pragma("unroll") for (int k = 0; k < 2; ++k) dst[n][k] = *(const PG8_LAS bf16x8*)(lds + PG8_SB(b, h) + boff + n * 2048 + k * 1024); } while (0)
; #define PG8_MMA(ai, bj, At, Bt) do { __builtin_amdgcn_s_setprio(1); _Pragma("unroll") for (int m = 0; m < 4; ++m) _Pragma("unroll") for (int n = 0; n < 2; ++n) _Pragma("unroll") for (int k = 0; k < 2; ++k) \
;         acc[ai][bj][m][n] = __builtin_amdgcn_mfma_f32_16x16x32_bf16(Bt[n][k], At[m][k], acc[ai][bj][m][n], 0, 0, 0); __builtin_amdgcn_s_setprio(0); } while (0)
; #define PG8_WAIT_V(n) asm volatile("s_waitcnt vmcnt(" #n ")" ::: "memory")
; #define PG8_WAIT_L(n) asm volatile("s_waitcnt lgkmcnt(" #n ")" ::: "memory")
; #define PG8_BAR __builtin_amdgcn_s_barrier()
; #define PG8_SCHED __builtin_amdgcn_sched_barrier(0)
; template <class Epi, class Sched, bool ALIGN_EPI = false, bool SP2 = false>
; __device__ __forceinline__ void gemm_phase(PG8_LAS unsigned char* lds, const Gemm g, const Sched& S, const Epi& E) {
;     ...
;             PG8_WAIT_V(8); PG8_WAIT_L(0); PG8_BAR; PG8_MMA(1, 0, At, B0); PG8_MMA(1, 1, At, B1); PG8_BAR; PG8_SCHED;
;             PG8_LDB(B0, 1, 0); PG8_LDB(B1, 1, 1); PG8_SCHED; PG8_LDA(At, 1, 0); PG8_STAGE(PG8_SA(0, 1), a2 + hstep, voffA);
;             PG8_WAIT_V(8); PG8_WAIT_L(0); PG8_BAR; PG8_MMA(0, 0, At, B0); PG8_MMA(0, 1, At, B1); PG8_BAR; PG8_SCHED;
	s_setprio 1
	s_waitcnt lgkmcnt(0)
	v_mfma_f32_16x16x32_bf16 v[62:65], v[150:153], v[182:185], v[62:65]
	v_mfma_f32_16x16x32_bf16 v[58:61], v[158:161], v[182:185], v[58:61]
	v_mfma_f32_16x16x32_bf16 v[54:57], v[150:153], v[190:193], v[54:57]
	v_mfma_f32_16x16x32_bf16 v[50:53], v[158:161], v[190:193], v[50:53]
	v_mfma_f32_16x16x32_bf16 v[38:41], v[150:153], v[198:201], v[38:41]
	v_mfma_f32_16x16x32_bf16 v[34:37], v[158:161], v[198:201], v[34:37]
	v_mfma_f32_16x16x32_bf16 v[22:25], v[150:153], v[206:209], v[22:25]
	v_mfma_f32_16x16x32_bf16 v[18:21], v[158:161], v[206:209], v[18:21]
	v_mfma_f32_16x16x32_bf16 v[62:65], v[154:157], v[186:189], v[62:65]
	v_mfma_f32_16x16x32_bf16 v[58:61], v[162:165], v[186:189], v[58:61]
	v_mfma_f32_16x16x32_bf16 v[54:57], v[154:157], v[194:197], v[54:57]
	v_mfma_f32_16x16x32_bf16 v[50:53], v[162:165], v[194:197], v[50:53]
	v_mfma_f32_16x16x32_bf16 v[38:41], v[154:157], v[202:205], v[38:41]
	v_mfma_f32_16x16x32_bf16 v[34:37], v[162:165], v[202:205], v[34:37]
	v_mfma_f32_16x16x32_bf16 v[22:25], v[154:157], v[210:213], v[22:25]
	v_mfma_f32_16x16x32_bf16 v[18:21], v[162:165], v[210:213], v[18:21]
	v_mfma_f32_16x16x32_bf16 v[46:49], v[166:169], v[182:185], v[46:49]
	v_mfma_f32_16x16x32_bf16 v[42:45], v[174:177], v[182:185], v[42:45]
	v_mfma_f32_16x16x32_bf16 v[30:33], v[166:169], v[190:193], v[30:33]
	v_mfma_f32_16x16x32_bf16 v[26:29], v[174:177], v[190:193], v[26:29]
	v_mfma_f32_16x16x32_bf16 v[14:17], v[166:169], v[198:201], v[14:17]
	v_mfma_f32_16x16x32_bf16 v[10:13], v[174:177], v[198:201], v[10:13]
	v_mfma_f32_16x16x32_bf16 v[6:9], v[166:169], v[206:209], v[6:9]
	v_mfma_f32_16x16x32_bf16 v[2:5], v[174:177], v[206:209], v[2:5]
	v_mfma_f32_16x16x32_bf16 v[46:49], v[170:173], v[186:189], v[46:49]
	v_mfma_f32_16x16x32_bf16 v[42:45], v[178:181], v[186:189], v[42:45]
	v_mfma_f32_16x16x32_bf16 v[30:33], v[170:173], v[194:197], v[30:33]
	v_mfma_f32_16x16x32_bf16 v[26:29], v[178:181], v[194:197], v[26:29]
	v_mfma_f32_16x16x32_bf16 v[14:17], v[170:173], v[202:205], v[14:17]
	v_mfma_f32_16x16x32_bf16 v[10:13], v[178:181], v[202:205], v[10:13]
	v_mfma_f32_16x16x32_bf16 v[6:9], v[170:173], v[210:213], v[6:9]
	v_mfma_f32_16x16x32_bf16 v[2:5], v[178:181], v[210:213], v[2:5]
	s_setprio 0
	s_barrier
	s_add_i32 s66, 0, 0x18000
	v_add_u32_e32 v149, s66, v144
	s_add_i32 s67, 0, 0x1c000
	ds_read_b128 v[150:153], v149
	ds_read_b128 v[154:157], v149 offset:1024
	ds_read_b128 v[158:161], v149 offset:2048
	ds_read_b128 v[162:165], v149 offset:3072
	v_add_u32_e32 v149, s67, v144
	ds_read_b128 v[166:169], v149
	ds_read_b128 v[170:173], v149 offset:1024
	ds_read_b128 v[174:177], v149 offset:2048
	ds_read_b128 v[178:181], v149 offset:3072
	s_add_u32 s36, s42, 0x1c0000
	s_addc_u32 s37, s43, 0
	s_mov_b32 m0, s52
	v_lshl_add_u64 v[222:223], s[36:37], 0, v[132:133]
	ds_read_b128 v[182:185], v148 offset:32768
	ds_read_b128 v[186:189], v148 offset:33792
	ds_read_b128 v[190:193], v148 offset:34816
	ds_read_b128 v[194:197], v148 offset:35840
	ds_read_b128 v[198:201], v148 offset:36864
	ds_read_b128 v[202:205], v148 offset:37888
	ds_read_b128 v[206:209], v148 offset:38912
	ds_read_b128 v[210:213], v148 offset:39936
	global_load_lds_dwordx4 v[222:223], off
	s_mov_b32 m0, s53
	v_lshl_add_u64 v[222:223], s[36:37], 0, v[134:135]
	global_load_lds_dwordx4 v[222:223], off
	s_waitcnt vmcnt(8)
	s_waitcnt lgkmcnt(0)
	s_barrier
	s_setprio 1
	s_waitcnt lgkmcnt(0)
	v_mfma_f32_16x16x32_bf16 v[126:129], v[150:153], v[182:185], v[126:129]
	v_mfma_f32_16x16x32_bf16 v[122:125], v[158:161], v[182:185], v[122:125]
	v_mfma_f32_16x16x32_bf16 v[118:121], v[150:153], v[190:193], v[118:121]
	v_mfma_f32_16x16x32_bf16 v[114:117], v[158:161], v[190:193], v[114:117]
	v_mfma_f32_16x16x32_bf16 v[102:105], v[150:153], v[198:201], v[102:105]
	v_mfma_f32_16x16x32_bf16 v[98:101], v[158:161], v[198:201], v[98:101]
	v_mfma_f32_16x16x32_bf16 v[86:89], v[150:153], v[206:209], v[86:89]
	v_mfma_f32_16x16x32_bf16 v[82:85], v[158:161], v[206:209], v[82:85]
	v_mfma_f32_16x16x32_bf16 v[126:129], v[154:157], v[186:189], v[126:129]
	v_mfma_f32_16x16x32_bf16 v[122:125], v[162:165], v[186:189], v[122:125]
	v_mfma_f32_16x16x32_bf16 v[118:121], v[154:157], v[194:197], v[118:121]
	v_mfma_f32_16x16x32_bf16 v[114:117], v[162:165], v[194:197], v[114:117]
	v_mfma_f32_16x16x32_bf16 v[102:105], v[154:157], v[202:205], v[102:105]
	v_mfma_f32_16x16x32_bf16 v[98:101], v[162:165], v[202:205], v[98:101]
	v_mfma_f32_16x16x32_bf16 v[86:89], v[154:157], v[210:213], v[86:89]
	v_mfma_f32_16x16x32_bf16 v[82:85], v[162:165], v[210:213], v[82:85]
	v_mfma_f32_16x16x32_bf16 v[110:113], v[166:169], v[182:185], v[110:113]
	v_mfma_f32_16x16x32_bf16 v[106:109], v[174:177], v[182:185], v[106:109]
	v_mfma_f32_16x16x32_bf16 v[94:97], v[166:169], v[190:193], v[94:97]
	v_mfma_f32_16x16x32_bf16 v[90:93], v[174:177], v[190:193], v[90:93]
	v_mfma_f32_16x16x32_bf16 v[78:81], v[166:169], v[198:201], v[78:81]
	v_mfma_f32_16x16x32_bf16 v[74:77], v[174:177], v[198:201], v[74:77]
	v_mfma_f32_16x16x32_bf16 v[70:73], v[166:169], v[206:209], v[70:73]
	v_mfma_f32_16x16x32_bf16 v[66:69], v[174:177], v[206:209], v[66:69]
	v_mfma_f32_16x16x32_bf16 v[110:113], v[170:173], v[186:189], v[110:113]
	v_mfma_f32_16x16x32_bf16 v[106:109], v[178:181], v[186:189], v[106:109]
	v_mfma_f32_16x16x32_bf16 v[94:97], v[170:173], v[194:197], v[94:97]
	v_mfma_f32_16x16x32_bf16 v[90:93], v[178:181], v[194:197], v[90:93]
	v_mfma_f32_16x16x32_bf16 v[78:81], v[170:173], v[202:205], v[78:81]
	v_mfma_f32_16x16x32_bf16 v[74:77], v[178:181], v[202:205], v[74:77]
	v_mfma_f32_16x16x32_bf16 v[70:73], v[170:173], v[210:213], v[70:73]
	v_mfma_f32_16x16x32_bf16 v[66:69], v[178:181], v[210:213], v[66:69]
	s_setprio 0
	s_barrier
; #define PG8_STAGE(bufoff, gbase, voff) do { _Pragma("unroll") for (int _i = 0; _i < 2; ++_i) \
;         __builtin_amdgcn_global_load_lds((const unsigned*)((const char*)(gbase) + (voff)[_i]), (PG8_LAS unsigned*)(lds + (bufoff) + ldsw + _i * 8192), 16, 0, 0); } while (0)
; #define PG8_LDA(dst, b, h) do { _Pragma("unroll") for (int m = 0; m < 4; ++m) _Pragma("unroll") for (int k = 0; k < 2; ++k) dst[m][k] = *(const PG8_LAS bf16x8*)(lds + PG8_SA(b, h) + aoff + m * 2048 + k * 1024); } while (0)
; #define PG8_MMA(ai, bj, At, Bt) do { __builtin_amdgcn_s_setprio(1); _Pragma("unroll") for (int m = 0; m < 4; ++m) _Pragma("unroll") for (int n = 0; n < 2; ++n) _Pragma("unroll") for (int k = 0; k < 2; ++k) \
;         acc[ai][bj][m][n] = __builtin_amdgcn_mfma_f32_16x16x32_bf16(Bt[n][k], At[m][k], acc[ai][bj][m][n], 0, 0, 0); __builtin_amdgcn_s_setprio(0); } while (0)
; #define PG8_WAIT_V(n) asm volatile("s_waitcnt vmcnt(" #n ")" ::: "memory")
; #define PG8_WAIT_L(n) asm volatile("s_waitcnt lgkmcnt(" #n ")" ::: "memory")
; #define PG8_BAR __builtin_amdgcn_s_barrier()
; #define PG8_SCHED __builtin_amdgcn_sched_barrier(0)
; template <class Epi, class Sched, bool ALIGN_EPI = false, bool SP2 = false>
; __device__ __forceinline__ void gemm_phase(PG8_LAS unsigned char* lds, const Gemm g, const Sched& S, const Epi& E) {
;     ...
;             PG8_LDA(At, 1, 1); PG8_STAGE(PG8_SB(1, 0), b3, voffB); PG8_STAGE(PG8_SB(1, 1), b3 + hstep, voffB); PG8_STAGE(PG8_SA(1, 0), a3, voffA);
;             PG8_WAIT_V(8); PG8_WAIT_L(0); PG8_BAR; PG8_MMA(1, 0, At, B0); PG8_MMA(1, 1, At, B1); PG8_BAR; PG8_SCHED;
	s_add_i32 s36, s66, s49
	v_lshl_add_u64 v[214:215], v[214:215], 0, s[18:19]
	s_mov_b32 m0, s36
	ds_read_b128 v[182:185], v148 offset:49152
	ds_read_b128 v[186:189], v148 offset:50176
	ds_read_b128 v[190:193], v148 offset:51200
	ds_read_b128 v[194:197], v148 offset:52224
	ds_read_b128 v[198:201], v148 offset:53248
	ds_read_b128 v[202:205], v148 offset:54272
	ds_read_b128 v[206:209], v148 offset:55296
	ds_read_b128 v[210:213], v148 offset:56320
	global_load_lds_dwordx4 v[214:215], off
	s_add_i32 m0, s36, 0x2000
	s_add_u32 s36, s40, 0x1c0080
	v_lshl_add_u64 v[214:215], v[216:217], 0, s[18:19]
	s_addc_u32 s37, s41, 0
	s_add_i32 s40, s67, s49
	global_load_lds_dwordx4 v[214:215], off
	s_mov_b32 m0, s40
	v_lshl_add_u64 v[214:215], s[36:37], 0, v[130:131]
	global_load_lds_dwordx4 v[214:215], off
	s_add_i32 m0, s40, 0x2000
	v_lshl_add_u64 v[214:215], s[36:37], 0, v[136:137]
	global_load_lds_dwordx4 v[214:215], off
	s_mov_b32 m0, s55
	v_lshl_add_u64 v[214:215], v[218:219], 0, s[18:19]
	global_load_lds_dwordx4 v[214:215], off
	s_mov_b32 m0, s56
	v_lshl_add_u64 v[214:215], v[220:221], 0, s[18:19]
	global_load_lds_dwordx4 v[214:215], off
	s_waitcnt vmcnt(8)
	s_waitcnt lgkmcnt(0)
	s_barrier
	s_setprio 1
	s_waitcnt lgkmcnt(0)
	v_mfma_f32_16x16x32_bf16 v[62:65], v[150:153], v[182:185], v[62:65]
	v_mfma_f32_16x16x32_bf16 v[58:61], v[158:161], v[182:185], v[58:61]
	v_mfma_f32_16x16x32_bf16 v[54:57], v[150:153], v[190:193], v[54:57]
	v_mfma_f32_16x16x32_bf16 v[50:53], v[158:161], v[190:193], v[50:53]
	v_mfma_f32_16x16x32_bf16 v[38:41], v[150:153], v[198:201], v[38:41]
	v_mfma_f32_16x16x32_bf16 v[34:37], v[158:161], v[198:201], v[34:37]
	v_mfma_f32_16x16x32_bf16 v[22:25], v[150:153], v[206:209], v[22:25]
	v_mfma_f32_16x16x32_bf16 v[18:21], v[158:161], v[206:209], v[18:21]
	v_mfma_f32_16x16x32_bf16 v[62:65], v[154:157], v[186:189], v[62:65]
	v_mfma_f32_16x16x32_bf16 v[58:61], v[162:165], v[186:189], v[58:61]
	v_mfma_f32_16x16x32_bf16 v[54:57], v[154:157], v[194:197], v[54:57]
	v_mfma_f32_16x16x32_bf16 v[50:53], v[162:165], v[194:197], v[50:53]
	v_mfma_f32_16x16x32_bf16 v[38:41], v[154:157], v[202:205], v[38:41]
	v_mfma_f32_16x16x32_bf16 v[34:37], v[162:165], v[202:205], v[34:37]
	v_mfma_f32_16x16x32_bf16 v[22:25], v[154:157], v[210:213], v[22:25]
	v_mfma_f32_16x16x32_bf16 v[18:21], v[162:165], v[210:213], v[18:21]
	v_mfma_f32_16x16x32_bf16 v[46:49], v[166:169], v[182:185], v[46:49]
	v_mfma_f32_16x16x32_bf16 v[42:45], v[174:177], v[182:185], v[42:45]
	v_mfma_f32_16x16x32_bf16 v[30:33], v[166:169], v[190:193], v[30:33]
	v_mfma_f32_16x16x32_bf16 v[26:29], v[174:177], v[190:193], v[26:29]
	v_mfma_f32_16x16x32_bf16 v[14:17], v[166:169], v[198:201], v[14:17]
	v_mfma_f32_16x16x32_bf16 v[10:13], v[174:177], v[198:201], v[10:13]
	v_mfma_f32_16x16x32_bf16 v[6:9], v[166:169], v[206:209], v[6:9]
	v_mfma_f32_16x16x32_bf16 v[2:5], v[174:177], v[206:209], v[2:5]
	v_mfma_f32_16x16x32_bf16 v[46:49], v[170:173], v[186:189], v[46:49]
	v_mfma_f32_16x16x32_bf16 v[42:45], v[178:181], v[186:189], v[42:45]
	v_mfma_f32_16x16x32_bf16 v[30:33], v[170:173], v[194:197], v[30:33]
	v_mfma_f32_16x16x32_bf16 v[26:29], v[178:181], v[194:197], v[26:29]
	v_mfma_f32_16x16x32_bf16 v[14:17], v[170:173], v[202:205], v[14:17]
	v_mfma_f32_16x16x32_bf16 v[10:13], v[178:181], v[202:205], v[10:13]
	v_mfma_f32_16x16x32_bf16 v[6:9], v[170:173], v[210:213], v[6:9]
	v_mfma_f32_16x16x32_bf16 v[2:5], v[178:181], v[210:213], v[2:5]
	s_setprio 0
	s_barrier
	s_add_i32 s65, s65, 2
	s_add_u32 s63, s63, 0x100
	s_addc_u32 s64, s64, 0
	s_cmpk_gt_u32 s65, 0x6d
	s_mov_b64 s[36:37], s[38:39]
	s_cbranch_scc0 .LBB0_2253
	s_and_b64 vcc, exec, s[22:23]
	s_cbranch_vccz .LBB0_2256
	s_barrier

; #define PG8_STAGE(bufoff, gbase, voff) do { _Pragma("unroll") for (int _i = 0; _i < 2; ++_i) \
;         __builtin_amdgcn_global_load_lds((const unsigned*)((const char*)(gbase) + (voff)[_i]), (PG8_LAS unsigned*)(lds + (bufoff) + ldsw + _i * 8192), 16, 0, 0); } while (0)
; #define PG8_LDA(dst, b, h) do { _Pragma("unroll") for (int m = 0; m < 4; ++m) _Pragma("unroll") for (int k = 0; k < 2; ++k) dst[m][k] = *(const PG8_LAS bf16x8*)(lds + PG8_SA(b, h) + aoff + m * 2048 + k * 1024); } while (0)
; #define PG8_LDB(dst, b, h) do { _Pragma("unroll") for (int n = 0; n < 2; ++n) _Pragma("unroll") for (int k = 0; k < 2; ++k) dst[n][k] = *(const PG8_LAS bf16x8*)(lds + PG8_SB(b, h) + boff + n * 2048 + k * 1024); } while (0)
; #define PG8_MMA(ai, bj, At, Bt) do { __builtin_amdgcn_s_setprio(1); _Pragma("unroll") for (int m = 0; m < 4; ++m) _Pragma("unroll") for (int n = 0; n < 2; ++n) _Pragma("unroll") for (int k = 0; k < 2; ++k) \
;         acc[ai][bj][m][n] = __builtin_amdgcn_mfma_f32_16x16x32_bf16(Bt[n][k], At[m][k], acc[ai][bj][m][n], 0, 0, 0); __builtin_amdgcn_s_setprio(0); } while (0)
; #define PG8_BAR __builtin_amdgcn_s_barrier()
; template <class Epi, class Sched, bool ALIGN_EPI = false, bool SP2 = false>
; __device__ __forceinline__ void gemm_phase(PG8_LAS unsigned char* lds, const Gemm g, const Sched& S, const Epi& E) {
;     ...
;         const char* nA = has_next ? (const char*)g.A + (size_t)nxt.pm * tstep + (size_t)nxt.k0 * 2 : cA; const char* nB = has_next ? (const char*)g.Bt + (size_t)nxt.pn * tstep + (size_t)nxt.k0 * 2 : cB;
;         for (int t = 0; t < nt; t += 2) {
;             const bool last = (t == nt - 2);
;             const char* a1 = cA + (size_t)(t + 1) * kstep;
;             const char* a2 = last ? nA : cA + (size_t)(t + 2) * kstep; const char* b2 = last ? nB : cB + (size_t)(t + 2) * kstep;
;             const char* a3 = a2 + kstep; const char* b3 = b2 + kstep;
;             if (last && has_next) S.a_ready(nxt);
;             if constexpr (SP2) {
;             PG8_LDB(B0, 0, 0); PG8_LDB(B1, 0, 1); PG8_SCHED; PG8_LDA(At, 0, 0); PG8_STAGE(PG8_SA(1, 1), a1 + hstep, voffA);
;             PG8_WAIT_V(8); PG8_WAIT_L(0); PG8_BAR; PG8_MMA(0, 0, At, B0); PG8_MMA(0, 1, At, B1); PG8_BAR; PG8_SCHED;
;             PG8_LDA(At, 0, 1); PG8_STAGE(PG8_SB(0, 0), b2, voffB); PG8_STAGE(PG8_SB(0, 1), b2 + hstep, voffB); PG8_STAGE(PG8_SA(0, 0), a2, voffA);
.LBB0_2279:
	ds_read_b128 v[146:149], v142
	ds_read_b128 v[150:153], v142 offset:1024
	ds_read_b128 v[154:157], v142 offset:2048
	ds_read_b128 v[158:161], v142 offset:3072
	ds_read_b128 v[162:165], v143
	ds_read_b128 v[166:169], v143 offset:1024
	ds_read_b128 v[170:173], v143 offset:2048
	ds_read_b128 v[174:177], v143 offset:3072
	s_add_i32 s60, s27, 2
	s_add_u32 s34, s30, 0x100
	s_addc_u32 s35, s31, 0
	s_cmp_eq_u32 s52, s27
	s_cselect_b32 s39, s5, s35
	s_cselect_b32 s38, s4, s34
	s_cselect_b32 s37, s29, s25
	s_cselect_b32 s36, s28, s23
	v_lshl_add_u64 v[210:211], s[30:31], 0, v[138:139]
	s_add_i32 m0, s7, 0xc000
	ds_read_b128 v[178:181], v144
	ds_read_b128 v[182:185], v144 offset:1024
	ds_read_b128 v[186:189], v144 offset:2048
	ds_read_b128 v[190:193], v144 offset:3072
	ds_read_b128 v[194:197], v144 offset:4096
	ds_read_b128 v[198:201], v144 offset:5120
	ds_read_b128 v[202:205], v144 offset:6144
	ds_read_b128 v[206:209], v144 offset:7168
	global_load_lds_dwordx4 v[210:211], off
	s_add_i32 m0, s7, 0xe000
	v_lshl_add_u64 v[210:211], s[30:31], 0, v[140:141]
	global_load_lds_dwordx4 v[210:211], off
	s_waitcnt vmcnt(8)
	s_waitcnt lgkmcnt(0)
	s_barrier
	s_setprio 1
	s_waitcnt lgkmcnt(0)
	v_mfma_f32_16x16x32_bf16 v[126:129], v[146:149], v[178:181], v[126:129]
	v_mfma_f32_16x16x32_bf16 v[122:125], v[154:157], v[178:181], v[122:125]
	v_mfma_f32_16x16x32_bf16 v[118:121], v[146:149], v[186:189], v[118:121]
	v_mfma_f32_16x16x32_bf16 v[114:117], v[154:157], v[186:189], v[114:117]
	v_mfma_f32_16x16x32_bf16 v[110:113], v[146:149], v[194:197], v[110:113]
	v_mfma_f32_16x16x32_bf16 v[102:105], v[154:157], v[194:197], v[102:105]
	v_mfma_f32_16x16x32_bf16 v[94:97], v[146:149], v[202:205], v[94:97]
	v_mfma_f32_16x16x32_bf16 v[86:89], v[154:157], v[202:205], v[86:89]
	v_mfma_f32_16x16x32_bf16 v[126:129], v[150:153], v[182:185], v[126:129]
	v_mfma_f32_16x16x32_bf16 v[122:125], v[158:161], v[182:185], v[122:125]
	v_mfma_f32_16x16x32_bf16 v[118:121], v[150:153], v[190:193], v[118:121]
	v_mfma_f32_16x16x32_bf16 v[114:117], v[158:161], v[190:193], v[114:117]
	v_mfma_f32_16x16x32_bf16 v[110:113], v[150:153], v[198:201], v[110:113]
	v_mfma_f32_16x16x32_bf16 v[102:105], v[158:161], v[198:201], v[102:105]
	v_mfma_f32_16x16x32_bf16 v[94:97], v[150:153], v[206:209], v[94:97]
	v_mfma_f32_16x16x32_bf16 v[86:89], v[158:161], v[206:209], v[86:89]
	v_mfma_f32_16x16x32_bf16 v[106:109], v[162:165], v[178:181], v[106:109]
	v_mfma_f32_16x16x32_bf16 v[98:101], v[170:173], v[178:181], v[98:101]
	v_mfma_f32_16x16x32_bf16 v[90:93], v[162:165], v[186:189], v[90:93]
	v_mfma_f32_16x16x32_bf16 v[82:85], v[170:173], v[186:189], v[82:85]
	v_mfma_f32_16x16x32_bf16 v[78:81], v[162:165], v[194:197], v[78:81]
	v_mfma_f32_16x16x32_bf16 v[74:77], v[170:173], v[194:197], v[74:77]
	v_mfma_f32_16x16x32_bf16 v[70:73], v[162:165], v[202:205], v[70:73]
	v_mfma_f32_16x16x32_bf16 v[66:69], v[170:173], v[202:205], v[66:69]
	v_mfma_f32_16x16x32_bf16 v[106:109], v[166:169], v[182:185], v[106:109]
	v_mfma_f32_16x16x32_bf16 v[98:101], v[174:177], v[182:185], v[98:101]
	v_mfma_f32_16x16x32_bf16 v[90:93], v[166:169], v[190:193], v[90:93]
	v_mfma_f32_16x16x32_bf16 v[82:85], v[174:177], v[190:193], v[82:85]
	v_mfma_f32_16x16x32_bf16 v[78:81], v[166:169], v[198:201], v[78:81]
	v_mfma_f32_16x16x32_bf16 v[74:77], v[174:177], v[198:201], v[74:77]
	v_mfma_f32_16x16x32_bf16 v[70:73], v[166:169], v[206:209], v[70:73]
	v_mfma_f32_16x16x32_bf16 v[66:69], v[174:177], v[206:209], v[66:69]
	s_setprio 0
	s_barrier
	s_add_i32 s27, s54, s41
	v_lshl_add_u64 v[210:211], s[36:37], 0, v[132:133]
	s_mov_b32 m0, s27
	ds_read_b128 v[178:181], v144 offset:16384
	ds_read_b128 v[182:185], v144 offset:17408
	ds_read_b128 v[186:189], v144 offset:18432
	ds_read_b128 v[190:193], v144 offset:19456
	ds_read_b128 v[194:197], v144 offset:20480
	ds_read_b128 v[198:201], v144 offset:21504
	ds_read_b128 v[202:205], v144 offset:22528
	ds_read_b128 v[206:209], v144 offset:23552
	global_load_lds_dwordx4 v[210:211], off
	s_add_i32 m0, s27, 0x2000
	s_add_u32 s30, s36, 0x1c0000
	v_lshl_add_u64 v[212:213], s[36:37], 0, v[134:135]
	s_addc_u32 s31, s37, 0
	s_add_i32 s27, s55, s41
	global_load_lds_dwordx4 v[212:213], off
	v_lshl_add_u64 v[214:215], s[30:31], 0, v[132:133]
	s_mov_b32 m0, s27
	v_lshl_add_u64 v[216:217], s[38:39], 0, v[134:135]
	global_load_lds_dwordx4 v[214:215], off
	s_add_i32 m0, s27, 0x2000
	v_lshl_add_u64 v[214:215], s[30:31], 0, v[134:135]
	global_load_lds_dwordx4 v[214:215], off
	s_mov_b32 m0, s7
	v_lshl_add_u64 v[214:215], s[38:39], 0, v[132:133]
	global_load_lds_dwordx4 v[214:215], off
	s_mov_b32 m0, s17
	s_nop 0
	global_load_lds_dwordx4 v[216:217], off
	s_waitcnt vmcnt(8)
	s_waitcnt lgkmcnt(0)
	s_barrier
; #define PG8_STAGE(bufoff, gbase, voff) do { _Pragma("unroll") for (int _i = 0; _i < 2; ++_i) \
;         __builtin_amdgcn_global_load_lds((const unsigned*)((const char*)(gbase) + (voff)[_i]), (PG8_LAS unsigned*)(lds + (bufoff) + ldsw + _i * 8192), 16, 0, 0); } while (0)
; #define PG8_LDA(dst, b, h) do { _Pragma("unroll") for (int m = 0; m < 4; ++m) _Pragma("unroll") for (int k = 0; k < 2; ++k) dst[m][k] = *(const PG8_LAS bf16x8*)(lds + PG8_SA(b, h) + aoff + m * 2048 + k * 1024); } while (0)
; #define PG8_LDB(dst, b, h) do { _Pragma("unroll") for (int n = 0; n < 2; ++n) _Pragma("unroll") for (int k = 0; k < 2; ++k) dst[n][k] = *(const PG8_LAS bf16x8*)(lds + PG8_SB(b, h) + boff + n * 2048 + k * 1024); } while (0)
; #define PG8_MMA(ai, bj, At, Bt) do { __builtin_amdgcn_s_setprio(1); _Pragma("unroll") for (int m = 0; m < 4; ++m) _Pragma("unroll") for (int n = 0; n < 2; ++n) _Pragma("unroll") for (int k = 0; k < 2; ++k) \
;         acc[ai][bj][m][n] = __builtin_amdgcn_mfma_f32_16x16x32_bf16(Bt[n][k], At[m][k], acc[ai][bj][m][n], 0, 0, 0); __builtin_amdgcn_s_setprio(0); } while (0)
; #define PG8_WAIT_V(n) asm volatile("s_waitcnt vmcnt(" #n ")" ::: "memory")
; #define PG8_WAIT_L(n) asm volatile("s_waitcnt lgkmcnt(" #n ")" ::: "memory")
; #define PG8_BAR __builtin_amdgcn_s_barrier()
; #define PG8_SCHED __builtin_amdgcn_sched_barrier(0)
; template <class Epi, class Sched, bool ALIGN_EPI = false, bool SP2 = false>
; __device__ __forceinline__ void gemm_phase(PG8_LAS unsigned char* lds, const Gemm g, const Sched& S, const Epi& E) {
;     ...
;             PG8_WAIT_V(8); PG8_WAIT_L(0); PG8_BAR; PG8_MMA(1, 0, At, B0); PG8_MMA(1, 1, At, B1); PG8_BAR; PG8_SCHED;
;             PG8_LDB(B0, 1, 0); PG8_LDB(B1, 1, 1); PG8_SCHED; PG8_LDA(At, 1, 0); PG8_STAGE(PG8_SA(0, 1), a2 + hstep, voffA);
;             PG8_WAIT_V(8); PG8_WAIT_L(0); PG8_BAR; PG8_MMA(0, 0, At, B0); PG8_MMA(0, 1, At, B1); PG8_BAR; PG8_SCHED;
	s_setprio 1
	s_waitcnt lgkmcnt(0)
	v_mfma_f32_16x16x32_bf16 v[62:65], v[146:149], v[178:181], v[62:65]
	v_mfma_f32_16x16x32_bf16 v[58:61], v[154:157], v[178:181], v[58:61]
	v_mfma_f32_16x16x32_bf16 v[54:57], v[146:149], v[186:189], v[54:57]
	v_mfma_f32_16x16x32_bf16 v[50:53], v[154:157], v[186:189], v[50:53]
	v_mfma_f32_16x16x32_bf16 v[46:49], v[146:149], v[194:197], v[46:49]
	v_mfma_f32_16x16x32_bf16 v[38:41], v[154:157], v[194:197], v[38:41]
	v_mfma_f32_16x16x32_bf16 v[30:33], v[146:149], v[202:205], v[30:33]
	v_mfma_f32_16x16x32_bf16 v[22:25], v[154:157], v[202:205], v[22:25]
	v_mfma_f32_16x16x32_bf16 v[62:65], v[150:153], v[182:185], v[62:65]
	v_mfma_f32_16x16x32_bf16 v[58:61], v[158:161], v[182:185], v[58:61]
	v_mfma_f32_16x16x32_bf16 v[54:57], v[150:153], v[190:193], v[54:57]
	v_mfma_f32_16x16x32_bf16 v[50:53], v[158:161], v[190:193], v[50:53]
	v_mfma_f32_16x16x32_bf16 v[46:49], v[150:153], v[198:201], v[46:49]
	v_mfma_f32_16x16x32_bf16 v[38:41], v[158:161], v[198:201], v[38:41]
	v_mfma_f32_16x16x32_bf16 v[30:33], v[150:153], v[206:209], v[30:33]
	v_mfma_f32_16x16x32_bf16 v[22:25], v[158:161], v[206:209], v[22:25]
	v_mfma_f32_16x16x32_bf16 v[42:45], v[162:165], v[178:181], v[42:45]
	v_mfma_f32_16x16x32_bf16 v[34:37], v[170:173], v[178:181], v[34:37]
	v_mfma_f32_16x16x32_bf16 v[26:29], v[162:165], v[186:189], v[26:29]
	v_mfma_f32_16x16x32_bf16 v[18:21], v[170:173], v[186:189], v[18:21]
	v_mfma_f32_16x16x32_bf16 v[14:17], v[162:165], v[194:197], v[14:17]
	v_mfma_f32_16x16x32_bf16 v[10:13], v[170:173], v[194:197], v[10:13]
	v_mfma_f32_16x16x32_bf16 v[6:9], v[162:165], v[202:205], v[6:9]
	v_mfma_f32_16x16x32_bf16 v[2:5], v[170:173], v[202:205], v[2:5]
	v_mfma_f32_16x16x32_bf16 v[42:45], v[166:169], v[182:185], v[42:45]
	v_mfma_f32_16x16x32_bf16 v[34:37], v[174:177], v[182:185], v[34:37]
	v_mfma_f32_16x16x32_bf16 v[26:29], v[166:169], v[190:193], v[26:29]
	v_mfma_f32_16x16x32_bf16 v[18:21], v[174:177], v[190:193], v[18:21]
	v_mfma_f32_16x16x32_bf16 v[14:17], v[166:169], v[198:201], v[14:17]
	v_mfma_f32_16x16x32_bf16 v[10:13], v[174:177], v[198:201], v[10:13]
	v_mfma_f32_16x16x32_bf16 v[6:9], v[166:169], v[206:209], v[6:9]
	v_mfma_f32_16x16x32_bf16 v[2:5], v[174:177], v[206:209], v[2:5]
	s_setprio 0
	s_barrier
	s_add_i32 s27, 0, 0x18000
	s_add_i32 s61, 0, 0x1c000
	v_add_u32_e32 v158, s27, v1
	v_add_u32_e32 v174, s61, v1
	ds_read_b128 v[146:149], v158
	ds_read_b128 v[150:153], v158 offset:1024
	ds_read_b128 v[154:157], v158 offset:2048
	ds_read_b128 v[158:161], v158 offset:3072
	ds_read_b128 v[162:165], v174
	ds_read_b128 v[166:169], v174 offset:1024
	ds_read_b128 v[170:173], v174 offset:2048
	ds_read_b128 v[174:177], v174 offset:3072
	s_add_u32 s30, s38, 0x1c0000
	s_addc_u32 s31, s39, 0
	s_mov_b32 m0, s44
	v_lshl_add_u64 v[218:219], s[30:31], 0, v[132:133]
	ds_read_b128 v[178:181], v144 offset:32768
	ds_read_b128 v[182:185], v144 offset:33792
	ds_read_b128 v[186:189], v144 offset:34816
	ds_read_b128 v[190:193], v144 offset:35840
	ds_read_b128 v[194:197], v144 offset:36864
	ds_read_b128 v[198:201], v144 offset:37888
	ds_read_b128 v[202:205], v144 offset:38912
	ds_read_b128 v[206:209], v144 offset:39936
	global_load_lds_dwordx4 v[218:219], off
	s_mov_b32 m0, s45
	v_lshl_add_u64 v[218:219], s[30:31], 0, v[134:135]
	global_load_lds_dwordx4 v[218:219], off
	s_waitcnt vmcnt(8)
	s_waitcnt lgkmcnt(0)
	s_barrier
	s_setprio 1
	s_waitcnt lgkmcnt(0)
	v_mfma_f32_16x16x32_bf16 v[126:129], v[146:149], v[178:181], v[126:129]
	v_mfma_f32_16x16x32_bf16 v[122:125], v[154:157], v[178:181], v[122:125]
	v_mfma_f32_16x16x32_bf16 v[118:121], v[146:149], v[186:189], v[118:121]
	v_mfma_f32_16x16x32_bf16 v[114:117], v[154:157], v[186:189], v[114:117]
	v_mfma_f32_16x16x32_bf16 v[110:113], v[146:149], v[194:197], v[110:113]
	v_mfma_f32_16x16x32_bf16 v[102:105], v[154:157], v[194:197], v[102:105]
	v_mfma_f32_16x16x32_bf16 v[94:97], v[146:149], v[202:205], v[94:97]
	v_mfma_f32_16x16x32_bf16 v[86:89], v[154:157], v[202:205], v[86:89]
	v_mfma_f32_16x16x32_bf16 v[126:129], v[150:153], v[182:185], v[126:129]
	v_mfma_f32_16x16x32_bf16 v[122:125], v[158:161], v[182:185], v[122:125]
	v_mfma_f32_16x16x32_bf16 v[118:121], v[150:153], v[190:193], v[118:121]
	v_mfma_f32_16x16x32_bf16 v[114:117], v[158:161], v[190:193], v[114:117]
	v_mfma_f32_16x16x32_bf16 v[110:113], v[150:153], v[198:201], v[110:113]
	v_mfma_f32_16x16x32_bf16 v[102:105], v[158:161], v[198:201], v[102:105]
	v_mfma_f32_16x16x32_bf16 v[94:97], v[150:153], v[206:209], v[94:97]
	v_mfma_f32_16x16x32_bf16 v[86:89], v[158:161], v[206:209], v[86:89]
	v_mfma_f32_16x16x32_bf16 v[106:109], v[162:165], v[178:181], v[106:109]
	v_mfma_f32_16x16x32_bf16 v[98:101], v[170:173], v[178:181], v[98:101]
	v_mfma_f32_16x16x32_bf16 v[90:93], v[162:165], v[186:189], v[90:93]
	v_mfma_f32_16x16x32_bf16 v[82:85], v[170:173], v[186:189], v[82:85]
	v_mfma_f32_16x16x32_bf16 v[78:81], v[162:165], v[194:197], v[78:81]
	v_mfma_f32_16x16x32_bf16 v[74:77], v[170:173], v[194:197], v[74:77]
	v_mfma_f32_16x16x32_bf16 v[70:73], v[162:165], v[202:205], v[70:73]
	v_mfma_f32_16x16x32_bf16 v[66:69], v[170:173], v[202:205], v[66:69]
	v_mfma_f32_16x16x32_bf16 v[106:109], v[166:169], v[182:185], v[106:109]
	v_mfma_f32_16x16x32_bf16 v[98:101], v[174:177], v[182:185], v[98:101]
	v_mfma_f32_16x16x32_bf16 v[90:93], v[166:169], v[190:193], v[90:93]
	v_mfma_f32_16x16x32_bf16 v[82:85], v[174:177], v[190:193], v[82:85]
	v_mfma_f32_16x16x32_bf16 v[78:81], v[166:169], v[198:201], v[78:81]
	v_mfma_f32_16x16x32_bf16 v[74:77], v[174:177], v[198:201], v[74:77]
	v_mfma_f32_16x16x32_bf16 v[70:73], v[166:169], v[206:209], v[70:73]
	v_mfma_f32_16x16x32_bf16 v[66:69], v[174:177], v[206:209], v[66:69]
	s_setprio 0
	s_barrier
; #define PG8_STAGE(bufoff, gbase, voff) do { _Pragma("unroll") for (int _i = 0; _i < 2; ++_i) \
;         __builtin_amdgcn_global_load_lds((const unsigned*)((const char*)(gbase) + (voff)[_i]), (PG8_LAS unsigned*)(lds + (bufoff) + ldsw + _i * 8192), 16, 0, 0); } while (0)
; #define PG8_LDA(dst, b, h) do { _Pragma("unroll") for (int m = 0; m < 4; ++m) _Pragma("unroll") for (int k = 0; k < 2; ++k) dst[m][k] = *(const PG8_LAS bf16x8*)(lds + PG8_SA(b, h) + aoff + m * 2048 + k * 1024); } while (0)
; #define PG8_MMA(ai, bj, At, Bt) do { __builtin_amdgcn_s_setprio(1); _Pragma("unroll") for (int m = 0; m < 4; ++m) _Pragma("unroll") for (int n = 0; n < 2; ++n) _Pragma("unroll") for (int k = 0; k < 2; ++k) \
;         acc[ai][bj][m][n] = __builtin_amdgcn_mfma_f32_16x16x32_bf16(Bt[n][k], At[m][k], acc[ai][bj][m][n], 0, 0, 0); __builtin_amdgcn_s_setprio(0); } while (0)
; #define PG8_WAIT_V(n) asm volatile("s_waitcnt vmcnt(" #n ")" ::: "memory")
; #define PG8_WAIT_L(n) asm volatile("s_waitcnt lgkmcnt(" #n ")" ::: "memory")
; #define PG8_BAR __builtin_amdgcn_s_barrier()
; #define PG8_SCHED __builtin_amdgcn_sched_barrier(0)
; template <class Epi, class Sched, bool ALIGN_EPI = false, bool SP2 = false>
; __device__ __forceinline__ void gemm_phase(PG8_LAS unsigned char* lds, const Gemm g, const Sched& S, const Epi& E) {
;     ...
;             PG8_LDA(At, 1, 1); PG8_STAGE(PG8_SB(1, 0), b3, voffB); PG8_STAGE(PG8_SB(1, 1), b3 + hstep, voffB); PG8_STAGE(PG8_SA(1, 0), a3, voffA);
;             PG8_WAIT_V(8); PG8_WAIT_L(0); PG8_BAR; PG8_MMA(1, 0, At, B0); PG8_MMA(1, 1, At, B1); PG8_BAR; PG8_SCHED;
	s_add_i32 s27, s27, s41
	v_lshl_add_u64 v[210:211], v[210:211], 0, s[18:19]
	s_mov_b32 m0, s27
	ds_read_b128 v[178:181], v144 offset:49152
	ds_read_b128 v[182:185], v144 offset:50176
	ds_read_b128 v[186:189], v144 offset:51200
	ds_read_b128 v[190:193], v144 offset:52224
	ds_read_b128 v[194:197], v144 offset:53248
	ds_read_b128 v[198:201], v144 offset:54272
	ds_read_b128 v[202:205], v144 offset:55296
	ds_read_b128 v[206:209], v144 offset:56320
	global_load_lds_dwordx4 v[210:211], off
	s_add_i32 m0, s27, 0x2000
	s_add_u32 s30, s36, 0x1c0080
	v_lshl_add_u64 v[210:211], v[212:213], 0, s[18:19]
	s_addc_u32 s31, s37, 0
	s_add_i32 s27, s61, s41
	global_load_lds_dwordx4 v[210:211], off
	s_mov_b32 m0, s27
	v_lshl_add_u64 v[210:211], s[30:31], 0, v[132:133]
	global_load_lds_dwordx4 v[210:211], off
	s_add_i32 m0, s27, 0x2000
	v_lshl_add_u64 v[210:211], s[30:31], 0, v[134:135]
	global_load_lds_dwordx4 v[210:211], off
	s_mov_b32 m0, s48
	v_lshl_add_u64 v[210:211], v[214:215], 0, s[18:19]
	global_load_lds_dwordx4 v[210:211], off
	s_mov_b32 m0, s49
	v_lshl_add_u64 v[210:211], v[216:217], 0, s[18:19]
	global_load_lds_dwordx4 v[210:211], off
	s_waitcnt vmcnt(8)
	s_waitcnt lgkmcnt(0)
	s_barrier
	s_setprio 1
	s_waitcnt lgkmcnt(0)
	v_mfma_f32_16x16x32_bf16 v[62:65], v[146:149], v[178:181], v[62:65]
	v_mfma_f32_16x16x32_bf16 v[58:61], v[154:157], v[178:181], v[58:61]
	v_mfma_f32_16x16x32_bf16 v[54:57], v[146:149], v[186:189], v[54:57]
	v_mfma_f32_16x16x32_bf16 v[50:53], v[154:157], v[186:189], v[50:53]
	v_mfma_f32_16x16x32_bf16 v[46:49], v[146:149], v[194:197], v[46:49]
	v_mfma_f32_16x16x32_bf16 v[38:41], v[154:157], v[194:197], v[38:41]
	v_mfma_f32_16x16x32_bf16 v[30:33], v[146:149], v[202:205], v[30:33]
	v_mfma_f32_16x16x32_bf16 v[22:25], v[154:157], v[202:205], v[22:25]
	v_mfma_f32_16x16x32_bf16 v[62:65], v[150:153], v[182:185], v[62:65]
	v_mfma_f32_16x16x32_bf16 v[58:61], v[158:161], v[182:185], v[58:61]
	v_mfma_f32_16x16x32_bf16 v[54:57], v[150:153], v[190:193], v[54:57]
	v_mfma_f32_16x16x32_bf16 v[50:53], v[158:161], v[190:193], v[50:53]
	v_mfma_f32_16x16x32_bf16 v[46:49], v[150:153], v[198:201], v[46:49]
	v_mfma_f32_16x16x32_bf16 v[38:41], v[158:161], v[198:201], v[38:41]
	v_mfma_f32_16x16x32_bf16 v[30:33], v[150:153], v[206:209], v[30:33]
	v_mfma_f32_16x16x32_bf16 v[22:25], v[158:161], v[206:209], v[22:25]
	v_mfma_f32_16x16x32_bf16 v[42:45], v[162:165], v[178:181], v[42:45]
	v_mfma_f32_16x16x32_bf16 v[34:37], v[170:173], v[178:181], v[34:37]
	v_mfma_f32_16x16x32_bf16 v[26:29], v[162:165], v[186:189], v[26:29]
	v_mfma_f32_16x16x32_bf16 v[18:21], v[170:173], v[186:189], v[18:21]
	v_mfma_f32_16x16x32_bf16 v[14:17], v[162:165], v[194:197], v[14:17]
	v_mfma_f32_16x16x32_bf16 v[10:13], v[170:173], v[194:197], v[10:13]
	v_mfma_f32_16x16x32_bf16 v[6:9], v[162:165], v[202:205], v[6:9]
	v_mfma_f32_16x16x32_bf16 v[2:5], v[170:173], v[202:205], v[2:5]
	v_mfma_f32_16x16x32_bf16 v[42:45], v[166:169], v[182:185], v[42:45]
	v_mfma_f32_16x16x32_bf16 v[34:37], v[174:177], v[182:185], v[34:37]
	v_mfma_f32_16x16x32_bf16 v[26:29], v[166:169], v[190:193], v[26:29]
	v_mfma_f32_16x16x32_bf16 v[18:21], v[174:177], v[190:193], v[18:21]
	v_mfma_f32_16x16x32_bf16 v[14:17], v[166:169], v[198:201], v[14:17]
	v_mfma_f32_16x16x32_bf16 v[10:13], v[174:177], v[198:201], v[10:13]
	v_mfma_f32_16x16x32_bf16 v[6:9], v[166:169], v[206:209], v[6:9]
	v_mfma_f32_16x16x32_bf16 v[2:5], v[174:177], v[206:209], v[2:5]
	s_setprio 0
	s_barrier
	s_add_u32 s23, s23, 0x100
	s_addc_u32 s25, s25, 0
	s_cmp_ge_u32 s60, s47
	s_mov_b64 s[30:31], s[34:35]
	s_mov_b32 s27, s60
	s_cbranch_scc0 .LBB0_2279
	s_and_b64 vcc, exec, s[20:21]
	s_cbranch_vccz .LBB0_2282
	s_barrier
